# expert GEMM K-loops rewritten by hand: two barriers per K-tile (24 fragment reads, then 32 MFMAs per wave) instead of eight, all four full-tile loops
# baseline (speedup 1.0000x reference)
; #define G_WAIT_V(n) asm volatile("s_waitcnt vmcnt(" #n ")" ::: "memory")
; #define G_BAR() __builtin_amdgcn_s_barrier()
; #define G_SCHED() __builtin_amdgcn_sched_barrier(0)
; #define D_STAGE_A(slot, half, kt) D_STAGE(rsA, voffA, slot, half, kt)
; #define D_STAGE_B(slot, half, kt) D_STAGE(rsB, voffB, slot, half, kt)
; #define D_LDA(dst, slot) do { _Pragma("unroll") for (int m = 0; m < 4; ++m) _Pragma("unroll") for (int k = 0; k < 2; ++k) \
;     dst[m][k] = *(const LDS_AS bf16x8*)(lds + (slot) + aoff + m * 2048 + k * 1024); } while (0)
; #define D_LDB(dst, slot) do { _Pragma("unroll") for (int n = 0; n < 2; ++n) _Pragma("unroll") for (int k = 0; k < 2; ++k) \
;     dst[n][k] = *(const LDS_AS bf16x8*)(lds + (slot) + boff + n * 2048 + k * 1024); } while (0)
; #define D_MMA(ai, bj, At, Bf) do { __builtin_amdgcn_s_setprio(1); _Pragma("unroll") for (int m = 0; m < 4; ++m) _Pragma("unroll") for (int n = 0; n < 2; ++n) _Pragma("unroll") for (int k = 0; k < 2; ++k) \
;     acc[ai][bj][m][n] = __builtin_amdgcn_mfma_f32_16x16x32_bf16(Bf[n][k], At[m][k], acc[ai][bj][m][n], 0, 0, 0); __builtin_amdgcn_s_setprio(0); } while (0)
; #define D_WAIT_L(n) asm volatile("s_waitcnt lgkmcnt(" #n ")" ::: "memory")
; #define D_STAGE_A(slot, half, kt) D_STAGE(rsA, voffA, slot, half, kt)
; #define D_WAIT_L(n) asm volatile("s_waitcnt lgkmcnt(" #n ")" ::: "memory")
;     ...
;   const int scw = cfg.scale_w(), scx = cfg.scale_x();
;     ...
; #pragma clang loop unroll(disable)
;   for (int t = 0; t < (F8_PEEL ? nt - 2 : nt); t += 2) {
;     const int t1 = t + 1;
;     const int t2 = (F8_PEEL || t + 2 < nt) ? t + 2 : t;
;     const int t3 = (F8_PEEL || t + 2 < nt) ? t + 3 : t + 1;
;     D_LDB(B0, G_SB(0, 0)); G_SCHED(); D_LDA(At, G_SA(0, 0)); D_STAGE_A(G_SA(1, 1), 1, t1);
;     D_WAIT_L(8); G_BAR(); D_WAIT_L(0); G_SCHED(); D_MMA(0, 0, At, B0); G_BAR(); G_SCHED();
;     D_LDB(B1, G_SB(0, 1)); D_STAGE_B(G_SB(0, 0), 0, t2);
;     G_BAR(); D_WAIT_L(0); G_SCHED(); D_MMA(0, 1, At, B1); G_BAR(); G_SCHED();
;     D_LDA(At, G_SA(0, 1)); D_STAGE_A(G_SA(0, 0), 0, t2);
;     G_BAR(); D_WAIT_L(0); G_SCHED(); D_MMA(1, 0, At, B0); G_BAR(); G_SCHED();
;     D_STAGE_B(G_SB(0, 1), 1, t2);
;     G_WAIT_V(6); G_BAR(); G_SCHED(); D_MMA(1, 1, At, B1); G_BAR(); G_SCHED();
.LBB0_1415:
	v_mov_b32_e32 v80, v148
	v_mov_b32_e32 v81, v149
	v_mov_b32_e32 v82, v150
	v_mov_b32_e32 v83, v151
	s_mov_b32 s81, 0x10010
	v_add_u32_e32 v130, s81, v125
	v_add_u32_e32 v131, s81, v126
	s_mov_b32 s81, 0x14010
	v_add_u32_e32 v132, s81, v125
	v_add_u32_e32 v133, s81, v126
	s_mov_b32 s81, 0x18010
	v_add_u32_e32 v134, s81, v125
	v_add_u32_e32 v135, s81, v126
	s_mov_b32 s81, 0x1c010
	v_add_u32_e32 v208, s81, v125
	v_add_u32_e32 v209, s81, v126
	s_movk_i32 s77, 0x80
	s_mov_b32 m0, s75
	s_nop 0
	buffer_load_dwordx4 v121, s[8:11], s77 offen lds
	s_mov_b32 m0, s76
	s_nop 0
	buffer_load_dwordx4 v124, s[8:11], s77 offen lds
	s_cmpk_lt_u32 s15, 0x100
	s_cbranch_scc0 .Lkl_m1npre_y
	s_mov_b32 s82, 0
.Lkl_m1npre_x:
	ds_read_b128 v[200:203], v130
	ds_read_b128 v[204:207], v131
	ds_read_b128 v[220:223], v130 offset:2048
	ds_read_b128 v[224:227], v131 offset:2048
	ds_read_b128 v[228:231], v132
	ds_read_b128 v[232:235], v133
	ds_read_b128 v[240:243], v132 offset:2048
	ds_read_b128 v[244:247], v133 offset:2048
	ds_read_b128 v[72:75], v127 offset:16
	ds_read_b128 v[76:79], v128 offset:16
	ds_read_b128 v[144:147], v127 offset:2064
	ds_read_b128 v[148:151], v128 offset:2064
	ds_read_b128 v[152:155], v127 offset:4112
	ds_read_b128 v[156:159], v128 offset:4112
	ds_read_b128 v[160:163], v127 offset:6160
	ds_read_b128 v[164:167], v128 offset:6160
	ds_read_b128 v[168:171], v127 offset:16400
	ds_read_b128 v[172:175], v128 offset:16400
	ds_read_b128 v[176:179], v127 offset:18448
	ds_read_b128 v[180:183], v128 offset:18448
	ds_read_b128 v[184:187], v127 offset:20496
	ds_read_b128 v[188:191], v128 offset:20496
	ds_read_b128 v[192:195], v127 offset:22544
	ds_read_b128 v[196:199], v128 offset:22544
	s_cmp_eq_u32 s82, 0
	s_cbranch_scc1 .Lkl_m1npre_x_nd0
	s_lshl_b32 s77, s82, 7
	s_addk_i32 s77, 0x80
	s_add_i32 s78, s77, 0x20000
	s_add_i32 s79, s77, 0x2000
	s_add_i32 s80, s77, 0x22000
	s_mov_b32 m0, s69
	s_nop 0
	buffer_load_dwordx4 v122, s[4:7], s77 offen lds
	s_mov_b32 m0, s71
	s_nop 0
	buffer_load_dwordx4 v120, s[8:11], s77 offen lds
	s_mov_b32 m0, s70
	s_nop 0
	buffer_load_dwordx4 v122, s[4:7], s78 offen lds
	s_mov_b32 m0, s72
	s_nop 0
	buffer_load_dwordx4 v123, s[8:11], s77 offen lds
	s_mov_b32 m0, s73
	s_nop 0
	buffer_load_dwordx4 v122, s[4:7], s79 offen lds
	s_mov_b32 m0, s75
	s_nop 0
	buffer_load_dwordx4 v121, s[8:11], s77 offen lds
	s_mov_b32 m0, s74
	s_nop 0
	buffer_load_dwordx4 v122, s[4:7], s80 offen lds
	s_mov_b32 m0, s76
	s_nop 0
	buffer_load_dwordx4 v124, s[8:11], s77 offen lds
.Lkl_m1npre_x_nd0:
	s_waitcnt lgkmcnt(0)
	s_barrier
	s_setprio 1
	v_mfma_scale_f32_16x16x128_f8f6f4 v[140:143], v[200:207], v[72:79], v[140:143], v81, v80 op_sel_hi:[0,0,0]
	v_mfma_scale_f32_16x16x128_f8f6f4 v[136:139], v[220:227], v[72:79], v[136:139], v81, v80 op_sel_hi:[0,0,0]
	v_mfma_scale_f32_16x16x128_f8f6f4 v[108:111], v[200:207], v[144:151], v[108:111], v81, v80 op_sel_hi:[0,0,0]
	v_mfma_scale_f32_16x16x128_f8f6f4 v[104:107], v[220:227], v[144:151], v[104:107], v81, v80 op_sel_hi:[0,0,0]
	v_mfma_scale_f32_16x16x128_f8f6f4 v[92:95], v[200:207], v[152:159], v[92:95], v81, v80 op_sel_hi:[0,0,0]
	v_mfma_scale_f32_16x16x128_f8f6f4 v[88:91], v[220:227], v[152:159], v[88:91], v81, v80 op_sel_hi:[0,0,0]
	v_mfma_scale_f32_16x16x128_f8f6f4 v[212:215], v[200:207], v[160:167], v[212:215], v81, v80 op_sel_hi:[0,0,0]
	v_mfma_scale_f32_16x16x128_f8f6f4 v[216:219], v[220:227], v[160:167], v[216:219], v81, v80 op_sel_hi:[0,0,0]
	v_mfma_scale_f32_16x16x128_f8f6f4 v[116:119], v[228:235], v[72:79], v[116:119], v81, v80 op_sel_hi:[0,0,0]
	v_mfma_scale_f32_16x16x128_f8f6f4 v[112:115], v[240:247], v[72:79], v[112:115], v81, v80 op_sel_hi:[0,0,0]
	v_mfma_scale_f32_16x16x128_f8f6f4 v[100:103], v[228:235], v[144:151], v[100:103], v81, v80 op_sel_hi:[0,0,0]
	v_mfma_scale_f32_16x16x128_f8f6f4 v[96:99], v[240:247], v[144:151], v[96:99], v81, v80 op_sel_hi:[0,0,0]
	v_mfma_scale_f32_16x16x128_f8f6f4 v[84:87], v[228:235], v[152:159], v[84:87], v81, v80 op_sel_hi:[0,0,0]
	v_mfma_scale_f32_16x16x128_f8f6f4 v[8:11], v[240:247], v[152:159], v[8:11], v81, v80 op_sel_hi:[0,0,0]
	v_mfma_scale_f32_16x16x128_f8f6f4 v[68:71], v[228:235], v[160:167], v[68:71], v81, v80 op_sel_hi:[0,0,0]
	v_mfma_scale_f32_16x16x128_f8f6f4 v[56:59], v[240:247], v[160:167], v[56:59], v81, v80 op_sel_hi:[0,0,0]
	v_mfma_scale_f32_16x16x128_f8f6f4 v[64:67], v[200:207], v[168:175], v[64:67], v81, v80 op_sel_hi:[0,0,0]
	v_mfma_scale_f32_16x16x128_f8f6f4 v[60:63], v[220:227], v[168:175], v[60:63], v81, v80 op_sel_hi:[0,0,0]
	v_mfma_scale_f32_16x16x128_f8f6f4 v[44:47], v[200:207], v[176:183], v[44:47], v81, v80 op_sel_hi:[0,0,0]
	v_mfma_scale_f32_16x16x128_f8f6f4 v[40:43], v[220:227], v[176:183], v[40:43], v81, v80 op_sel_hi:[0,0,0]
	v_mfma_scale_f32_16x16x128_f8f6f4 v[28:31], v[200:207], v[184:191], v[28:31], v81, v80 op_sel_hi:[0,0,0]
	v_mfma_scale_f32_16x16x128_f8f6f4 v[24:27], v[220:227], v[184:191], v[24:27], v81, v80 op_sel_hi:[0,0,0]
	v_mfma_scale_f32_16x16x128_f8f6f4 v[12:15], v[200:207], v[192:199], v[12:15], v81, v80 op_sel_hi:[0,0,0]
	v_mfma_scale_f32_16x16x128_f8f6f4 v[236:239], v[220:227], v[192:199], v[236:239], v81, v80 op_sel_hi:[0,0,0]
	v_mfma_scale_f32_16x16x128_f8f6f4 v[52:55], v[228:235], v[168:175], v[52:55], v81, v80 op_sel_hi:[0,0,0]
	v_mfma_scale_f32_16x16x128_f8f6f4 v[48:51], v[240:247], v[168:175], v[48:51], v81, v80 op_sel_hi:[0,0,0]
	v_mfma_scale_f32_16x16x128_f8f6f4 v[36:39], v[228:235], v[176:183], v[36:39], v81, v80 op_sel_hi:[0,0,0]
	v_mfma_scale_f32_16x16x128_f8f6f4 v[32:35], v[240:247], v[176:183], v[32:35], v81, v80 op_sel_hi:[0,0,0]
	v_mfma_scale_f32_16x16x128_f8f6f4 v[20:23], v[228:235], v[184:191], v[20:23], v81, v80 op_sel_hi:[0,0,0]
	v_mfma_scale_f32_16x16x128_f8f6f4 v[16:19], v[240:247], v[184:191], v[16:19], v81, v80 op_sel_hi:[0,0,0]
	v_mfma_scale_f32_16x16x128_f8f6f4 v[4:7], v[228:235], v[192:199], v[4:7], v81, v80 op_sel_hi:[0,0,0]
	v_mfma_scale_f32_16x16x128_f8f6f4 v[0:3], v[240:247], v[192:199], v[0:3], v81, v80 op_sel_hi:[0,0,0]
	s_setprio 0
	s_waitcnt vmcnt(0)
	s_barrier
; #define G_WAIT_V(n) asm volatile("s_waitcnt vmcnt(" #n ")" ::: "memory")
; #define G_BAR() __builtin_amdgcn_s_barrier()
; #define G_SCHED() __builtin_amdgcn_sched_barrier(0)
; #define D_STAGE_A(slot, half, kt) D_STAGE(rsA, voffA, slot, half, kt)
; #define D_STAGE_B(slot, half, kt) D_STAGE(rsB, voffB, slot, half, kt)
; #define D_LDA(dst, slot) do { _Pragma("unroll") for (int m = 0; m < 4; ++m) _Pragma("unroll") for (int k = 0; k < 2; ++k) \
;     dst[m][k] = *(const LDS_AS bf16x8*)(lds + (slot) + aoff + m * 2048 + k * 1024); } while (0)
; #define D_LDB(dst, slot) do { _Pragma("unroll") for (int n = 0; n < 2; ++n) _Pragma("unroll") for (int k = 0; k < 2; ++k) \
;     dst[n][k] = *(const LDS_AS bf16x8*)(lds + (slot) + boff + n * 2048 + k * 1024); } while (0)
; #define D_MMA(ai, bj, At, Bf) do { __builtin_amdgcn_s_setprio(1); _Pragma("unroll") for (int m = 0; m < 4; ++m) _Pragma("unroll") for (int n = 0; n < 2; ++n) _Pragma("unroll") for (int k = 0; k < 2; ++k) \
;     acc[ai][bj][m][n] = __builtin_amdgcn_mfma_f32_16x16x32_bf16(Bf[n][k], At[m][k], acc[ai][bj][m][n], 0, 0, 0); __builtin_amdgcn_s_setprio(0); } while (0)
; #define D_WAIT_L(n) asm volatile("s_waitcnt lgkmcnt(" #n ")" ::: "memory")
; #define D_STAGE_A(slot, half, kt) D_STAGE(rsA, voffA, slot, half, kt)
; #define D_STAGE_B(slot, half, kt) do { _Pragma("unroll") for (int _i = 0; _i < 2; ++_i) { const unsigned _m0 = ldsw + (unsigned)((slot) + _i * 8192); const unsigned _so = (unsigned)(kt) * 128u + (half) * bt_half + _i * bt_piece; \
;     asm volatile("s_mov_b32 m0, %0\n\ts_nop 4\n\tbuffer_load_dwordx4 %1, %2, %3 offen lds" :: "s"(_m0), "v"(voffB0), "s"(rsB), "s"(_so) : "m0", "memory"); } } while (0)
; #define D_WAIT_L(n) asm volatile("s_waitcnt lgkmcnt(" #n ")" ::: "memory")
;     ...
;   const int scw = cfg.scale_w(), scx = cfg.scale_x();
;     ...
;     D_LDB(B0, G_SB(1, 0)); G_SCHED(); D_LDA(At, G_SA(1, 0)); D_STAGE_A(G_SA(0, 1), 1, t2);
;     D_WAIT_L(8); G_BAR(); D_WAIT_L(0); G_SCHED(); D_MMA(0, 0, At, B0); G_BAR(); G_SCHED();
;     D_LDB(B1, G_SB(1, 1)); D_STAGE_B(G_SB(1, 0), 0, t3);
;     G_BAR(); D_WAIT_L(0); G_SCHED(); D_MMA(0, 1, At, B1); G_BAR(); G_SCHED();
;     D_LDA(At, G_SA(1, 1)); D_STAGE_A(G_SA(1, 0), 0, t3);
;     G_BAR(); D_WAIT_L(0); G_SCHED(); D_MMA(1, 0, At, B0); G_BAR(); G_SCHED();
;     D_STAGE_B(G_SB(1, 1), 1, t3);
;     G_WAIT_V(6); G_BAR(); G_SCHED(); D_MMA(1, 1, At, B1); G_BAR(); G_SCHED();
	ds_read_b128 v[200:203], v134
	ds_read_b128 v[204:207], v135
	ds_read_b128 v[220:223], v134 offset:2048
	ds_read_b128 v[224:227], v135 offset:2048
	ds_read_b128 v[228:231], v208
	ds_read_b128 v[232:235], v209
	ds_read_b128 v[240:243], v208 offset:2048
	ds_read_b128 v[244:247], v209 offset:2048
	ds_read_b128 v[72:75], v127 offset:32784
	ds_read_b128 v[76:79], v128 offset:32784
	ds_read_b128 v[144:147], v127 offset:34832
	ds_read_b128 v[148:151], v128 offset:34832
	ds_read_b128 v[152:155], v127 offset:36880
	ds_read_b128 v[156:159], v128 offset:36880
	ds_read_b128 v[160:163], v127 offset:38928
	ds_read_b128 v[164:167], v128 offset:38928
	ds_read_b128 v[168:171], v127 offset:49168
	ds_read_b128 v[172:175], v128 offset:49168
	ds_read_b128 v[176:179], v127 offset:51216
	ds_read_b128 v[180:183], v128 offset:51216
	ds_read_b128 v[184:187], v127 offset:53264
	ds_read_b128 v[188:191], v128 offset:53264
	ds_read_b128 v[192:195], v127 offset:55312
	ds_read_b128 v[196:199], v128 offset:55312
	s_cmp_ge_u32 s82, 14
	s_cbranch_scc1 .Lkl_m1npre_x_nd1
	s_lshl_b32 s77, s82, 7
	s_addk_i32 s77, 0x100
	s_add_i32 s78, s77, 0x20000
	s_add_i32 s79, s77, 0x2000
	s_add_i32 s80, s77, 0x22000
	s_mov_b32 m0, s23
	s_nop 0
	buffer_load_dwordx4 v122, s[4:7], s77 offen lds
	s_mov_b32 m0, s61
	s_nop 0
	buffer_load_dwordx4 v120, s[8:11], s77 offen lds
	s_mov_b32 m0, s39
	s_nop 0
	buffer_load_dwordx4 v122, s[4:7], s78 offen lds
	s_mov_b32 m0, s62
	s_nop 0
	buffer_load_dwordx4 v123, s[8:11], s77 offen lds
	s_mov_b32 m0, s63
	s_nop 0
	buffer_load_dwordx4 v122, s[4:7], s79 offen lds
	s_mov_b32 m0, s67
	s_nop 0
	buffer_load_dwordx4 v121, s[8:11], s77 offen lds
	s_mov_b32 m0, s66
	s_nop 0
	buffer_load_dwordx4 v122, s[4:7], s80 offen lds
	s_mov_b32 m0, s68
	s_nop 0
	buffer_load_dwordx4 v124, s[8:11], s77 offen lds
.Lkl_m1npre_x_nd1:
	s_waitcnt lgkmcnt(0)
	s_barrier
	s_setprio 1
	v_mfma_scale_f32_16x16x128_f8f6f4 v[140:143], v[200:207], v[72:79], v[140:143], v81, v80 op_sel_hi:[0,0,0]
	v_mfma_scale_f32_16x16x128_f8f6f4 v[136:139], v[220:227], v[72:79], v[136:139], v81, v80 op_sel_hi:[0,0,0]
	v_mfma_scale_f32_16x16x128_f8f6f4 v[108:111], v[200:207], v[144:151], v[108:111], v81, v80 op_sel_hi:[0,0,0]
	v_mfma_scale_f32_16x16x128_f8f6f4 v[104:107], v[220:227], v[144:151], v[104:107], v81, v80 op_sel_hi:[0,0,0]
	v_mfma_scale_f32_16x16x128_f8f6f4 v[92:95], v[200:207], v[152:159], v[92:95], v81, v80 op_sel_hi:[0,0,0]
	v_mfma_scale_f32_16x16x128_f8f6f4 v[88:91], v[220:227], v[152:159], v[88:91], v81, v80 op_sel_hi:[0,0,0]
	v_mfma_scale_f32_16x16x128_f8f6f4 v[212:215], v[200:207], v[160:167], v[212:215], v81, v80 op_sel_hi:[0,0,0]
	v_mfma_scale_f32_16x16x128_f8f6f4 v[216:219], v[220:227], v[160:167], v[216:219], v81, v80 op_sel_hi:[0,0,0]
	v_mfma_scale_f32_16x16x128_f8f6f4 v[116:119], v[228:235], v[72:79], v[116:119], v81, v80 op_sel_hi:[0,0,0]
	v_mfma_scale_f32_16x16x128_f8f6f4 v[112:115], v[240:247], v[72:79], v[112:115], v81, v80 op_sel_hi:[0,0,0]
	v_mfma_scale_f32_16x16x128_f8f6f4 v[100:103], v[228:235], v[144:151], v[100:103], v81, v80 op_sel_hi:[0,0,0]
	v_mfma_scale_f32_16x16x128_f8f6f4 v[96:99], v[240:247], v[144:151], v[96:99], v81, v80 op_sel_hi:[0,0,0]
	v_mfma_scale_f32_16x16x128_f8f6f4 v[84:87], v[228:235], v[152:159], v[84:87], v81, v80 op_sel_hi:[0,0,0]
	v_mfma_scale_f32_16x16x128_f8f6f4 v[8:11], v[240:247], v[152:159], v[8:11], v81, v80 op_sel_hi:[0,0,0]
	v_mfma_scale_f32_16x16x128_f8f6f4 v[68:71], v[228:235], v[160:167], v[68:71], v81, v80 op_sel_hi:[0,0,0]
	v_mfma_scale_f32_16x16x128_f8f6f4 v[56:59], v[240:247], v[160:167], v[56:59], v81, v80 op_sel_hi:[0,0,0]
	v_mfma_scale_f32_16x16x128_f8f6f4 v[64:67], v[200:207], v[168:175], v[64:67], v81, v80 op_sel_hi:[0,0,0]
	v_mfma_scale_f32_16x16x128_f8f6f4 v[60:63], v[220:227], v[168:175], v[60:63], v81, v80 op_sel_hi:[0,0,0]
	v_mfma_scale_f32_16x16x128_f8f6f4 v[44:47], v[200:207], v[176:183], v[44:47], v81, v80 op_sel_hi:[0,0,0]
	v_mfma_scale_f32_16x16x128_f8f6f4 v[40:43], v[220:227], v[176:183], v[40:43], v81, v80 op_sel_hi:[0,0,0]
	v_mfma_scale_f32_16x16x128_f8f6f4 v[28:31], v[200:207], v[184:191], v[28:31], v81, v80 op_sel_hi:[0,0,0]
	v_mfma_scale_f32_16x16x128_f8f6f4 v[24:27], v[220:227], v[184:191], v[24:27], v81, v80 op_sel_hi:[0,0,0]
	v_mfma_scale_f32_16x16x128_f8f6f4 v[12:15], v[200:207], v[192:199], v[12:15], v81, v80 op_sel_hi:[0,0,0]
	v_mfma_scale_f32_16x16x128_f8f6f4 v[236:239], v[220:227], v[192:199], v[236:239], v81, v80 op_sel_hi:[0,0,0]
	v_mfma_scale_f32_16x16x128_f8f6f4 v[52:55], v[228:235], v[168:175], v[52:55], v81, v80 op_sel_hi:[0,0,0]
	v_mfma_scale_f32_16x16x128_f8f6f4 v[48:51], v[240:247], v[168:175], v[48:51], v81, v80 op_sel_hi:[0,0,0]
	v_mfma_scale_f32_16x16x128_f8f6f4 v[36:39], v[228:235], v[176:183], v[36:39], v81, v80 op_sel_hi:[0,0,0]
	v_mfma_scale_f32_16x16x128_f8f6f4 v[32:35], v[240:247], v[176:183], v[32:35], v81, v80 op_sel_hi:[0,0,0]
	v_mfma_scale_f32_16x16x128_f8f6f4 v[20:23], v[228:235], v[184:191], v[20:23], v81, v80 op_sel_hi:[0,0,0]
	v_mfma_scale_f32_16x16x128_f8f6f4 v[16:19], v[240:247], v[184:191], v[16:19], v81, v80 op_sel_hi:[0,0,0]
	v_mfma_scale_f32_16x16x128_f8f6f4 v[4:7], v[228:235], v[192:199], v[4:7], v81, v80 op_sel_hi:[0,0,0]
	v_mfma_scale_f32_16x16x128_f8f6f4 v[0:3], v[240:247], v[192:199], v[0:3], v81, v80 op_sel_hi:[0,0,0]
	s_setprio 0
	s_waitcnt vmcnt(0)
	s_barrier
	s_add_i32 s82, s82, 2
	s_cmp_lt_u32 s82, 16
	s_cbranch_scc1 .Lkl_m1npre_x
	s_branch .Lkl_m1npre_end
.Lkl_m1npre_y:
	s_mov_b32 s82, 0
; #define G_WAIT_V(n) asm volatile("s_waitcnt vmcnt(" #n ")" ::: "memory")
; #define G_BAR() __builtin_amdgcn_s_barrier()
; #define G_SCHED() __builtin_amdgcn_sched_barrier(0)
; #define D_STAGE_A(slot, half, kt) D_STAGE(rsA, voffA, slot, half, kt)
; #define D_STAGE_B(slot, half, kt) D_STAGE(rsB, voffB, slot, half, kt)
; #define D_LDA(dst, slot) do { _Pragma("unroll") for (int m = 0; m < 4; ++m) _Pragma("unroll") for (int k = 0; k < 2; ++k) \
;     dst[m][k] = *(const LDS_AS bf16x8*)(lds + (slot) + aoff + m * 2048 + k * 1024); } while (0)
; #define D_LDB(dst, slot) do { _Pragma("unroll") for (int n = 0; n < 2; ++n) _Pragma("unroll") for (int k = 0; k < 2; ++k) \
;     dst[n][k] = *(const LDS_AS bf16x8*)(lds + (slot) + boff + n * 2048 + k * 1024); } while (0)
; #define D_MMA(ai, bj, At, Bf) do { __builtin_amdgcn_s_setprio(1); _Pragma("unroll") for (int m = 0; m < 4; ++m) _Pragma("unroll") for (int n = 0; n < 2; ++n) _Pragma("unroll") for (int k = 0; k < 2; ++k) \
;     acc[ai][bj][m][n] = __builtin_amdgcn_mfma_f32_16x16x32_bf16(Bf[n][k], At[m][k], acc[ai][bj][m][n], 0, 0, 0); __builtin_amdgcn_s_setprio(0); } while (0)
; #define D_WAIT_L(n) asm volatile("s_waitcnt lgkmcnt(" #n ")" ::: "memory")
; #define D_STAGE_A(slot, half, kt) D_STAGE(rsA, voffA, slot, half, kt)
; #define D_STAGE_B(slot, half, kt) do { _Pragma("unroll") for (int _i = 0; _i < 2; ++_i) { const unsigned _m0 = ldsw + (unsigned)((slot) + _i * 8192); const unsigned _so = (unsigned)(kt) * 128u + (half) * bt_half + _i * bt_piece; \
;     asm volatile("s_mov_b32 m0, %0\n\ts_nop 4\n\tbuffer_load_dwordx4 %1, %2, %3 offen lds" :: "s"(_m0), "v"(voffB0), "s"(rsB), "s"(_so) : "m0", "memory"); } } while (0)
; #define D_WAIT_L(n) asm volatile("s_waitcnt lgkmcnt(" #n ")" ::: "memory")
;     ...
;     D_LDB(B0, G_SB(0, 0)); G_SCHED(); D_LDA(At, G_SA(0, 0)); D_STAGE_A(G_SA(1, 1), 1, t1);
;     D_WAIT_L(8); G_BAR(); D_WAIT_L(0); G_SCHED(); D_MMA(0, 0, At, B0); G_BAR(); G_SCHED();
;     D_LDB(B1, G_SB(0, 1)); D_STAGE_B(G_SB(0, 0), 0, t2);
;     G_BAR(); D_WAIT_L(0); G_SCHED(); D_MMA(0, 1, At, B1); G_BAR(); G_SCHED();
;     D_LDA(At, G_SA(0, 1)); D_STAGE_A(G_SA(0, 0), 0, t2);
;     G_BAR(); D_WAIT_L(0); G_SCHED(); D_MMA(1, 0, At, B0); G_BAR(); G_SCHED();
;     D_STAGE_B(G_SB(0, 1), 1, t2);
;     G_WAIT_V(6); G_BAR(); G_SCHED(); D_MMA(1, 1, At, B1); G_BAR(); G_SCHED();
.Lkl_m1npre_yl:
	ds_read_b128 v[200:203], v130
	ds_read_b128 v[204:207], v131
	ds_read_b128 v[220:223], v130 offset:2048
	ds_read_b128 v[224:227], v131 offset:2048
	ds_read_b128 v[228:231], v132
	ds_read_b128 v[232:235], v133
	ds_read_b128 v[240:243], v132 offset:2048
	ds_read_b128 v[244:247], v133 offset:2048
	ds_read_b128 v[72:75], v127 offset:16
	ds_read_b128 v[76:79], v128 offset:16
	ds_read_b128 v[144:147], v127 offset:2064
	ds_read_b128 v[148:151], v128 offset:2064
	ds_read_b128 v[152:155], v127 offset:4112
	ds_read_b128 v[156:159], v128 offset:4112
	ds_read_b128 v[160:163], v127 offset:6160
	ds_read_b128 v[164:167], v128 offset:6160
	ds_read_b128 v[168:171], v127 offset:16400
	ds_read_b128 v[172:175], v128 offset:16400
	ds_read_b128 v[176:179], v127 offset:18448
	ds_read_b128 v[180:183], v128 offset:18448
	ds_read_b128 v[184:187], v127 offset:20496
	ds_read_b128 v[188:191], v128 offset:20496
	ds_read_b128 v[192:195], v127 offset:22544
	ds_read_b128 v[196:199], v128 offset:22544
	s_waitcnt lgkmcnt(0)
	s_waitcnt vmcnt(0)
	s_barrier
	s_setprio 1
	s_cmp_ge_u32 s82, 14
	s_cbranch_scc1 .Lkl_m1npre_y_nd0
	s_lshl_b32 s77, s82, 7
	s_addk_i32 s77, 0x100
	s_add_i32 s78, s77, 0x20000
	s_add_i32 s79, s77, 0x2000
	s_add_i32 s80, s77, 0x22000
	v_mfma_scale_f32_16x16x128_f8f6f4 v[140:143], v[200:207], v[72:79], v[140:143], v81, v80 op_sel_hi:[0,0,0]
	v_mfma_scale_f32_16x16x128_f8f6f4 v[136:139], v[220:227], v[72:79], v[136:139], v81, v80 op_sel_hi:[0,0,0]
	v_mfma_scale_f32_16x16x128_f8f6f4 v[108:111], v[200:207], v[144:151], v[108:111], v81, v80 op_sel_hi:[0,0,0]
	s_mov_b32 m0, s23
	s_nop 0
	buffer_load_dwordx4 v122, s[4:7], s77 offen lds
	v_mfma_scale_f32_16x16x128_f8f6f4 v[104:107], v[220:227], v[144:151], v[104:107], v81, v80 op_sel_hi:[0,0,0]
	v_mfma_scale_f32_16x16x128_f8f6f4 v[92:95], v[200:207], v[152:159], v[92:95], v81, v80 op_sel_hi:[0,0,0]
	v_mfma_scale_f32_16x16x128_f8f6f4 v[88:91], v[220:227], v[152:159], v[88:91], v81, v80 op_sel_hi:[0,0,0]
	s_mov_b32 m0, s61
	s_nop 0
	buffer_load_dwordx4 v120, s[8:11], s77 offen lds
	v_mfma_scale_f32_16x16x128_f8f6f4 v[212:215], v[200:207], v[160:167], v[212:215], v81, v80 op_sel_hi:[0,0,0]
	v_mfma_scale_f32_16x16x128_f8f6f4 v[216:219], v[220:227], v[160:167], v[216:219], v81, v80 op_sel_hi:[0,0,0]
	v_mfma_scale_f32_16x16x128_f8f6f4 v[116:119], v[228:235], v[72:79], v[116:119], v81, v80 op_sel_hi:[0,0,0]
	s_mov_b32 m0, s39
	s_nop 0
	buffer_load_dwordx4 v122, s[4:7], s78 offen lds
	v_mfma_scale_f32_16x16x128_f8f6f4 v[112:115], v[240:247], v[72:79], v[112:115], v81, v80 op_sel_hi:[0,0,0]
	v_mfma_scale_f32_16x16x128_f8f6f4 v[100:103], v[228:235], v[144:151], v[100:103], v81, v80 op_sel_hi:[0,0,0]
	v_mfma_scale_f32_16x16x128_f8f6f4 v[96:99], v[240:247], v[144:151], v[96:99], v81, v80 op_sel_hi:[0,0,0]
	s_mov_b32 m0, s62
	s_nop 0
	buffer_load_dwordx4 v123, s[8:11], s77 offen lds
	v_mfma_scale_f32_16x16x128_f8f6f4 v[84:87], v[228:235], v[152:159], v[84:87], v81, v80 op_sel_hi:[0,0,0]
	v_mfma_scale_f32_16x16x128_f8f6f4 v[8:11], v[240:247], v[152:159], v[8:11], v81, v80 op_sel_hi:[0,0,0]
	v_mfma_scale_f32_16x16x128_f8f6f4 v[68:71], v[228:235], v[160:167], v[68:71], v81, v80 op_sel_hi:[0,0,0]
	s_mov_b32 m0, s63
	s_nop 0
	buffer_load_dwordx4 v122, s[4:7], s79 offen lds
	v_mfma_scale_f32_16x16x128_f8f6f4 v[56:59], v[240:247], v[160:167], v[56:59], v81, v80 op_sel_hi:[0,0,0]
	v_mfma_scale_f32_16x16x128_f8f6f4 v[64:67], v[200:207], v[168:175], v[64:67], v81, v80 op_sel_hi:[0,0,0]
	v_mfma_scale_f32_16x16x128_f8f6f4 v[60:63], v[220:227], v[168:175], v[60:63], v81, v80 op_sel_hi:[0,0,0]
	s_mov_b32 m0, s67
	s_nop 0
	buffer_load_dwordx4 v121, s[8:11], s77 offen lds
	v_mfma_scale_f32_16x16x128_f8f6f4 v[44:47], v[200:207], v[176:183], v[44:47], v81, v80 op_sel_hi:[0,0,0]
	v_mfma_scale_f32_16x16x128_f8f6f4 v[40:43], v[220:227], v[176:183], v[40:43], v81, v80 op_sel_hi:[0,0,0]
	v_mfma_scale_f32_16x16x128_f8f6f4 v[28:31], v[200:207], v[184:191], v[28:31], v81, v80 op_sel_hi:[0,0,0]
	s_mov_b32 m0, s66
	s_nop 0
	buffer_load_dwordx4 v122, s[4:7], s80 offen lds
	v_mfma_scale_f32_16x16x128_f8f6f4 v[24:27], v[220:227], v[184:191], v[24:27], v81, v80 op_sel_hi:[0,0,0]
	v_mfma_scale_f32_16x16x128_f8f6f4 v[12:15], v[200:207], v[192:199], v[12:15], v81, v80 op_sel_hi:[0,0,0]
	v_mfma_scale_f32_16x16x128_f8f6f4 v[236:239], v[220:227], v[192:199], v[236:239], v81, v80 op_sel_hi:[0,0,0]
	s_mov_b32 m0, s68
	s_nop 0
	buffer_load_dwordx4 v124, s[8:11], s77 offen lds
	v_mfma_scale_f32_16x16x128_f8f6f4 v[52:55], v[228:235], v[168:175], v[52:55], v81, v80 op_sel_hi:[0,0,0]
	v_mfma_scale_f32_16x16x128_f8f6f4 v[48:51], v[240:247], v[168:175], v[48:51], v81, v80 op_sel_hi:[0,0,0]
	v_mfma_scale_f32_16x16x128_f8f6f4 v[36:39], v[228:235], v[176:183], v[36:39], v81, v80 op_sel_hi:[0,0,0]
	v_mfma_scale_f32_16x16x128_f8f6f4 v[32:35], v[240:247], v[176:183], v[32:35], v81, v80 op_sel_hi:[0,0,0]
	v_mfma_scale_f32_16x16x128_f8f6f4 v[20:23], v[228:235], v[184:191], v[20:23], v81, v80 op_sel_hi:[0,0,0]
	v_mfma_scale_f32_16x16x128_f8f6f4 v[16:19], v[240:247], v[184:191], v[16:19], v81, v80 op_sel_hi:[0,0,0]
	v_mfma_scale_f32_16x16x128_f8f6f4 v[4:7], v[228:235], v[192:199], v[4:7], v81, v80 op_sel_hi:[0,0,0]
	v_mfma_scale_f32_16x16x128_f8f6f4 v[0:3], v[240:247], v[192:199], v[0:3], v81, v80 op_sel_hi:[0,0,0]
	s_branch .Lkl_m1npre_y_nd0_j
.Lkl_m1npre_y_nd0:
	v_mfma_scale_f32_16x16x128_f8f6f4 v[140:143], v[200:207], v[72:79], v[140:143], v81, v80 op_sel_hi:[0,0,0]
	v_mfma_scale_f32_16x16x128_f8f6f4 v[136:139], v[220:227], v[72:79], v[136:139], v81, v80 op_sel_hi:[0,0,0]
	v_mfma_scale_f32_16x16x128_f8f6f4 v[108:111], v[200:207], v[144:151], v[108:111], v81, v80 op_sel_hi:[0,0,0]
	v_mfma_scale_f32_16x16x128_f8f6f4 v[104:107], v[220:227], v[144:151], v[104:107], v81, v80 op_sel_hi:[0,0,0]
	v_mfma_scale_f32_16x16x128_f8f6f4 v[92:95], v[200:207], v[152:159], v[92:95], v81, v80 op_sel_hi:[0,0,0]
	v_mfma_scale_f32_16x16x128_f8f6f4 v[88:91], v[220:227], v[152:159], v[88:91], v81, v80 op_sel_hi:[0,0,0]
	v_mfma_scale_f32_16x16x128_f8f6f4 v[212:215], v[200:207], v[160:167], v[212:215], v81, v80 op_sel_hi:[0,0,0]
	v_mfma_scale_f32_16x16x128_f8f6f4 v[216:219], v[220:227], v[160:167], v[216:219], v81, v80 op_sel_hi:[0,0,0]
	v_mfma_scale_f32_16x16x128_f8f6f4 v[116:119], v[228:235], v[72:79], v[116:119], v81, v80 op_sel_hi:[0,0,0]
	v_mfma_scale_f32_16x16x128_f8f6f4 v[112:115], v[240:247], v[72:79], v[112:115], v81, v80 op_sel_hi:[0,0,0]
	v_mfma_scale_f32_16x16x128_f8f6f4 v[100:103], v[228:235], v[144:151], v[100:103], v81, v80 op_sel_hi:[0,0,0]
	v_mfma_scale_f32_16x16x128_f8f6f4 v[96:99], v[240:247], v[144:151], v[96:99], v81, v80 op_sel_hi:[0,0,0]
	v_mfma_scale_f32_16x16x128_f8f6f4 v[84:87], v[228:235], v[152:159], v[84:87], v81, v80 op_sel_hi:[0,0,0]
	v_mfma_scale_f32_16x16x128_f8f6f4 v[8:11], v[240:247], v[152:159], v[8:11], v81, v80 op_sel_hi:[0,0,0]
	v_mfma_scale_f32_16x16x128_f8f6f4 v[68:71], v[228:235], v[160:167], v[68:71], v81, v80 op_sel_hi:[0,0,0]
	v_mfma_scale_f32_16x16x128_f8f6f4 v[56:59], v[240:247], v[160:167], v[56:59], v81, v80 op_sel_hi:[0,0,0]
	v_mfma_scale_f32_16x16x128_f8f6f4 v[64:67], v[200:207], v[168:175], v[64:67], v81, v80 op_sel_hi:[0,0,0]
	v_mfma_scale_f32_16x16x128_f8f6f4 v[60:63], v[220:227], v[168:175], v[60:63], v81, v80 op_sel_hi:[0,0,0]
	v_mfma_scale_f32_16x16x128_f8f6f4 v[44:47], v[200:207], v[176:183], v[44:47], v81, v80 op_sel_hi:[0,0,0]
	v_mfma_scale_f32_16x16x128_f8f6f4 v[40:43], v[220:227], v[176:183], v[40:43], v81, v80 op_sel_hi:[0,0,0]
	v_mfma_scale_f32_16x16x128_f8f6f4 v[28:31], v[200:207], v[184:191], v[28:31], v81, v80 op_sel_hi:[0,0,0]
	v_mfma_scale_f32_16x16x128_f8f6f4 v[24:27], v[220:227], v[184:191], v[24:27], v81, v80 op_sel_hi:[0,0,0]
	v_mfma_scale_f32_16x16x128_f8f6f4 v[12:15], v[200:207], v[192:199], v[12:15], v81, v80 op_sel_hi:[0,0,0]
	v_mfma_scale_f32_16x16x128_f8f6f4 v[236:239], v[220:227], v[192:199], v[236:239], v81, v80 op_sel_hi:[0,0,0]
	v_mfma_scale_f32_16x16x128_f8f6f4 v[52:55], v[228:235], v[168:175], v[52:55], v81, v80 op_sel_hi:[0,0,0]
	v_mfma_scale_f32_16x16x128_f8f6f4 v[48:51], v[240:247], v[168:175], v[48:51], v81, v80 op_sel_hi:[0,0,0]
	v_mfma_scale_f32_16x16x128_f8f6f4 v[36:39], v[228:235], v[176:183], v[36:39], v81, v80 op_sel_hi:[0,0,0]
	v_mfma_scale_f32_16x16x128_f8f6f4 v[32:35], v[240:247], v[176:183], v[32:35], v81, v80 op_sel_hi:[0,0,0]
	v_mfma_scale_f32_16x16x128_f8f6f4 v[20:23], v[228:235], v[184:191], v[20:23], v81, v80 op_sel_hi:[0,0,0]
	v_mfma_scale_f32_16x16x128_f8f6f4 v[16:19], v[240:247], v[184:191], v[16:19], v81, v80 op_sel_hi:[0,0,0]
	v_mfma_scale_f32_16x16x128_f8f6f4 v[4:7], v[228:235], v[192:199], v[4:7], v81, v80 op_sel_hi:[0,0,0]
	v_mfma_scale_f32_16x16x128_f8f6f4 v[0:3], v[240:247], v[192:199], v[0:3], v81, v80 op_sel_hi:[0,0,0]
; #define G_WAIT_V(n) asm volatile("s_waitcnt vmcnt(" #n ")" ::: "memory")
; #define G_BAR() __builtin_amdgcn_s_barrier()
; #define G_SCHED() __builtin_amdgcn_sched_barrier(0)
; #define D_STAGE_A(slot, half, kt) D_STAGE(rsA, voffA, slot, half, kt)
; #define D_STAGE_B(slot, half, kt) D_STAGE(rsB, voffB, slot, half, kt)
; #define D_LDA(dst, slot) do { _Pragma("unroll") for (int m = 0; m < 4; ++m) _Pragma("unroll") for (int k = 0; k < 2; ++k) \
;     dst[m][k] = *(const LDS_AS bf16x8*)(lds + (slot) + aoff + m * 2048 + k * 1024); } while (0)
; #define D_LDB(dst, slot) do { _Pragma("unroll") for (int n = 0; n < 2; ++n) _Pragma("unroll") for (int k = 0; k < 2; ++k) \
;     dst[n][k] = *(const LDS_AS bf16x8*)(lds + (slot) + boff + n * 2048 + k * 1024); } while (0)
; #define D_MMA(ai, bj, At, Bf) do { __builtin_amdgcn_s_setprio(1); _Pragma("unroll") for (int m = 0; m < 4; ++m) _Pragma("unroll") for (int n = 0; n < 2; ++n) _Pragma("unroll") for (int k = 0; k < 2; ++k) \
;     acc[ai][bj][m][n] = __builtin_amdgcn_mfma_f32_16x16x32_bf16(Bf[n][k], At[m][k], acc[ai][bj][m][n], 0, 0, 0); __builtin_amdgcn_s_setprio(0); } while (0)
; #define D_WAIT_L(n) asm volatile("s_waitcnt lgkmcnt(" #n ")" ::: "memory")
; #define D_STAGE_A(slot, half, kt) D_STAGE(rsA, voffA, slot, half, kt)
; #define D_STAGE_B(slot, half, kt) do { _Pragma("unroll") for (int _i = 0; _i < 2; ++_i) { const unsigned _m0 = ldsw + (unsigned)((slot) + _i * 8192); const unsigned _so = (unsigned)(kt) * 128u + (half) * bt_half + _i * bt_piece; \
;     asm volatile("s_mov_b32 m0, %0\n\ts_nop 4\n\tbuffer_load_dwordx4 %1, %2, %3 offen lds" :: "s"(_m0), "v"(voffB0), "s"(rsB), "s"(_so) : "m0", "memory"); } } while (0)
; #define D_WAIT_L(n) asm volatile("s_waitcnt lgkmcnt(" #n ")" ::: "memory")
;     ...
;     D_LDB(B0, G_SB(1, 0)); G_SCHED(); D_LDA(At, G_SA(1, 0)); D_STAGE_A(G_SA(0, 1), 1, t2);
;     D_WAIT_L(8); G_BAR(); D_WAIT_L(0); G_SCHED(); D_MMA(0, 0, At, B0); G_BAR(); G_SCHED();
;     D_LDB(B1, G_SB(1, 1)); D_STAGE_B(G_SB(1, 0), 0, t3);
;     G_BAR(); D_WAIT_L(0); G_SCHED(); D_MMA(0, 1, At, B1); G_BAR(); G_SCHED();
;     D_LDA(At, G_SA(1, 1)); D_STAGE_A(G_SA(1, 0), 0, t3);
;     G_BAR(); D_WAIT_L(0); G_SCHED(); D_MMA(1, 0, At, B0); G_BAR(); G_SCHED();
;     D_STAGE_B(G_SB(1, 1), 1, t3);
;     G_WAIT_V(6); G_BAR(); G_SCHED(); D_MMA(1, 1, At, B1); G_BAR(); G_SCHED();
.Lkl_m1npre_y_nd0_j:
	s_setprio 0
	s_barrier
	ds_read_b128 v[200:203], v134
	ds_read_b128 v[204:207], v135
	ds_read_b128 v[220:223], v134 offset:2048
	ds_read_b128 v[224:227], v135 offset:2048
	ds_read_b128 v[228:231], v208
	ds_read_b128 v[232:235], v209
	ds_read_b128 v[240:243], v208 offset:2048
	ds_read_b128 v[244:247], v209 offset:2048
	ds_read_b128 v[72:75], v127 offset:32784
	ds_read_b128 v[76:79], v128 offset:32784
	ds_read_b128 v[144:147], v127 offset:34832
	ds_read_b128 v[148:151], v128 offset:34832
	ds_read_b128 v[152:155], v127 offset:36880
	ds_read_b128 v[156:159], v128 offset:36880
	ds_read_b128 v[160:163], v127 offset:38928
	ds_read_b128 v[164:167], v128 offset:38928
	ds_read_b128 v[168:171], v127 offset:49168
	ds_read_b128 v[172:175], v128 offset:49168
	ds_read_b128 v[176:179], v127 offset:51216
	ds_read_b128 v[180:183], v128 offset:51216
	ds_read_b128 v[184:187], v127 offset:53264
	ds_read_b128 v[188:191], v128 offset:53264
	ds_read_b128 v[192:195], v127 offset:55312
	ds_read_b128 v[196:199], v128 offset:55312
	s_waitcnt lgkmcnt(0)
	s_waitcnt vmcnt(0)
	s_barrier
	s_setprio 1
	s_cmp_ge_u32 s82, 14
	s_cbranch_scc1 .Lkl_m1npre_y_nd1
	s_lshl_b32 s77, s82, 7
	s_addk_i32 s77, 0x180
	s_add_i32 s78, s77, 0x20000
	s_add_i32 s79, s77, 0x2000
	s_add_i32 s80, s77, 0x22000
	v_mfma_scale_f32_16x16x128_f8f6f4 v[140:143], v[200:207], v[72:79], v[140:143], v81, v80 op_sel_hi:[0,0,0]
	v_mfma_scale_f32_16x16x128_f8f6f4 v[136:139], v[220:227], v[72:79], v[136:139], v81, v80 op_sel_hi:[0,0,0]
	v_mfma_scale_f32_16x16x128_f8f6f4 v[108:111], v[200:207], v[144:151], v[108:111], v81, v80 op_sel_hi:[0,0,0]
	s_mov_b32 m0, s69
	s_nop 0
	buffer_load_dwordx4 v122, s[4:7], s77 offen lds
	v_mfma_scale_f32_16x16x128_f8f6f4 v[104:107], v[220:227], v[144:151], v[104:107], v81, v80 op_sel_hi:[0,0,0]
	v_mfma_scale_f32_16x16x128_f8f6f4 v[92:95], v[200:207], v[152:159], v[92:95], v81, v80 op_sel_hi:[0,0,0]
	v_mfma_scale_f32_16x16x128_f8f6f4 v[88:91], v[220:227], v[152:159], v[88:91], v81, v80 op_sel_hi:[0,0,0]
	s_mov_b32 m0, s71
	s_nop 0
	buffer_load_dwordx4 v120, s[8:11], s77 offen lds
	v_mfma_scale_f32_16x16x128_f8f6f4 v[212:215], v[200:207], v[160:167], v[212:215], v81, v80 op_sel_hi:[0,0,0]
	v_mfma_scale_f32_16x16x128_f8f6f4 v[216:219], v[220:227], v[160:167], v[216:219], v81, v80 op_sel_hi:[0,0,0]
	v_mfma_scale_f32_16x16x128_f8f6f4 v[116:119], v[228:235], v[72:79], v[116:119], v81, v80 op_sel_hi:[0,0,0]
	s_mov_b32 m0, s70
	s_nop 0
	buffer_load_dwordx4 v122, s[4:7], s78 offen lds
	v_mfma_scale_f32_16x16x128_f8f6f4 v[112:115], v[240:247], v[72:79], v[112:115], v81, v80 op_sel_hi:[0,0,0]
	v_mfma_scale_f32_16x16x128_f8f6f4 v[100:103], v[228:235], v[144:151], v[100:103], v81, v80 op_sel_hi:[0,0,0]
	v_mfma_scale_f32_16x16x128_f8f6f4 v[96:99], v[240:247], v[144:151], v[96:99], v81, v80 op_sel_hi:[0,0,0]
	s_mov_b32 m0, s72
	s_nop 0
	buffer_load_dwordx4 v123, s[8:11], s77 offen lds
	v_mfma_scale_f32_16x16x128_f8f6f4 v[84:87], v[228:235], v[152:159], v[84:87], v81, v80 op_sel_hi:[0,0,0]
	v_mfma_scale_f32_16x16x128_f8f6f4 v[8:11], v[240:247], v[152:159], v[8:11], v81, v80 op_sel_hi:[0,0,0]
	v_mfma_scale_f32_16x16x128_f8f6f4 v[68:71], v[228:235], v[160:167], v[68:71], v81, v80 op_sel_hi:[0,0,0]
	s_mov_b32 m0, s73
	s_nop 0
	buffer_load_dwordx4 v122, s[4:7], s79 offen lds
	v_mfma_scale_f32_16x16x128_f8f6f4 v[56:59], v[240:247], v[160:167], v[56:59], v81, v80 op_sel_hi:[0,0,0]
	v_mfma_scale_f32_16x16x128_f8f6f4 v[64:67], v[200:207], v[168:175], v[64:67], v81, v80 op_sel_hi:[0,0,0]
	v_mfma_scale_f32_16x16x128_f8f6f4 v[60:63], v[220:227], v[168:175], v[60:63], v81, v80 op_sel_hi:[0,0,0]
	s_mov_b32 m0, s75
	s_nop 0
	buffer_load_dwordx4 v121, s[8:11], s77 offen lds
	v_mfma_scale_f32_16x16x128_f8f6f4 v[44:47], v[200:207], v[176:183], v[44:47], v81, v80 op_sel_hi:[0,0,0]
	v_mfma_scale_f32_16x16x128_f8f6f4 v[40:43], v[220:227], v[176:183], v[40:43], v81, v80 op_sel_hi:[0,0,0]
	v_mfma_scale_f32_16x16x128_f8f6f4 v[28:31], v[200:207], v[184:191], v[28:31], v81, v80 op_sel_hi:[0,0,0]
	s_mov_b32 m0, s74
	s_nop 0
	buffer_load_dwordx4 v122, s[4:7], s80 offen lds
	v_mfma_scale_f32_16x16x128_f8f6f4 v[24:27], v[220:227], v[184:191], v[24:27], v81, v80 op_sel_hi:[0,0,0]
	v_mfma_scale_f32_16x16x128_f8f6f4 v[12:15], v[200:207], v[192:199], v[12:15], v81, v80 op_sel_hi:[0,0,0]
	v_mfma_scale_f32_16x16x128_f8f6f4 v[236:239], v[220:227], v[192:199], v[236:239], v81, v80 op_sel_hi:[0,0,0]
	s_mov_b32 m0, s76
	s_nop 0
	buffer_load_dwordx4 v124, s[8:11], s77 offen lds
	v_mfma_scale_f32_16x16x128_f8f6f4 v[52:55], v[228:235], v[168:175], v[52:55], v81, v80 op_sel_hi:[0,0,0]
	v_mfma_scale_f32_16x16x128_f8f6f4 v[48:51], v[240:247], v[168:175], v[48:51], v81, v80 op_sel_hi:[0,0,0]
	v_mfma_scale_f32_16x16x128_f8f6f4 v[36:39], v[228:235], v[176:183], v[36:39], v81, v80 op_sel_hi:[0,0,0]
	v_mfma_scale_f32_16x16x128_f8f6f4 v[32:35], v[240:247], v[176:183], v[32:35], v81, v80 op_sel_hi:[0,0,0]
	v_mfma_scale_f32_16x16x128_f8f6f4 v[20:23], v[228:235], v[184:191], v[20:23], v81, v80 op_sel_hi:[0,0,0]
	v_mfma_scale_f32_16x16x128_f8f6f4 v[16:19], v[240:247], v[184:191], v[16:19], v81, v80 op_sel_hi:[0,0,0]
	v_mfma_scale_f32_16x16x128_f8f6f4 v[4:7], v[228:235], v[192:199], v[4:7], v81, v80 op_sel_hi:[0,0,0]
	v_mfma_scale_f32_16x16x128_f8f6f4 v[0:3], v[240:247], v[192:199], v[0:3], v81, v80 op_sel_hi:[0,0,0]
	s_branch .Lkl_m1npre_y_nd1_j

; #define G_WAIT_V(n) asm volatile("s_waitcnt vmcnt(" #n ")" ::: "memory")
; #define G_BAR() __builtin_amdgcn_s_barrier()
; #define G_SCHED() __builtin_amdgcn_sched_barrier(0)
; #define D_MMA(ai, bj, At, Bf) do { __builtin_amdgcn_s_setprio(1); _Pragma("unroll") for (int m = 0; m < 4; ++m) _Pragma("unroll") for (int n = 0; n < 2; ++n) _Pragma("unroll") for (int k = 0; k < 2; ++k) \
;     acc[ai][bj][m][n] = __builtin_amdgcn_mfma_f32_16x16x32_bf16(Bf[n][k], At[m][k], acc[ai][bj][m][n], 0, 0, 0); __builtin_amdgcn_s_setprio(0); } while (0)
; #define D_MMA(ai, bj, At, Bf) do { if ((ai) && TOPHALF) break; __builtin_amdgcn_s_setprio(1); _Pragma("unroll") for (int m = 0; m < 4; ++m) _Pragma("unroll") for (int n = 0; n < 2; ++n) \
;     acc[ai][bj][m][n] = __builtin_amdgcn_mfma_scale_f32_16x16x128_f8f6f4(Bf[n], At[m], acc[ai][bj][m][n], 0, 0, 0, scw, 0, scx); __builtin_amdgcn_s_setprio(0); } while (0)
;     ...
;     G_WAIT_V(6); G_BAR(); G_SCHED(); D_MMA(1, 1, At, B1); G_BAR(); G_SCHED();
;   }
;   if (!F8_PEEL) G_WAIT_V(0);
.Lkl_m1npre_y_nd1_j:
	s_setprio 0
	s_barrier
	s_add_i32 s82, s82, 2
	s_cmp_lt_u32 s82, 16
	s_cbranch_scc1 .Lkl_m1npre_yl
.Lkl_m1npre_end:
	v_mov_b32_e32 v148, v80
	v_mov_b32_e32 v149, v81
	v_mov_b32_e32 v150, v82
	v_mov_b32_e32 v151, v83
	s_waitcnt vmcnt(0)
	s_cmpk_lt_u32 s15, 0x100
	s_cbranch_scc0 .LBB0_1418
	s_barrier

; #define G_WAIT_V(n) asm volatile("s_waitcnt vmcnt(" #n ")" ::: "memory")
; #define G_BAR() __builtin_amdgcn_s_barrier()
; #define G_SCHED() __builtin_amdgcn_sched_barrier(0)
; #define D_STAGE_A(slot, half, kt) D_STAGE(rsA, voffA, slot, half, kt)
; #define D_STAGE_B(slot, half, kt) D_STAGE(rsB, voffB, slot, half, kt)
; #define D_LDA(dst, slot) do { _Pragma("unroll") for (int m = 0; m < 4; ++m) _Pragma("unroll") for (int k = 0; k < 2; ++k) \
;     dst[m][k] = *(const LDS_AS bf16x8*)(lds + (slot) + aoff + m * 2048 + k * 1024); } while (0)
; #define D_LDB(dst, slot) do { _Pragma("unroll") for (int n = 0; n < 2; ++n) _Pragma("unroll") for (int k = 0; k < 2; ++k) \
;     dst[n][k] = *(const LDS_AS bf16x8*)(lds + (slot) + boff + n * 2048 + k * 1024); } while (0)
; #define D_MMA(ai, bj, At, Bf) do { __builtin_amdgcn_s_setprio(1); _Pragma("unroll") for (int m = 0; m < 4; ++m) _Pragma("unroll") for (int n = 0; n < 2; ++n) _Pragma("unroll") for (int k = 0; k < 2; ++k) \
;     acc[ai][bj][m][n] = __builtin_amdgcn_mfma_f32_16x16x32_bf16(Bf[n][k], At[m][k], acc[ai][bj][m][n], 0, 0, 0); __builtin_amdgcn_s_setprio(0); } while (0)
; #define D_WAIT_L(n) asm volatile("s_waitcnt lgkmcnt(" #n ")" ::: "memory")
; #define D_STAGE_A(slot, half, kt) D_STAGE(rsA, voffA, slot, half, kt)
; #define D_WAIT_L(n) asm volatile("s_waitcnt lgkmcnt(" #n ")" ::: "memory")
;     ...
;   const int scw = cfg.scale_w(), scx = cfg.scale_x();
;     ...
; #pragma clang loop unroll(disable)
;   for (int t = 0; t < (F8_PEEL ? nt - 2 : nt); t += 2) {
;     const int t1 = t + 1;
;     const int t2 = (F8_PEEL || t + 2 < nt) ? t + 2 : t;
;     const int t3 = (F8_PEEL || t + 2 < nt) ? t + 3 : t + 1;
;     D_LDB(B0, G_SB(0, 0)); G_SCHED(); D_LDA(At, G_SA(0, 0)); D_STAGE_A(G_SA(1, 1), 1, t1);
;     D_WAIT_L(8); G_BAR(); D_WAIT_L(0); G_SCHED(); D_MMA(0, 0, At, B0); G_BAR(); G_SCHED();
;     D_LDB(B1, G_SB(0, 1)); D_STAGE_B(G_SB(0, 0), 0, t2);
;     G_BAR(); D_WAIT_L(0); G_SCHED(); D_MMA(0, 1, At, B1); G_BAR(); G_SCHED();
;     D_LDA(At, G_SA(0, 1)); D_STAGE_A(G_SA(0, 0), 0, t2);
;     G_BAR(); D_WAIT_L(0); G_SCHED(); D_MMA(1, 0, At, B0); G_BAR(); G_SCHED();
;     D_STAGE_B(G_SB(0, 1), 1, t2);
;     G_WAIT_V(6); G_BAR(); G_SCHED(); D_MMA(1, 1, At, B1); G_BAR(); G_SCHED();
.LBB0_1483:
	v_mov_b32_e32 v80, v148
	v_mov_b32_e32 v81, v149
	v_mov_b32_e32 v82, v150
	v_mov_b32_e32 v83, v151
	s_mov_b32 s76, 0x10010
	v_add_u32_e32 v130, s76, v124
	v_add_u32_e32 v131, s76, v125
	s_mov_b32 s76, 0x14010
	v_add_u32_e32 v132, s76, v124
	v_add_u32_e32 v133, s76, v125
	s_mov_b32 s76, 0x18010
	v_add_u32_e32 v134, s76, v124
	v_add_u32_e32 v135, s76, v125
	s_mov_b32 s76, 0x1c010
	v_add_u32_e32 v216, s76, v124
	v_add_u32_e32 v217, s76, v125
	s_movk_i32 s72, 0x80
	s_mov_b32 m0, s26
	s_nop 0
	buffer_load_dwordx4 v122, s[8:11], s72 offen lds
	s_mov_b32 m0, s62
	s_nop 0
	buffer_load_dwordx4 v123, s[8:11], s72 offen lds
	s_cmpk_lt_u32 s15, 0x100
	s_cbranch_scc0 .Lkl_m1pre_y
	s_mov_b32 s77, 0
.Lkl_m1pre_x:
	ds_read_b128 v[200:203], v130
	ds_read_b128 v[204:207], v131
	ds_read_b128 v[208:211], v130 offset:2048
	ds_read_b128 v[212:215], v131 offset:2048
	ds_read_b128 v[228:231], v132
	ds_read_b128 v[232:235], v133
	ds_read_b128 v[236:239], v132 offset:2048
	ds_read_b128 v[240:243], v133 offset:2048
	ds_read_b128 v[72:75], v127 offset:16
	ds_read_b128 v[76:79], v128 offset:16
	ds_read_b128 v[144:147], v127 offset:2064
	ds_read_b128 v[148:151], v128 offset:2064
	ds_read_b128 v[152:155], v127 offset:4112
	ds_read_b128 v[156:159], v128 offset:4112
	ds_read_b128 v[160:163], v127 offset:6160
	ds_read_b128 v[164:167], v128 offset:6160
	ds_read_b128 v[168:171], v127 offset:16400
	ds_read_b128 v[172:175], v128 offset:16400
	ds_read_b128 v[176:179], v127 offset:18448
	ds_read_b128 v[180:183], v128 offset:18448
	ds_read_b128 v[184:187], v127 offset:20496
	ds_read_b128 v[188:191], v128 offset:20496
	ds_read_b128 v[192:195], v127 offset:22544
	ds_read_b128 v[196:199], v128 offset:22544
	s_cmp_eq_u32 s77, 0
	s_cbranch_scc1 .Lkl_m1pre_x_nd0
	s_lshl_b32 s72, s77, 7
	s_addk_i32 s72, 0x80
	s_add_i32 s73, s72, 0x20000
	s_add_i32 s74, s72, 0x2000
	s_add_i32 s75, s72, 0x22000
	s_mov_b32 m0, s39
	s_nop 0
	buffer_load_dwordx4 v126, s[4:7], s72 offen lds
	s_mov_b32 m0, s60
	s_nop 0
	buffer_load_dwordx4 v120, s[8:11], s72 offen lds
	s_mov_b32 m0, s69
	s_nop 0
	buffer_load_dwordx4 v126, s[4:7], s73 offen lds
	s_mov_b32 m0, s70
	s_nop 0
	buffer_load_dwordx4 v121, s[8:11], s72 offen lds
	s_mov_b32 m0, s61
	s_nop 0
	buffer_load_dwordx4 v126, s[4:7], s74 offen lds
	s_mov_b32 m0, s26
	s_nop 0
	buffer_load_dwordx4 v122, s[8:11], s72 offen lds
	s_mov_b32 m0, s71
	s_nop 0
	buffer_load_dwordx4 v126, s[4:7], s75 offen lds
	s_mov_b32 m0, s62
	s_nop 0
	buffer_load_dwordx4 v123, s[8:11], s72 offen lds
.Lkl_m1pre_x_nd0:
	s_waitcnt lgkmcnt(0)
	s_barrier
	s_setprio 1
	v_mfma_scale_f32_16x16x128_f8f6f4 v[140:143], v[200:207], v[72:79], v[140:143], v81, v80 op_sel_hi:[0,0,0]
	v_mfma_scale_f32_16x16x128_f8f6f4 v[136:139], v[208:215], v[72:79], v[136:139], v81, v80 op_sel_hi:[0,0,0]
	v_mfma_scale_f32_16x16x128_f8f6f4 v[108:111], v[200:207], v[144:151], v[108:111], v81, v80 op_sel_hi:[0,0,0]
	v_mfma_scale_f32_16x16x128_f8f6f4 v[104:107], v[208:215], v[144:151], v[104:107], v81, v80 op_sel_hi:[0,0,0]
	v_mfma_scale_f32_16x16x128_f8f6f4 v[92:95], v[200:207], v[152:159], v[92:95], v81, v80 op_sel_hi:[0,0,0]
	v_mfma_scale_f32_16x16x128_f8f6f4 v[88:91], v[208:215], v[152:159], v[88:91], v81, v80 op_sel_hi:[0,0,0]
	v_mfma_scale_f32_16x16x128_f8f6f4 v[220:223], v[200:207], v[160:167], v[220:223], v81, v80 op_sel_hi:[0,0,0]
	v_mfma_scale_f32_16x16x128_f8f6f4 v[224:227], v[208:215], v[160:167], v[224:227], v81, v80 op_sel_hi:[0,0,0]
	v_mfma_scale_f32_16x16x128_f8f6f4 v[116:119], v[228:235], v[72:79], v[116:119], v81, v80 op_sel_hi:[0,0,0]
	v_mfma_scale_f32_16x16x128_f8f6f4 v[112:115], v[236:243], v[72:79], v[112:115], v81, v80 op_sel_hi:[0,0,0]
	v_mfma_scale_f32_16x16x128_f8f6f4 v[100:103], v[228:235], v[144:151], v[100:103], v81, v80 op_sel_hi:[0,0,0]
	v_mfma_scale_f32_16x16x128_f8f6f4 v[96:99], v[236:243], v[144:151], v[96:99], v81, v80 op_sel_hi:[0,0,0]
	v_mfma_scale_f32_16x16x128_f8f6f4 v[84:87], v[228:235], v[152:159], v[84:87], v81, v80 op_sel_hi:[0,0,0]
	v_mfma_scale_f32_16x16x128_f8f6f4 v[8:11], v[236:243], v[152:159], v[8:11], v81, v80 op_sel_hi:[0,0,0]
	v_mfma_scale_f32_16x16x128_f8f6f4 v[68:71], v[228:235], v[160:167], v[68:71], v81, v80 op_sel_hi:[0,0,0]
	v_mfma_scale_f32_16x16x128_f8f6f4 v[56:59], v[236:243], v[160:167], v[56:59], v81, v80 op_sel_hi:[0,0,0]
	v_mfma_scale_f32_16x16x128_f8f6f4 v[64:67], v[200:207], v[168:175], v[64:67], v81, v80 op_sel_hi:[0,0,0]
	v_mfma_scale_f32_16x16x128_f8f6f4 v[60:63], v[208:215], v[168:175], v[60:63], v81, v80 op_sel_hi:[0,0,0]
	v_mfma_scale_f32_16x16x128_f8f6f4 v[44:47], v[200:207], v[176:183], v[44:47], v81, v80 op_sel_hi:[0,0,0]
	v_mfma_scale_f32_16x16x128_f8f6f4 v[40:43], v[208:215], v[176:183], v[40:43], v81, v80 op_sel_hi:[0,0,0]
	v_mfma_scale_f32_16x16x128_f8f6f4 v[28:31], v[200:207], v[184:191], v[28:31], v81, v80 op_sel_hi:[0,0,0]
	v_mfma_scale_f32_16x16x128_f8f6f4 v[24:27], v[208:215], v[184:191], v[24:27], v81, v80 op_sel_hi:[0,0,0]
	v_mfma_scale_f32_16x16x128_f8f6f4 v[12:15], v[200:207], v[192:199], v[12:15], v81, v80 op_sel_hi:[0,0,0]
	v_mfma_scale_f32_16x16x128_f8f6f4 v[244:247], v[208:215], v[192:199], v[244:247], v81, v80 op_sel_hi:[0,0,0]
	v_mfma_scale_f32_16x16x128_f8f6f4 v[52:55], v[228:235], v[168:175], v[52:55], v81, v80 op_sel_hi:[0,0,0]
	v_mfma_scale_f32_16x16x128_f8f6f4 v[48:51], v[236:243], v[168:175], v[48:51], v81, v80 op_sel_hi:[0,0,0]
	v_mfma_scale_f32_16x16x128_f8f6f4 v[36:39], v[228:235], v[176:183], v[36:39], v81, v80 op_sel_hi:[0,0,0]
	v_mfma_scale_f32_16x16x128_f8f6f4 v[32:35], v[236:243], v[176:183], v[32:35], v81, v80 op_sel_hi:[0,0,0]
	v_mfma_scale_f32_16x16x128_f8f6f4 v[20:23], v[228:235], v[184:191], v[20:23], v81, v80 op_sel_hi:[0,0,0]
	v_mfma_scale_f32_16x16x128_f8f6f4 v[16:19], v[236:243], v[184:191], v[16:19], v81, v80 op_sel_hi:[0,0,0]
	v_mfma_scale_f32_16x16x128_f8f6f4 v[4:7], v[228:235], v[192:199], v[4:7], v81, v80 op_sel_hi:[0,0,0]
	v_mfma_scale_f32_16x16x128_f8f6f4 v[0:3], v[236:243], v[192:199], v[0:3], v81, v80 op_sel_hi:[0,0,0]
	s_setprio 0
	s_waitcnt vmcnt(0)
	s_barrier
; #define G_WAIT_V(n) asm volatile("s_waitcnt vmcnt(" #n ")" ::: "memory")
; #define G_BAR() __builtin_amdgcn_s_barrier()
; #define G_SCHED() __builtin_amdgcn_sched_barrier(0)
; #define D_STAGE_A(slot, half, kt) D_STAGE(rsA, voffA, slot, half, kt)
; #define D_STAGE_B(slot, half, kt) D_STAGE(rsB, voffB, slot, half, kt)
; #define D_LDA(dst, slot) do { _Pragma("unroll") for (int m = 0; m < 4; ++m) _Pragma("unroll") for (int k = 0; k < 2; ++k) \
;     dst[m][k] = *(const LDS_AS bf16x8*)(lds + (slot) + aoff + m * 2048 + k * 1024); } while (0)
; #define D_LDB(dst, slot) do { _Pragma("unroll") for (int n = 0; n < 2; ++n) _Pragma("unroll") for (int k = 0; k < 2; ++k) \
;     dst[n][k] = *(const LDS_AS bf16x8*)(lds + (slot) + boff + n * 2048 + k * 1024); } while (0)
; #define D_MMA(ai, bj, At, Bf) do { __builtin_amdgcn_s_setprio(1); _Pragma("unroll") for (int m = 0; m < 4; ++m) _Pragma("unroll") for (int n = 0; n < 2; ++n) _Pragma("unroll") for (int k = 0; k < 2; ++k) \
;     acc[ai][bj][m][n] = __builtin_amdgcn_mfma_f32_16x16x32_bf16(Bf[n][k], At[m][k], acc[ai][bj][m][n], 0, 0, 0); __builtin_amdgcn_s_setprio(0); } while (0)
; #define D_WAIT_L(n) asm volatile("s_waitcnt lgkmcnt(" #n ")" ::: "memory")
; #define D_STAGE_A(slot, half, kt) D_STAGE(rsA, voffA, slot, half, kt)
; #define D_STAGE_B(slot, half, kt) do { _Pragma("unroll") for (int _i = 0; _i < 2; ++_i) { const unsigned _m0 = ldsw + (unsigned)((slot) + _i * 8192); const unsigned _so = (unsigned)(kt) * 128u + (half) * bt_half + _i * bt_piece; \
;     asm volatile("s_mov_b32 m0, %0\n\ts_nop 4\n\tbuffer_load_dwordx4 %1, %2, %3 offen lds" :: "s"(_m0), "v"(voffB0), "s"(rsB), "s"(_so) : "m0", "memory"); } } while (0)
; #define D_WAIT_L(n) asm volatile("s_waitcnt lgkmcnt(" #n ")" ::: "memory")
;     ...
;   const int scw = cfg.scale_w(), scx = cfg.scale_x();
;     ...
;     D_LDB(B0, G_SB(1, 0)); G_SCHED(); D_LDA(At, G_SA(1, 0)); D_STAGE_A(G_SA(0, 1), 1, t2);
;     D_WAIT_L(8); G_BAR(); D_WAIT_L(0); G_SCHED(); D_MMA(0, 0, At, B0); G_BAR(); G_SCHED();
;     D_LDB(B1, G_SB(1, 1)); D_STAGE_B(G_SB(1, 0), 0, t3);
;     G_BAR(); D_WAIT_L(0); G_SCHED(); D_MMA(0, 1, At, B1); G_BAR(); G_SCHED();
;     D_LDA(At, G_SA(1, 1)); D_STAGE_A(G_SA(1, 0), 0, t3);
;     G_BAR(); D_WAIT_L(0); G_SCHED(); D_MMA(1, 0, At, B0); G_BAR(); G_SCHED();
;     D_STAGE_B(G_SB(1, 1), 1, t3);
;     G_WAIT_V(6); G_BAR(); G_SCHED(); D_MMA(1, 1, At, B1); G_BAR(); G_SCHED();
	ds_read_b128 v[200:203], v134
	ds_read_b128 v[204:207], v135
	ds_read_b128 v[208:211], v134 offset:2048
	ds_read_b128 v[212:215], v135 offset:2048
	ds_read_b128 v[228:231], v216
	ds_read_b128 v[232:235], v217
	ds_read_b128 v[236:239], v216 offset:2048
	ds_read_b128 v[240:243], v217 offset:2048
	ds_read_b128 v[72:75], v127 offset:32784
	ds_read_b128 v[76:79], v128 offset:32784
	ds_read_b128 v[144:147], v127 offset:34832
	ds_read_b128 v[148:151], v128 offset:34832
	ds_read_b128 v[152:155], v127 offset:36880
	ds_read_b128 v[156:159], v128 offset:36880
	ds_read_b128 v[160:163], v127 offset:38928
	ds_read_b128 v[164:167], v128 offset:38928
	ds_read_b128 v[168:171], v127 offset:49168
	ds_read_b128 v[172:175], v128 offset:49168
	ds_read_b128 v[176:179], v127 offset:51216
	ds_read_b128 v[180:183], v128 offset:51216
	ds_read_b128 v[184:187], v127 offset:53264
	ds_read_b128 v[188:191], v128 offset:53264
	ds_read_b128 v[192:195], v127 offset:55312
	ds_read_b128 v[196:199], v128 offset:55312
	s_cmp_ge_u32 s77, 14
	s_cbranch_scc1 .Lkl_m1pre_x_nd1
	s_lshl_b32 s72, s77, 7
	s_addk_i32 s72, 0x100
	s_add_i32 s73, s72, 0x20000
	s_add_i32 s74, s72, 0x2000
	s_add_i32 s75, s72, 0x22000
	s_mov_b32 m0, s27
	s_nop 0
	buffer_load_dwordx4 v126, s[4:7], s72 offen lds
	s_mov_b32 m0, s17
	s_nop 0
	buffer_load_dwordx4 v120, s[8:11], s72 offen lds
	s_mov_b32 m0, s63
	s_nop 0
	buffer_load_dwordx4 v126, s[4:7], s73 offen lds
	s_mov_b32 m0, s66
	s_nop 0
	buffer_load_dwordx4 v121, s[8:11], s72 offen lds
	s_mov_b32 m0, s28
	s_nop 0
	buffer_load_dwordx4 v126, s[4:7], s74 offen lds
	s_mov_b32 m0, s29
	s_nop 0
	buffer_load_dwordx4 v122, s[8:11], s72 offen lds
	s_mov_b32 m0, s67
	s_nop 0
	buffer_load_dwordx4 v126, s[4:7], s75 offen lds
	s_mov_b32 m0, s68
	s_nop 0
	buffer_load_dwordx4 v123, s[8:11], s72 offen lds
.Lkl_m1pre_x_nd1:
	s_waitcnt lgkmcnt(0)
	s_barrier
	s_setprio 1
	v_mfma_scale_f32_16x16x128_f8f6f4 v[140:143], v[200:207], v[72:79], v[140:143], v81, v80 op_sel_hi:[0,0,0]
	v_mfma_scale_f32_16x16x128_f8f6f4 v[136:139], v[208:215], v[72:79], v[136:139], v81, v80 op_sel_hi:[0,0,0]
	v_mfma_scale_f32_16x16x128_f8f6f4 v[108:111], v[200:207], v[144:151], v[108:111], v81, v80 op_sel_hi:[0,0,0]
	v_mfma_scale_f32_16x16x128_f8f6f4 v[104:107], v[208:215], v[144:151], v[104:107], v81, v80 op_sel_hi:[0,0,0]
	v_mfma_scale_f32_16x16x128_f8f6f4 v[92:95], v[200:207], v[152:159], v[92:95], v81, v80 op_sel_hi:[0,0,0]
	v_mfma_scale_f32_16x16x128_f8f6f4 v[88:91], v[208:215], v[152:159], v[88:91], v81, v80 op_sel_hi:[0,0,0]
	v_mfma_scale_f32_16x16x128_f8f6f4 v[220:223], v[200:207], v[160:167], v[220:223], v81, v80 op_sel_hi:[0,0,0]
	v_mfma_scale_f32_16x16x128_f8f6f4 v[224:227], v[208:215], v[160:167], v[224:227], v81, v80 op_sel_hi:[0,0,0]
	v_mfma_scale_f32_16x16x128_f8f6f4 v[116:119], v[228:235], v[72:79], v[116:119], v81, v80 op_sel_hi:[0,0,0]
	v_mfma_scale_f32_16x16x128_f8f6f4 v[112:115], v[236:243], v[72:79], v[112:115], v81, v80 op_sel_hi:[0,0,0]
	v_mfma_scale_f32_16x16x128_f8f6f4 v[100:103], v[228:235], v[144:151], v[100:103], v81, v80 op_sel_hi:[0,0,0]
	v_mfma_scale_f32_16x16x128_f8f6f4 v[96:99], v[236:243], v[144:151], v[96:99], v81, v80 op_sel_hi:[0,0,0]
	v_mfma_scale_f32_16x16x128_f8f6f4 v[84:87], v[228:235], v[152:159], v[84:87], v81, v80 op_sel_hi:[0,0,0]
	v_mfma_scale_f32_16x16x128_f8f6f4 v[8:11], v[236:243], v[152:159], v[8:11], v81, v80 op_sel_hi:[0,0,0]
	v_mfma_scale_f32_16x16x128_f8f6f4 v[68:71], v[228:235], v[160:167], v[68:71], v81, v80 op_sel_hi:[0,0,0]
	v_mfma_scale_f32_16x16x128_f8f6f4 v[56:59], v[236:243], v[160:167], v[56:59], v81, v80 op_sel_hi:[0,0,0]
	v_mfma_scale_f32_16x16x128_f8f6f4 v[64:67], v[200:207], v[168:175], v[64:67], v81, v80 op_sel_hi:[0,0,0]
	v_mfma_scale_f32_16x16x128_f8f6f4 v[60:63], v[208:215], v[168:175], v[60:63], v81, v80 op_sel_hi:[0,0,0]
	v_mfma_scale_f32_16x16x128_f8f6f4 v[44:47], v[200:207], v[176:183], v[44:47], v81, v80 op_sel_hi:[0,0,0]
	v_mfma_scale_f32_16x16x128_f8f6f4 v[40:43], v[208:215], v[176:183], v[40:43], v81, v80 op_sel_hi:[0,0,0]
	v_mfma_scale_f32_16x16x128_f8f6f4 v[28:31], v[200:207], v[184:191], v[28:31], v81, v80 op_sel_hi:[0,0,0]
	v_mfma_scale_f32_16x16x128_f8f6f4 v[24:27], v[208:215], v[184:191], v[24:27], v81, v80 op_sel_hi:[0,0,0]
	v_mfma_scale_f32_16x16x128_f8f6f4 v[12:15], v[200:207], v[192:199], v[12:15], v81, v80 op_sel_hi:[0,0,0]
	v_mfma_scale_f32_16x16x128_f8f6f4 v[244:247], v[208:215], v[192:199], v[244:247], v81, v80 op_sel_hi:[0,0,0]
	v_mfma_scale_f32_16x16x128_f8f6f4 v[52:55], v[228:235], v[168:175], v[52:55], v81, v80 op_sel_hi:[0,0,0]
	v_mfma_scale_f32_16x16x128_f8f6f4 v[48:51], v[236:243], v[168:175], v[48:51], v81, v80 op_sel_hi:[0,0,0]
	v_mfma_scale_f32_16x16x128_f8f6f4 v[36:39], v[228:235], v[176:183], v[36:39], v81, v80 op_sel_hi:[0,0,0]
	v_mfma_scale_f32_16x16x128_f8f6f4 v[32:35], v[236:243], v[176:183], v[32:35], v81, v80 op_sel_hi:[0,0,0]
	v_mfma_scale_f32_16x16x128_f8f6f4 v[20:23], v[228:235], v[184:191], v[20:23], v81, v80 op_sel_hi:[0,0,0]
	v_mfma_scale_f32_16x16x128_f8f6f4 v[16:19], v[236:243], v[184:191], v[16:19], v81, v80 op_sel_hi:[0,0,0]
	v_mfma_scale_f32_16x16x128_f8f6f4 v[4:7], v[228:235], v[192:199], v[4:7], v81, v80 op_sel_hi:[0,0,0]
	v_mfma_scale_f32_16x16x128_f8f6f4 v[0:3], v[236:243], v[192:199], v[0:3], v81, v80 op_sel_hi:[0,0,0]
	s_setprio 0
	s_waitcnt vmcnt(0)
	s_barrier
	s_add_i32 s77, s77, 2
	s_cmp_lt_u32 s77, 16
	s_cbranch_scc1 .Lkl_m1pre_x
	s_branch .Lkl_m1pre_end
.Lkl_m1pre_y:
	s_mov_b32 s77, 0
; #define G_WAIT_V(n) asm volatile("s_waitcnt vmcnt(" #n ")" ::: "memory")
; #define G_BAR() __builtin_amdgcn_s_barrier()
; #define G_SCHED() __builtin_amdgcn_sched_barrier(0)
; #define D_STAGE_A(slot, half, kt) D_STAGE(rsA, voffA, slot, half, kt)
; #define D_STAGE_B(slot, half, kt) D_STAGE(rsB, voffB, slot, half, kt)
; #define D_LDA(dst, slot) do { _Pragma("unroll") for (int m = 0; m < 4; ++m) _Pragma("unroll") for (int k = 0; k < 2; ++k) \
;     dst[m][k] = *(const LDS_AS bf16x8*)(lds + (slot) + aoff + m * 2048 + k * 1024); } while (0)
; #define D_LDB(dst, slot) do { _Pragma("unroll") for (int n = 0; n < 2; ++n) _Pragma("unroll") for (int k = 0; k < 2; ++k) \
;     dst[n][k] = *(const LDS_AS bf16x8*)(lds + (slot) + boff + n * 2048 + k * 1024); } while (0)
; #define D_MMA(ai, bj, At, Bf) do { __builtin_amdgcn_s_setprio(1); _Pragma("unroll") for (int m = 0; m < 4; ++m) _Pragma("unroll") for (int n = 0; n < 2; ++n) _Pragma("unroll") for (int k = 0; k < 2; ++k) \
;     acc[ai][bj][m][n] = __builtin_amdgcn_mfma_f32_16x16x32_bf16(Bf[n][k], At[m][k], acc[ai][bj][m][n], 0, 0, 0); __builtin_amdgcn_s_setprio(0); } while (0)
; #define D_WAIT_L(n) asm volatile("s_waitcnt lgkmcnt(" #n ")" ::: "memory")
; #define D_STAGE_A(slot, half, kt) D_STAGE(rsA, voffA, slot, half, kt)
; #define D_STAGE_B(slot, half, kt) do { _Pragma("unroll") for (int _i = 0; _i < 2; ++_i) { const unsigned _m0 = ldsw + (unsigned)((slot) + _i * 8192); const unsigned _so = (unsigned)(kt) * 128u + (half) * bt_half + _i * bt_piece; \
;     asm volatile("s_mov_b32 m0, %0\n\ts_nop 4\n\tbuffer_load_dwordx4 %1, %2, %3 offen lds" :: "s"(_m0), "v"(voffB0), "s"(rsB), "s"(_so) : "m0", "memory"); } } while (0)
; #define D_WAIT_L(n) asm volatile("s_waitcnt lgkmcnt(" #n ")" ::: "memory")
;     ...
;     D_LDB(B0, G_SB(0, 0)); G_SCHED(); D_LDA(At, G_SA(0, 0)); D_STAGE_A(G_SA(1, 1), 1, t1);
;     D_WAIT_L(8); G_BAR(); D_WAIT_L(0); G_SCHED(); D_MMA(0, 0, At, B0); G_BAR(); G_SCHED();
;     D_LDB(B1, G_SB(0, 1)); D_STAGE_B(G_SB(0, 0), 0, t2);
;     G_BAR(); D_WAIT_L(0); G_SCHED(); D_MMA(0, 1, At, B1); G_BAR(); G_SCHED();
;     D_LDA(At, G_SA(0, 1)); D_STAGE_A(G_SA(0, 0), 0, t2);
;     G_BAR(); D_WAIT_L(0); G_SCHED(); D_MMA(1, 0, At, B0); G_BAR(); G_SCHED();
;     D_STAGE_B(G_SB(0, 1), 1, t2);
;     G_WAIT_V(6); G_BAR(); G_SCHED(); D_MMA(1, 1, At, B1); G_BAR(); G_SCHED();
.Lkl_m1pre_yl:
	ds_read_b128 v[200:203], v130
	ds_read_b128 v[204:207], v131
	ds_read_b128 v[208:211], v130 offset:2048
	ds_read_b128 v[212:215], v131 offset:2048
	ds_read_b128 v[228:231], v132
	ds_read_b128 v[232:235], v133
	ds_read_b128 v[236:239], v132 offset:2048
	ds_read_b128 v[240:243], v133 offset:2048
	ds_read_b128 v[72:75], v127 offset:16
	ds_read_b128 v[76:79], v128 offset:16
	ds_read_b128 v[144:147], v127 offset:2064
	ds_read_b128 v[148:151], v128 offset:2064
	ds_read_b128 v[152:155], v127 offset:4112
	ds_read_b128 v[156:159], v128 offset:4112
	ds_read_b128 v[160:163], v127 offset:6160
	ds_read_b128 v[164:167], v128 offset:6160
	ds_read_b128 v[168:171], v127 offset:16400
	ds_read_b128 v[172:175], v128 offset:16400
	ds_read_b128 v[176:179], v127 offset:18448
	ds_read_b128 v[180:183], v128 offset:18448
	ds_read_b128 v[184:187], v127 offset:20496
	ds_read_b128 v[188:191], v128 offset:20496
	ds_read_b128 v[192:195], v127 offset:22544
	ds_read_b128 v[196:199], v128 offset:22544
	s_waitcnt lgkmcnt(0)
	s_waitcnt vmcnt(0)
	s_barrier
	s_setprio 1
	s_cmp_ge_u32 s77, 14
	s_cbranch_scc1 .Lkl_m1pre_y_nd0
	s_lshl_b32 s72, s77, 7
	s_addk_i32 s72, 0x100
	s_add_i32 s73, s72, 0x20000
	s_add_i32 s74, s72, 0x2000
	s_add_i32 s75, s72, 0x22000
	v_mfma_scale_f32_16x16x128_f8f6f4 v[140:143], v[200:207], v[72:79], v[140:143], v81, v80 op_sel_hi:[0,0,0]
	v_mfma_scale_f32_16x16x128_f8f6f4 v[136:139], v[208:215], v[72:79], v[136:139], v81, v80 op_sel_hi:[0,0,0]
	v_mfma_scale_f32_16x16x128_f8f6f4 v[108:111], v[200:207], v[144:151], v[108:111], v81, v80 op_sel_hi:[0,0,0]
	s_mov_b32 m0, s27
	s_nop 0
	buffer_load_dwordx4 v126, s[4:7], s72 offen lds
	v_mfma_scale_f32_16x16x128_f8f6f4 v[104:107], v[208:215], v[144:151], v[104:107], v81, v80 op_sel_hi:[0,0,0]
	v_mfma_scale_f32_16x16x128_f8f6f4 v[92:95], v[200:207], v[152:159], v[92:95], v81, v80 op_sel_hi:[0,0,0]
	v_mfma_scale_f32_16x16x128_f8f6f4 v[88:91], v[208:215], v[152:159], v[88:91], v81, v80 op_sel_hi:[0,0,0]
	s_mov_b32 m0, s17
	s_nop 0
	buffer_load_dwordx4 v120, s[8:11], s72 offen lds
	v_mfma_scale_f32_16x16x128_f8f6f4 v[220:223], v[200:207], v[160:167], v[220:223], v81, v80 op_sel_hi:[0,0,0]
	v_mfma_scale_f32_16x16x128_f8f6f4 v[224:227], v[208:215], v[160:167], v[224:227], v81, v80 op_sel_hi:[0,0,0]
	v_mfma_scale_f32_16x16x128_f8f6f4 v[116:119], v[228:235], v[72:79], v[116:119], v81, v80 op_sel_hi:[0,0,0]
	s_mov_b32 m0, s63
	s_nop 0
	buffer_load_dwordx4 v126, s[4:7], s73 offen lds
	v_mfma_scale_f32_16x16x128_f8f6f4 v[112:115], v[236:243], v[72:79], v[112:115], v81, v80 op_sel_hi:[0,0,0]
	v_mfma_scale_f32_16x16x128_f8f6f4 v[100:103], v[228:235], v[144:151], v[100:103], v81, v80 op_sel_hi:[0,0,0]
	v_mfma_scale_f32_16x16x128_f8f6f4 v[96:99], v[236:243], v[144:151], v[96:99], v81, v80 op_sel_hi:[0,0,0]
	s_mov_b32 m0, s66
	s_nop 0
	buffer_load_dwordx4 v121, s[8:11], s72 offen lds
	v_mfma_scale_f32_16x16x128_f8f6f4 v[84:87], v[228:235], v[152:159], v[84:87], v81, v80 op_sel_hi:[0,0,0]
	v_mfma_scale_f32_16x16x128_f8f6f4 v[8:11], v[236:243], v[152:159], v[8:11], v81, v80 op_sel_hi:[0,0,0]
	v_mfma_scale_f32_16x16x128_f8f6f4 v[68:71], v[228:235], v[160:167], v[68:71], v81, v80 op_sel_hi:[0,0,0]
	s_mov_b32 m0, s28
	s_nop 0
	buffer_load_dwordx4 v126, s[4:7], s74 offen lds
	v_mfma_scale_f32_16x16x128_f8f6f4 v[56:59], v[236:243], v[160:167], v[56:59], v81, v80 op_sel_hi:[0,0,0]
	v_mfma_scale_f32_16x16x128_f8f6f4 v[64:67], v[200:207], v[168:175], v[64:67], v81, v80 op_sel_hi:[0,0,0]
	v_mfma_scale_f32_16x16x128_f8f6f4 v[60:63], v[208:215], v[168:175], v[60:63], v81, v80 op_sel_hi:[0,0,0]
	s_mov_b32 m0, s29
	s_nop 0
	buffer_load_dwordx4 v122, s[8:11], s72 offen lds
	v_mfma_scale_f32_16x16x128_f8f6f4 v[44:47], v[200:207], v[176:183], v[44:47], v81, v80 op_sel_hi:[0,0,0]
	v_mfma_scale_f32_16x16x128_f8f6f4 v[40:43], v[208:215], v[176:183], v[40:43], v81, v80 op_sel_hi:[0,0,0]
	v_mfma_scale_f32_16x16x128_f8f6f4 v[28:31], v[200:207], v[184:191], v[28:31], v81, v80 op_sel_hi:[0,0,0]
	s_mov_b32 m0, s67
	s_nop 0
	buffer_load_dwordx4 v126, s[4:7], s75 offen lds
	v_mfma_scale_f32_16x16x128_f8f6f4 v[24:27], v[208:215], v[184:191], v[24:27], v81, v80 op_sel_hi:[0,0,0]
	v_mfma_scale_f32_16x16x128_f8f6f4 v[12:15], v[200:207], v[192:199], v[12:15], v81, v80 op_sel_hi:[0,0,0]
	v_mfma_scale_f32_16x16x128_f8f6f4 v[244:247], v[208:215], v[192:199], v[244:247], v81, v80 op_sel_hi:[0,0,0]
	s_mov_b32 m0, s68
	s_nop 0
	buffer_load_dwordx4 v123, s[8:11], s72 offen lds
	v_mfma_scale_f32_16x16x128_f8f6f4 v[52:55], v[228:235], v[168:175], v[52:55], v81, v80 op_sel_hi:[0,0,0]
	v_mfma_scale_f32_16x16x128_f8f6f4 v[48:51], v[236:243], v[168:175], v[48:51], v81, v80 op_sel_hi:[0,0,0]
	v_mfma_scale_f32_16x16x128_f8f6f4 v[36:39], v[228:235], v[176:183], v[36:39], v81, v80 op_sel_hi:[0,0,0]
	v_mfma_scale_f32_16x16x128_f8f6f4 v[32:35], v[236:243], v[176:183], v[32:35], v81, v80 op_sel_hi:[0,0,0]
	v_mfma_scale_f32_16x16x128_f8f6f4 v[20:23], v[228:235], v[184:191], v[20:23], v81, v80 op_sel_hi:[0,0,0]
	v_mfma_scale_f32_16x16x128_f8f6f4 v[16:19], v[236:243], v[184:191], v[16:19], v81, v80 op_sel_hi:[0,0,0]
	v_mfma_scale_f32_16x16x128_f8f6f4 v[4:7], v[228:235], v[192:199], v[4:7], v81, v80 op_sel_hi:[0,0,0]
	v_mfma_scale_f32_16x16x128_f8f6f4 v[0:3], v[236:243], v[192:199], v[0:3], v81, v80 op_sel_hi:[0,0,0]
	s_branch .Lkl_m1pre_y_nd0_j
.Lkl_m1pre_y_nd0:
	v_mfma_scale_f32_16x16x128_f8f6f4 v[140:143], v[200:207], v[72:79], v[140:143], v81, v80 op_sel_hi:[0,0,0]
	v_mfma_scale_f32_16x16x128_f8f6f4 v[136:139], v[208:215], v[72:79], v[136:139], v81, v80 op_sel_hi:[0,0,0]
	v_mfma_scale_f32_16x16x128_f8f6f4 v[108:111], v[200:207], v[144:151], v[108:111], v81, v80 op_sel_hi:[0,0,0]
	v_mfma_scale_f32_16x16x128_f8f6f4 v[104:107], v[208:215], v[144:151], v[104:107], v81, v80 op_sel_hi:[0,0,0]
	v_mfma_scale_f32_16x16x128_f8f6f4 v[92:95], v[200:207], v[152:159], v[92:95], v81, v80 op_sel_hi:[0,0,0]
	v_mfma_scale_f32_16x16x128_f8f6f4 v[88:91], v[208:215], v[152:159], v[88:91], v81, v80 op_sel_hi:[0,0,0]
	v_mfma_scale_f32_16x16x128_f8f6f4 v[220:223], v[200:207], v[160:167], v[220:223], v81, v80 op_sel_hi:[0,0,0]
	v_mfma_scale_f32_16x16x128_f8f6f4 v[224:227], v[208:215], v[160:167], v[224:227], v81, v80 op_sel_hi:[0,0,0]
	v_mfma_scale_f32_16x16x128_f8f6f4 v[116:119], v[228:235], v[72:79], v[116:119], v81, v80 op_sel_hi:[0,0,0]
	v_mfma_scale_f32_16x16x128_f8f6f4 v[112:115], v[236:243], v[72:79], v[112:115], v81, v80 op_sel_hi:[0,0,0]
	v_mfma_scale_f32_16x16x128_f8f6f4 v[100:103], v[228:235], v[144:151], v[100:103], v81, v80 op_sel_hi:[0,0,0]
	v_mfma_scale_f32_16x16x128_f8f6f4 v[96:99], v[236:243], v[144:151], v[96:99], v81, v80 op_sel_hi:[0,0,0]
	v_mfma_scale_f32_16x16x128_f8f6f4 v[84:87], v[228:235], v[152:159], v[84:87], v81, v80 op_sel_hi:[0,0,0]
	v_mfma_scale_f32_16x16x128_f8f6f4 v[8:11], v[236:243], v[152:159], v[8:11], v81, v80 op_sel_hi:[0,0,0]
	v_mfma_scale_f32_16x16x128_f8f6f4 v[68:71], v[228:235], v[160:167], v[68:71], v81, v80 op_sel_hi:[0,0,0]
	v_mfma_scale_f32_16x16x128_f8f6f4 v[56:59], v[236:243], v[160:167], v[56:59], v81, v80 op_sel_hi:[0,0,0]
	v_mfma_scale_f32_16x16x128_f8f6f4 v[64:67], v[200:207], v[168:175], v[64:67], v81, v80 op_sel_hi:[0,0,0]
	v_mfma_scale_f32_16x16x128_f8f6f4 v[60:63], v[208:215], v[168:175], v[60:63], v81, v80 op_sel_hi:[0,0,0]
	v_mfma_scale_f32_16x16x128_f8f6f4 v[44:47], v[200:207], v[176:183], v[44:47], v81, v80 op_sel_hi:[0,0,0]
	v_mfma_scale_f32_16x16x128_f8f6f4 v[40:43], v[208:215], v[176:183], v[40:43], v81, v80 op_sel_hi:[0,0,0]
	v_mfma_scale_f32_16x16x128_f8f6f4 v[28:31], v[200:207], v[184:191], v[28:31], v81, v80 op_sel_hi:[0,0,0]
	v_mfma_scale_f32_16x16x128_f8f6f4 v[24:27], v[208:215], v[184:191], v[24:27], v81, v80 op_sel_hi:[0,0,0]
	v_mfma_scale_f32_16x16x128_f8f6f4 v[12:15], v[200:207], v[192:199], v[12:15], v81, v80 op_sel_hi:[0,0,0]
	v_mfma_scale_f32_16x16x128_f8f6f4 v[244:247], v[208:215], v[192:199], v[244:247], v81, v80 op_sel_hi:[0,0,0]
	v_mfma_scale_f32_16x16x128_f8f6f4 v[52:55], v[228:235], v[168:175], v[52:55], v81, v80 op_sel_hi:[0,0,0]
	v_mfma_scale_f32_16x16x128_f8f6f4 v[48:51], v[236:243], v[168:175], v[48:51], v81, v80 op_sel_hi:[0,0,0]
	v_mfma_scale_f32_16x16x128_f8f6f4 v[36:39], v[228:235], v[176:183], v[36:39], v81, v80 op_sel_hi:[0,0,0]
	v_mfma_scale_f32_16x16x128_f8f6f4 v[32:35], v[236:243], v[176:183], v[32:35], v81, v80 op_sel_hi:[0,0,0]
	v_mfma_scale_f32_16x16x128_f8f6f4 v[20:23], v[228:235], v[184:191], v[20:23], v81, v80 op_sel_hi:[0,0,0]
	v_mfma_scale_f32_16x16x128_f8f6f4 v[16:19], v[236:243], v[184:191], v[16:19], v81, v80 op_sel_hi:[0,0,0]
	v_mfma_scale_f32_16x16x128_f8f6f4 v[4:7], v[228:235], v[192:199], v[4:7], v81, v80 op_sel_hi:[0,0,0]
	v_mfma_scale_f32_16x16x128_f8f6f4 v[0:3], v[236:243], v[192:199], v[0:3], v81, v80 op_sel_hi:[0,0,0]
; #define G_WAIT_V(n) asm volatile("s_waitcnt vmcnt(" #n ")" ::: "memory")
; #define G_BAR() __builtin_amdgcn_s_barrier()
; #define G_SCHED() __builtin_amdgcn_sched_barrier(0)
; #define D_STAGE_A(slot, half, kt) D_STAGE(rsA, voffA, slot, half, kt)
; #define D_STAGE_B(slot, half, kt) D_STAGE(rsB, voffB, slot, half, kt)
; #define D_LDA(dst, slot) do { _Pragma("unroll") for (int m = 0; m < 4; ++m) _Pragma("unroll") for (int k = 0; k < 2; ++k) \
;     dst[m][k] = *(const LDS_AS bf16x8*)(lds + (slot) + aoff + m * 2048 + k * 1024); } while (0)
; #define D_LDB(dst, slot) do { _Pragma("unroll") for (int n = 0; n < 2; ++n) _Pragma("unroll") for (int k = 0; k < 2; ++k) \
;     dst[n][k] = *(const LDS_AS bf16x8*)(lds + (slot) + boff + n * 2048 + k * 1024); } while (0)
; #define D_MMA(ai, bj, At, Bf) do { __builtin_amdgcn_s_setprio(1); _Pragma("unroll") for (int m = 0; m < 4; ++m) _Pragma("unroll") for (int n = 0; n < 2; ++n) _Pragma("unroll") for (int k = 0; k < 2; ++k) \
;     acc[ai][bj][m][n] = __builtin_amdgcn_mfma_f32_16x16x32_bf16(Bf[n][k], At[m][k], acc[ai][bj][m][n], 0, 0, 0); __builtin_amdgcn_s_setprio(0); } while (0)
; #define D_WAIT_L(n) asm volatile("s_waitcnt lgkmcnt(" #n ")" ::: "memory")
; #define D_STAGE_A(slot, half, kt) D_STAGE(rsA, voffA, slot, half, kt)
; #define D_STAGE_B(slot, half, kt) do { _Pragma("unroll") for (int _i = 0; _i < 2; ++_i) { const unsigned _m0 = ldsw + (unsigned)((slot) + _i * 8192); const unsigned _so = (unsigned)(kt) * 128u + (half) * bt_half + _i * bt_piece; \
;     asm volatile("s_mov_b32 m0, %0\n\ts_nop 4\n\tbuffer_load_dwordx4 %1, %2, %3 offen lds" :: "s"(_m0), "v"(voffB0), "s"(rsB), "s"(_so) : "m0", "memory"); } } while (0)
; #define D_WAIT_L(n) asm volatile("s_waitcnt lgkmcnt(" #n ")" ::: "memory")
;     ...
;     D_LDB(B0, G_SB(1, 0)); G_SCHED(); D_LDA(At, G_SA(1, 0)); D_STAGE_A(G_SA(0, 1), 1, t2);
;     D_WAIT_L(8); G_BAR(); D_WAIT_L(0); G_SCHED(); D_MMA(0, 0, At, B0); G_BAR(); G_SCHED();
;     D_LDB(B1, G_SB(1, 1)); D_STAGE_B(G_SB(1, 0), 0, t3);
;     G_BAR(); D_WAIT_L(0); G_SCHED(); D_MMA(0, 1, At, B1); G_BAR(); G_SCHED();
;     D_LDA(At, G_SA(1, 1)); D_STAGE_A(G_SA(1, 0), 0, t3);
;     G_BAR(); D_WAIT_L(0); G_SCHED(); D_MMA(1, 0, At, B0); G_BAR(); G_SCHED();
;     D_STAGE_B(G_SB(1, 1), 1, t3);
;     G_WAIT_V(6); G_BAR(); G_SCHED(); D_MMA(1, 1, At, B1); G_BAR(); G_SCHED();
.Lkl_m1pre_y_nd0_j:
	s_setprio 0
	s_barrier
	ds_read_b128 v[200:203], v134
	ds_read_b128 v[204:207], v135
	ds_read_b128 v[208:211], v134 offset:2048
	ds_read_b128 v[212:215], v135 offset:2048
	ds_read_b128 v[228:231], v216
	ds_read_b128 v[232:235], v217
	ds_read_b128 v[236:239], v216 offset:2048
	ds_read_b128 v[240:243], v217 offset:2048
	ds_read_b128 v[72:75], v127 offset:32784
	ds_read_b128 v[76:79], v128 offset:32784
	ds_read_b128 v[144:147], v127 offset:34832
	ds_read_b128 v[148:151], v128 offset:34832
	ds_read_b128 v[152:155], v127 offset:36880
	ds_read_b128 v[156:159], v128 offset:36880
	ds_read_b128 v[160:163], v127 offset:38928
	ds_read_b128 v[164:167], v128 offset:38928
	ds_read_b128 v[168:171], v127 offset:49168
	ds_read_b128 v[172:175], v128 offset:49168
	ds_read_b128 v[176:179], v127 offset:51216
	ds_read_b128 v[180:183], v128 offset:51216
	ds_read_b128 v[184:187], v127 offset:53264
	ds_read_b128 v[188:191], v128 offset:53264
	ds_read_b128 v[192:195], v127 offset:55312
	ds_read_b128 v[196:199], v128 offset:55312
	s_waitcnt lgkmcnt(0)
	s_waitcnt vmcnt(0)
	s_barrier
	s_setprio 1
	s_cmp_ge_u32 s77, 14
	s_cbranch_scc1 .Lkl_m1pre_y_nd1
	s_lshl_b32 s72, s77, 7
	s_addk_i32 s72, 0x180
	s_add_i32 s73, s72, 0x20000
	s_add_i32 s74, s72, 0x2000
	s_add_i32 s75, s72, 0x22000
	v_mfma_scale_f32_16x16x128_f8f6f4 v[140:143], v[200:207], v[72:79], v[140:143], v81, v80 op_sel_hi:[0,0,0]
	v_mfma_scale_f32_16x16x128_f8f6f4 v[136:139], v[208:215], v[72:79], v[136:139], v81, v80 op_sel_hi:[0,0,0]
	v_mfma_scale_f32_16x16x128_f8f6f4 v[108:111], v[200:207], v[144:151], v[108:111], v81, v80 op_sel_hi:[0,0,0]
	s_mov_b32 m0, s39
	s_nop 0
	buffer_load_dwordx4 v126, s[4:7], s72 offen lds
	v_mfma_scale_f32_16x16x128_f8f6f4 v[104:107], v[208:215], v[144:151], v[104:107], v81, v80 op_sel_hi:[0,0,0]
	v_mfma_scale_f32_16x16x128_f8f6f4 v[92:95], v[200:207], v[152:159], v[92:95], v81, v80 op_sel_hi:[0,0,0]
	v_mfma_scale_f32_16x16x128_f8f6f4 v[88:91], v[208:215], v[152:159], v[88:91], v81, v80 op_sel_hi:[0,0,0]
	s_mov_b32 m0, s60
	s_nop 0
	buffer_load_dwordx4 v120, s[8:11], s72 offen lds
	v_mfma_scale_f32_16x16x128_f8f6f4 v[220:223], v[200:207], v[160:167], v[220:223], v81, v80 op_sel_hi:[0,0,0]
	v_mfma_scale_f32_16x16x128_f8f6f4 v[224:227], v[208:215], v[160:167], v[224:227], v81, v80 op_sel_hi:[0,0,0]
	v_mfma_scale_f32_16x16x128_f8f6f4 v[116:119], v[228:235], v[72:79], v[116:119], v81, v80 op_sel_hi:[0,0,0]
	s_mov_b32 m0, s69
	s_nop 0
	buffer_load_dwordx4 v126, s[4:7], s73 offen lds
	v_mfma_scale_f32_16x16x128_f8f6f4 v[112:115], v[236:243], v[72:79], v[112:115], v81, v80 op_sel_hi:[0,0,0]
	v_mfma_scale_f32_16x16x128_f8f6f4 v[100:103], v[228:235], v[144:151], v[100:103], v81, v80 op_sel_hi:[0,0,0]
	v_mfma_scale_f32_16x16x128_f8f6f4 v[96:99], v[236:243], v[144:151], v[96:99], v81, v80 op_sel_hi:[0,0,0]
	s_mov_b32 m0, s70
	s_nop 0
	buffer_load_dwordx4 v121, s[8:11], s72 offen lds
	v_mfma_scale_f32_16x16x128_f8f6f4 v[84:87], v[228:235], v[152:159], v[84:87], v81, v80 op_sel_hi:[0,0,0]
	v_mfma_scale_f32_16x16x128_f8f6f4 v[8:11], v[236:243], v[152:159], v[8:11], v81, v80 op_sel_hi:[0,0,0]
	v_mfma_scale_f32_16x16x128_f8f6f4 v[68:71], v[228:235], v[160:167], v[68:71], v81, v80 op_sel_hi:[0,0,0]
	s_mov_b32 m0, s61
	s_nop 0
	buffer_load_dwordx4 v126, s[4:7], s74 offen lds
	v_mfma_scale_f32_16x16x128_f8f6f4 v[56:59], v[236:243], v[160:167], v[56:59], v81, v80 op_sel_hi:[0,0,0]
	v_mfma_scale_f32_16x16x128_f8f6f4 v[64:67], v[200:207], v[168:175], v[64:67], v81, v80 op_sel_hi:[0,0,0]
	v_mfma_scale_f32_16x16x128_f8f6f4 v[60:63], v[208:215], v[168:175], v[60:63], v81, v80 op_sel_hi:[0,0,0]
	s_mov_b32 m0, s26
	s_nop 0
	buffer_load_dwordx4 v122, s[8:11], s72 offen lds
	v_mfma_scale_f32_16x16x128_f8f6f4 v[44:47], v[200:207], v[176:183], v[44:47], v81, v80 op_sel_hi:[0,0,0]
	v_mfma_scale_f32_16x16x128_f8f6f4 v[40:43], v[208:215], v[176:183], v[40:43], v81, v80 op_sel_hi:[0,0,0]
	v_mfma_scale_f32_16x16x128_f8f6f4 v[28:31], v[200:207], v[184:191], v[28:31], v81, v80 op_sel_hi:[0,0,0]
	s_mov_b32 m0, s71
	s_nop 0
	buffer_load_dwordx4 v126, s[4:7], s75 offen lds
	v_mfma_scale_f32_16x16x128_f8f6f4 v[24:27], v[208:215], v[184:191], v[24:27], v81, v80 op_sel_hi:[0,0,0]
	v_mfma_scale_f32_16x16x128_f8f6f4 v[12:15], v[200:207], v[192:199], v[12:15], v81, v80 op_sel_hi:[0,0,0]
	v_mfma_scale_f32_16x16x128_f8f6f4 v[244:247], v[208:215], v[192:199], v[244:247], v81, v80 op_sel_hi:[0,0,0]
	s_mov_b32 m0, s62
	s_nop 0
	buffer_load_dwordx4 v123, s[8:11], s72 offen lds
	v_mfma_scale_f32_16x16x128_f8f6f4 v[52:55], v[228:235], v[168:175], v[52:55], v81, v80 op_sel_hi:[0,0,0]
	v_mfma_scale_f32_16x16x128_f8f6f4 v[48:51], v[236:243], v[168:175], v[48:51], v81, v80 op_sel_hi:[0,0,0]
	v_mfma_scale_f32_16x16x128_f8f6f4 v[36:39], v[228:235], v[176:183], v[36:39], v81, v80 op_sel_hi:[0,0,0]
	v_mfma_scale_f32_16x16x128_f8f6f4 v[32:35], v[236:243], v[176:183], v[32:35], v81, v80 op_sel_hi:[0,0,0]
	v_mfma_scale_f32_16x16x128_f8f6f4 v[20:23], v[228:235], v[184:191], v[20:23], v81, v80 op_sel_hi:[0,0,0]
	v_mfma_scale_f32_16x16x128_f8f6f4 v[16:19], v[236:243], v[184:191], v[16:19], v81, v80 op_sel_hi:[0,0,0]
	v_mfma_scale_f32_16x16x128_f8f6f4 v[4:7], v[228:235], v[192:199], v[4:7], v81, v80 op_sel_hi:[0,0,0]
	v_mfma_scale_f32_16x16x128_f8f6f4 v[0:3], v[236:243], v[192:199], v[0:3], v81, v80 op_sel_hi:[0,0,0]
	s_branch .Lkl_m1pre_y_nd1_j

; #define G_WAIT_V(n) asm volatile("s_waitcnt vmcnt(" #n ")" ::: "memory")
; #define G_BAR() __builtin_amdgcn_s_barrier()
; #define G_SCHED() __builtin_amdgcn_sched_barrier(0)
; #define D_MMA(ai, bj, At, Bf) do { __builtin_amdgcn_s_setprio(1); _Pragma("unroll") for (int m = 0; m < 4; ++m) _Pragma("unroll") for (int n = 0; n < 2; ++n) _Pragma("unroll") for (int k = 0; k < 2; ++k) \
;     acc[ai][bj][m][n] = __builtin_amdgcn_mfma_f32_16x16x32_bf16(Bf[n][k], At[m][k], acc[ai][bj][m][n], 0, 0, 0); __builtin_amdgcn_s_setprio(0); } while (0)
; #define D_MMA(ai, bj, At, Bf) do { if ((ai) && TOPHALF) break; __builtin_amdgcn_s_setprio(1); _Pragma("unroll") for (int m = 0; m < 4; ++m) _Pragma("unroll") for (int n = 0; n < 2; ++n) \
;     acc[ai][bj][m][n] = __builtin_amdgcn_mfma_scale_f32_16x16x128_f8f6f4(Bf[n], At[m], acc[ai][bj][m][n], 0, 0, 0, scw, 0, scx); __builtin_amdgcn_s_setprio(0); } while (0)
;     ...
;     G_WAIT_V(6); G_BAR(); G_SCHED(); D_MMA(1, 1, At, B1); G_BAR(); G_SCHED();
;   }
.Lkl_m1pre_y_nd1_j:
	s_setprio 0
	s_barrier
	s_add_i32 s77, s77, 2
	s_cmp_lt_u32 s77, 16
	s_cbranch_scc1 .Lkl_m1pre_yl

; #define G_WAIT_V(n) asm volatile("s_waitcnt vmcnt(" #n ")" ::: "memory")
; #define G_BAR() __builtin_amdgcn_s_barrier()
; #define G_SCHED() __builtin_amdgcn_sched_barrier(0)
; #define D_STAGE_A(slot, half, kt) D_STAGE(rsA, voffA, slot, half, kt)
; #define D_STAGE_B(slot, half, kt) D_STAGE(rsB, voffB, slot, half, kt)
; #define D_LDA(dst, slot) do { _Pragma("unroll") for (int m = 0; m < 4; ++m) _Pragma("unroll") for (int k = 0; k < 2; ++k) \
;     dst[m][k] = *(const LDS_AS bf16x8*)(lds + (slot) + aoff + m * 2048 + k * 1024); } while (0)
; #define D_LDB(dst, slot) do { _Pragma("unroll") for (int n = 0; n < 2; ++n) _Pragma("unroll") for (int k = 0; k < 2; ++k) \
;     dst[n][k] = *(const LDS_AS bf16x8*)(lds + (slot) + boff + n * 2048 + k * 1024); } while (0)
; #define D_MMA(ai, bj, At, Bf) do { __builtin_amdgcn_s_setprio(1); _Pragma("unroll") for (int m = 0; m < 4; ++m) _Pragma("unroll") for (int n = 0; n < 2; ++n) _Pragma("unroll") for (int k = 0; k < 2; ++k) \
;     acc[ai][bj][m][n] = __builtin_amdgcn_mfma_f32_16x16x32_bf16(Bf[n][k], At[m][k], acc[ai][bj][m][n], 0, 0, 0); __builtin_amdgcn_s_setprio(0); } while (0)
; #define D_WAIT_L(n) asm volatile("s_waitcnt lgkmcnt(" #n ")" ::: "memory")
; #define D_STAGE_A(slot, half, kt) D_STAGE(rsA, voffA, slot, half, kt)
; #define D_WAIT_L(n) asm volatile("s_waitcnt lgkmcnt(" #n ")" ::: "memory")
;     ...
;   const int scw = cfg.scale_w(), scx = cfg.scale_x();
;     ...
; #pragma clang loop unroll(disable)
;   for (int t = 0; t < (F8_PEEL ? nt - 2 : nt); t += 2) {
;     const int t1 = t + 1;
;     const int t2 = (F8_PEEL || t + 2 < nt) ? t + 2 : t;
;     const int t3 = (F8_PEEL || t + 2 < nt) ? t + 3 : t + 1;
;     D_LDB(B0, G_SB(0, 0)); G_SCHED(); D_LDA(At, G_SA(0, 0)); D_STAGE_A(G_SA(1, 1), 1, t1);
;     D_WAIT_L(8); G_BAR(); D_WAIT_L(0); G_SCHED(); D_MMA(0, 0, At, B0); G_BAR(); G_SCHED();
;     D_LDB(B1, G_SB(0, 1)); D_STAGE_B(G_SB(0, 0), 0, t2);
;     G_BAR(); D_WAIT_L(0); G_SCHED(); D_MMA(0, 1, At, B1); G_BAR(); G_SCHED();
;     D_LDA(At, G_SA(0, 1)); D_STAGE_A(G_SA(0, 0), 0, t2);
;     G_BAR(); D_WAIT_L(0); G_SCHED(); D_MMA(1, 0, At, B0); G_BAR(); G_SCHED();
;     D_STAGE_B(G_SB(0, 1), 1, t2);
;     G_WAIT_V(6); G_BAR(); G_SCHED(); D_MMA(1, 1, At, B1); G_BAR(); G_SCHED();
.LBB0_1606:
	s_mov_b32 s73, 0x10010
	v_add_u32_e32 v214, s73, v133
	v_add_u32_e32 v215, s73, v134
	s_mov_b32 s73, 0x14010
	v_add_u32_e32 v220, s73, v133
	v_add_u32_e32 v221, s73, v134
	s_mov_b32 s73, 0x18010
	v_add_u32_e32 v222, s73, v133
	v_add_u32_e32 v223, s73, v134
	s_mov_b32 s73, 0x1c010
	v_add_u32_e32 v244, s73, v133
	v_add_u32_e32 v245, s73, v134
	s_movk_i32 s69, 0x80
	s_mov_b32 m0, s67
	s_nop 0
	buffer_load_dwordx4 v129, s[8:11], s69 offen lds
	s_mov_b32 m0, s68
	s_nop 0
	buffer_load_dwordx4 v132, s[8:11], s69 offen lds
	s_cmpk_lt_u32 s13, 0x100
	s_cbranch_scc0 .Lkl_m2npre_y
	s_mov_b32 s74, 0
.Lkl_m2npre_x:
	ds_read_b128 v[198:201], v214
	ds_read_b128 v[202:205], v215
	ds_read_b128 v[206:209], v214 offset:2048
	ds_read_b128 v[210:213], v215 offset:2048
	ds_read_b128 v[228:231], v220
	ds_read_b128 v[232:235], v221
	ds_read_b128 v[236:239], v220 offset:2048
	ds_read_b128 v[240:243], v221 offset:2048
	ds_read_b128 v[68:71], v135 offset:16
	ds_read_b128 v[72:75], v136 offset:16
	ds_read_b128 v[138:141], v135 offset:2064
	ds_read_b128 v[142:145], v136 offset:2064
	ds_read_b128 v[146:149], v135 offset:4112
	ds_read_b128 v[150:153], v136 offset:4112
	ds_read_b128 v[154:157], v135 offset:6160
	ds_read_b128 v[158:161], v136 offset:6160
	ds_read_b128 v[166:169], v135 offset:16400
	ds_read_b128 v[170:173], v136 offset:16400
	ds_read_b128 v[174:177], v135 offset:18448
	ds_read_b128 v[178:181], v136 offset:18448
	ds_read_b128 v[182:185], v135 offset:20496
	ds_read_b128 v[186:189], v136 offset:20496
	ds_read_b128 v[190:193], v135 offset:22544
	ds_read_b128 v[194:197], v136 offset:22544
	s_cmp_eq_u32 s74, 0
	s_cbranch_scc1 .Lkl_m2npre_x_nd0
	s_lshl_b32 s69, s74, 7
	s_addk_i32 s69, 0x80
	s_add_i32 s70, s69, 0x20000
	s_add_i32 s71, s69, 0x40000
	s_add_i32 s72, s69, 0x60000
	s_mov_b32 m0, s61
	s_nop 0
	buffer_load_dwordx4 v130, s[4:7], s69 offen lds
	s_mov_b32 m0, s63
	s_nop 0
	buffer_load_dwordx4 v128, s[8:11], s69 offen lds
	s_mov_b32 m0, s62
	s_nop 0
	buffer_load_dwordx4 v130, s[4:7], s70 offen lds
	s_mov_b32 m0, s64
	s_nop 0
	buffer_load_dwordx4 v131, s[8:11], s69 offen lds
	s_mov_b32 m0, s65
	s_nop 0
	buffer_load_dwordx4 v130, s[4:7], s71 offen lds
	s_mov_b32 m0, s67
	s_nop 0
	buffer_load_dwordx4 v129, s[8:11], s69 offen lds
	s_mov_b32 m0, s66
	s_nop 0
	buffer_load_dwordx4 v130, s[4:7], s72 offen lds
	s_mov_b32 m0, s68
	s_nop 0
	buffer_load_dwordx4 v132, s[8:11], s69 offen lds
.Lkl_m2npre_x_nd0:
	s_waitcnt lgkmcnt(0)
	s_barrier
	s_setprio 1
	v_mfma_scale_f32_16x16x128_f8f6f4 v[124:127], v[198:205], v[68:75], v[124:127], v165, v164 op_sel_hi:[0,0,0]
	v_mfma_scale_f32_16x16x128_f8f6f4 v[120:123], v[206:213], v[68:75], v[120:123], v165, v164 op_sel_hi:[0,0,0]
	v_mfma_scale_f32_16x16x128_f8f6f4 v[108:111], v[198:205], v[138:145], v[108:111], v165, v164 op_sel_hi:[0,0,0]
	v_mfma_scale_f32_16x16x128_f8f6f4 v[100:103], v[206:213], v[138:145], v[100:103], v165, v164 op_sel_hi:[0,0,0]
	v_mfma_scale_f32_16x16x128_f8f6f4 v[84:87], v[198:205], v[146:153], v[84:87], v165, v164 op_sel_hi:[0,0,0]
	v_mfma_scale_f32_16x16x128_f8f6f4 v[80:83], v[206:213], v[146:153], v[80:83], v165, v164 op_sel_hi:[0,0,0]
	v_mfma_scale_f32_16x16x128_f8f6f4 v[216:219], v[198:205], v[154:161], v[216:219], v165, v164 op_sel_hi:[0,0,0]
	v_mfma_scale_f32_16x16x128_f8f6f4 v[48:51], v[206:213], v[154:161], v[48:51], v165, v164 op_sel_hi:[0,0,0]
	v_mfma_scale_f32_16x16x128_f8f6f4 v[116:119], v[228:235], v[68:75], v[116:119], v165, v164 op_sel_hi:[0,0,0]
	v_mfma_scale_f32_16x16x128_f8f6f4 v[112:115], v[236:243], v[68:75], v[112:115], v165, v164 op_sel_hi:[0,0,0]
	v_mfma_scale_f32_16x16x128_f8f6f4 v[104:107], v[228:235], v[138:145], v[104:107], v165, v164 op_sel_hi:[0,0,0]
	v_mfma_scale_f32_16x16x128_f8f6f4 v[96:99], v[236:243], v[138:145], v[96:99], v165, v164 op_sel_hi:[0,0,0]
	v_mfma_scale_f32_16x16x128_f8f6f4 v[92:95], v[228:235], v[146:153], v[92:95], v165, v164 op_sel_hi:[0,0,0]
	v_mfma_scale_f32_16x16x128_f8f6f4 v[88:91], v[236:243], v[146:153], v[88:91], v165, v164 op_sel_hi:[0,0,0]
	v_mfma_scale_f32_16x16x128_f8f6f4 v[76:79], v[228:235], v[154:161], v[76:79], v165, v164 op_sel_hi:[0,0,0]
	v_mfma_scale_f32_16x16x128_f8f6f4 v[16:19], v[236:243], v[154:161], v[16:19], v165, v164 op_sel_hi:[0,0,0]
	v_mfma_scale_f32_16x16x128_f8f6f4 v[56:59], v[198:205], v[166:173], v[56:59], v165, v164 op_sel_hi:[0,0,0]
	v_mfma_scale_f32_16x16x128_f8f6f4 v[52:55], v[206:213], v[166:173], v[52:55], v165, v164 op_sel_hi:[0,0,0]
	v_mfma_scale_f32_16x16x128_f8f6f4 v[36:39], v[198:205], v[174:181], v[36:39], v165, v164 op_sel_hi:[0,0,0]
	v_mfma_scale_f32_16x16x128_f8f6f4 v[32:35], v[206:213], v[174:181], v[32:35], v165, v164 op_sel_hi:[0,0,0]
	v_mfma_scale_f32_16x16x128_f8f6f4 v[20:23], v[198:205], v[182:189], v[20:23], v165, v164 op_sel_hi:[0,0,0]
	v_mfma_scale_f32_16x16x128_f8f6f4 v[224:227], v[206:213], v[182:189], v[224:227], v165, v164 op_sel_hi:[0,0,0]
	v_mfma_scale_f32_16x16x128_f8f6f4 v[4:7], v[198:205], v[190:197], v[4:7], v165, v164 op_sel_hi:[0,0,0]
	v_mfma_scale_f32_16x16x128_f8f6f4 v[0:3], v[206:213], v[190:197], v[0:3], v165, v164 op_sel_hi:[0,0,0]
	v_mfma_scale_f32_16x16x128_f8f6f4 v[64:67], v[228:235], v[166:173], v[64:67], v165, v164 op_sel_hi:[0,0,0]
	v_mfma_scale_f32_16x16x128_f8f6f4 v[60:63], v[236:243], v[166:173], v[60:63], v165, v164 op_sel_hi:[0,0,0]
	v_mfma_scale_f32_16x16x128_f8f6f4 v[44:47], v[228:235], v[174:181], v[44:47], v165, v164 op_sel_hi:[0,0,0]
	v_mfma_scale_f32_16x16x128_f8f6f4 v[40:43], v[236:243], v[174:181], v[40:43], v165, v164 op_sel_hi:[0,0,0]
	v_mfma_scale_f32_16x16x128_f8f6f4 v[28:31], v[228:235], v[182:189], v[28:31], v165, v164 op_sel_hi:[0,0,0]
	v_mfma_scale_f32_16x16x128_f8f6f4 v[24:27], v[236:243], v[182:189], v[24:27], v165, v164 op_sel_hi:[0,0,0]
	v_mfma_scale_f32_16x16x128_f8f6f4 v[12:15], v[228:235], v[190:197], v[12:15], v165, v164 op_sel_hi:[0,0,0]
	v_mfma_scale_f32_16x16x128_f8f6f4 v[8:11], v[236:243], v[190:197], v[8:11], v165, v164 op_sel_hi:[0,0,0]
	s_setprio 0
	s_waitcnt vmcnt(0)
	s_barrier
; #define G_WAIT_V(n) asm volatile("s_waitcnt vmcnt(" #n ")" ::: "memory")
; #define G_BAR() __builtin_amdgcn_s_barrier()
; #define G_SCHED() __builtin_amdgcn_sched_barrier(0)
; #define D_STAGE_A(slot, half, kt) D_STAGE(rsA, voffA, slot, half, kt)
; #define D_STAGE_B(slot, half, kt) D_STAGE(rsB, voffB, slot, half, kt)
; #define D_LDA(dst, slot) do { _Pragma("unroll") for (int m = 0; m < 4; ++m) _Pragma("unroll") for (int k = 0; k < 2; ++k) \
;     dst[m][k] = *(const LDS_AS bf16x8*)(lds + (slot) + aoff + m * 2048 + k * 1024); } while (0)
; #define D_LDB(dst, slot) do { _Pragma("unroll") for (int n = 0; n < 2; ++n) _Pragma("unroll") for (int k = 0; k < 2; ++k) \
;     dst[n][k] = *(const LDS_AS bf16x8*)(lds + (slot) + boff + n * 2048 + k * 1024); } while (0)
; #define D_MMA(ai, bj, At, Bf) do { __builtin_amdgcn_s_setprio(1); _Pragma("unroll") for (int m = 0; m < 4; ++m) _Pragma("unroll") for (int n = 0; n < 2; ++n) _Pragma("unroll") for (int k = 0; k < 2; ++k) \
;     acc[ai][bj][m][n] = __builtin_amdgcn_mfma_f32_16x16x32_bf16(Bf[n][k], At[m][k], acc[ai][bj][m][n], 0, 0, 0); __builtin_amdgcn_s_setprio(0); } while (0)
; #define D_WAIT_L(n) asm volatile("s_waitcnt lgkmcnt(" #n ")" ::: "memory")
;     ...
;     D_LDB(B0, G_SB(0, 0)); G_SCHED(); D_LDA(At, G_SA(0, 0)); D_STAGE_A(G_SA(1, 1), 1, t1);
;     D_WAIT_L(8); G_BAR(); D_WAIT_L(0); G_SCHED(); D_MMA(0, 0, At, B0); G_BAR(); G_SCHED();
;     D_LDB(B1, G_SB(0, 1)); D_STAGE_B(G_SB(0, 0), 0, t2);
;     G_BAR(); D_WAIT_L(0); G_SCHED(); D_MMA(0, 1, At, B1); G_BAR(); G_SCHED();
;     D_LDA(At, G_SA(0, 1)); D_STAGE_A(G_SA(0, 0), 0, t2);
;     G_BAR(); D_WAIT_L(0); G_SCHED(); D_MMA(1, 0, At, B0); G_BAR(); G_SCHED();
;     D_STAGE_B(G_SB(0, 1), 1, t2);
;     G_WAIT_V(6); G_BAR(); G_SCHED(); D_MMA(1, 1, At, B1); G_BAR(); G_SCHED();
;     D_LDB(B0, G_SB(1, 0)); G_SCHED(); D_LDA(At, G_SA(1, 0)); D_STAGE_A(G_SA(0, 1), 1, t2);
;     D_WAIT_L(8); G_BAR(); D_WAIT_L(0); G_SCHED(); D_MMA(0, 0, At, B0); G_BAR(); G_SCHED();
;     D_LDB(B1, G_SB(1, 1)); D_STAGE_B(G_SB(1, 0), 0, t3);
;     G_BAR(); D_WAIT_L(0); G_SCHED(); D_MMA(0, 1, At, B1); G_BAR(); G_SCHED();
;     D_LDA(At, G_SA(1, 1)); D_STAGE_A(G_SA(1, 0), 0, t3);
;     G_BAR(); D_WAIT_L(0); G_SCHED(); D_MMA(1, 0, At, B0); G_BAR(); G_SCHED();
;     D_STAGE_B(G_SB(1, 1), 1, t3);
;     G_WAIT_V(6); G_BAR(); G_SCHED(); D_MMA(1, 1, At, B1); G_BAR(); G_SCHED();
;   }
	ds_read_b128 v[198:201], v222
	ds_read_b128 v[202:205], v223
	ds_read_b128 v[206:209], v222 offset:2048
	ds_read_b128 v[210:213], v223 offset:2048
	ds_read_b128 v[228:231], v244
	ds_read_b128 v[232:235], v245
	ds_read_b128 v[236:239], v244 offset:2048
	ds_read_b128 v[240:243], v245 offset:2048
	ds_read_b128 v[68:71], v135 offset:32784
	ds_read_b128 v[72:75], v136 offset:32784
	ds_read_b128 v[138:141], v135 offset:34832
	ds_read_b128 v[142:145], v136 offset:34832
	ds_read_b128 v[146:149], v135 offset:36880
	ds_read_b128 v[150:153], v136 offset:36880
	ds_read_b128 v[154:157], v135 offset:38928
	ds_read_b128 v[158:161], v136 offset:38928
	ds_read_b128 v[166:169], v135 offset:49168
	ds_read_b128 v[170:173], v136 offset:49168
	ds_read_b128 v[174:177], v135 offset:51216
	ds_read_b128 v[178:181], v136 offset:51216
	ds_read_b128 v[182:185], v135 offset:53264
	ds_read_b128 v[186:189], v136 offset:53264
	ds_read_b128 v[190:193], v135 offset:55312
	ds_read_b128 v[194:197], v136 offset:55312
	s_cmp_ge_u32 s74, 14
	s_cbranch_scc1 .Lkl_m2npre_x_nd1
	s_lshl_b32 s69, s74, 7
	s_addk_i32 s69, 0x100
	s_add_i32 s70, s69, 0x20000
	s_add_i32 s71, s69, 0x40000
	s_add_i32 s72, s69, 0x60000
	s_mov_b32 m0, s39
	s_nop 0
	buffer_load_dwordx4 v130, s[4:7], s69 offen lds
	s_mov_b32 m0, s51
	s_nop 0
	buffer_load_dwordx4 v128, s[8:11], s69 offen lds
	s_mov_b32 m0, s50
	s_nop 0
	buffer_load_dwordx4 v130, s[4:7], s70 offen lds
	s_mov_b32 m0, s54
	s_nop 0
	buffer_load_dwordx4 v131, s[8:11], s69 offen lds
	s_mov_b32 m0, s55
	s_nop 0
	buffer_load_dwordx4 v130, s[4:7], s71 offen lds
	s_mov_b32 m0, s59
	s_nop 0
	buffer_load_dwordx4 v129, s[8:11], s69 offen lds
	s_mov_b32 m0, s58
	s_nop 0
	buffer_load_dwordx4 v130, s[4:7], s72 offen lds
	s_mov_b32 m0, s60
	s_nop 0
	buffer_load_dwordx4 v132, s[8:11], s69 offen lds
.Lkl_m2npre_x_nd1:
	s_waitcnt lgkmcnt(0)
	s_barrier
	s_setprio 1
	v_mfma_scale_f32_16x16x128_f8f6f4 v[124:127], v[198:205], v[68:75], v[124:127], v165, v164 op_sel_hi:[0,0,0]
	v_mfma_scale_f32_16x16x128_f8f6f4 v[120:123], v[206:213], v[68:75], v[120:123], v165, v164 op_sel_hi:[0,0,0]
	v_mfma_scale_f32_16x16x128_f8f6f4 v[108:111], v[198:205], v[138:145], v[108:111], v165, v164 op_sel_hi:[0,0,0]
	v_mfma_scale_f32_16x16x128_f8f6f4 v[100:103], v[206:213], v[138:145], v[100:103], v165, v164 op_sel_hi:[0,0,0]
	v_mfma_scale_f32_16x16x128_f8f6f4 v[84:87], v[198:205], v[146:153], v[84:87], v165, v164 op_sel_hi:[0,0,0]
	v_mfma_scale_f32_16x16x128_f8f6f4 v[80:83], v[206:213], v[146:153], v[80:83], v165, v164 op_sel_hi:[0,0,0]
	v_mfma_scale_f32_16x16x128_f8f6f4 v[216:219], v[198:205], v[154:161], v[216:219], v165, v164 op_sel_hi:[0,0,0]
	v_mfma_scale_f32_16x16x128_f8f6f4 v[48:51], v[206:213], v[154:161], v[48:51], v165, v164 op_sel_hi:[0,0,0]
	v_mfma_scale_f32_16x16x128_f8f6f4 v[116:119], v[228:235], v[68:75], v[116:119], v165, v164 op_sel_hi:[0,0,0]
	v_mfma_scale_f32_16x16x128_f8f6f4 v[112:115], v[236:243], v[68:75], v[112:115], v165, v164 op_sel_hi:[0,0,0]
	v_mfma_scale_f32_16x16x128_f8f6f4 v[104:107], v[228:235], v[138:145], v[104:107], v165, v164 op_sel_hi:[0,0,0]
	v_mfma_scale_f32_16x16x128_f8f6f4 v[96:99], v[236:243], v[138:145], v[96:99], v165, v164 op_sel_hi:[0,0,0]
	v_mfma_scale_f32_16x16x128_f8f6f4 v[92:95], v[228:235], v[146:153], v[92:95], v165, v164 op_sel_hi:[0,0,0]
	v_mfma_scale_f32_16x16x128_f8f6f4 v[88:91], v[236:243], v[146:153], v[88:91], v165, v164 op_sel_hi:[0,0,0]
	v_mfma_scale_f32_16x16x128_f8f6f4 v[76:79], v[228:235], v[154:161], v[76:79], v165, v164 op_sel_hi:[0,0,0]
	v_mfma_scale_f32_16x16x128_f8f6f4 v[16:19], v[236:243], v[154:161], v[16:19], v165, v164 op_sel_hi:[0,0,0]
	v_mfma_scale_f32_16x16x128_f8f6f4 v[56:59], v[198:205], v[166:173], v[56:59], v165, v164 op_sel_hi:[0,0,0]
	v_mfma_scale_f32_16x16x128_f8f6f4 v[52:55], v[206:213], v[166:173], v[52:55], v165, v164 op_sel_hi:[0,0,0]
	v_mfma_scale_f32_16x16x128_f8f6f4 v[36:39], v[198:205], v[174:181], v[36:39], v165, v164 op_sel_hi:[0,0,0]
	v_mfma_scale_f32_16x16x128_f8f6f4 v[32:35], v[206:213], v[174:181], v[32:35], v165, v164 op_sel_hi:[0,0,0]
	v_mfma_scale_f32_16x16x128_f8f6f4 v[20:23], v[198:205], v[182:189], v[20:23], v165, v164 op_sel_hi:[0,0,0]
	v_mfma_scale_f32_16x16x128_f8f6f4 v[224:227], v[206:213], v[182:189], v[224:227], v165, v164 op_sel_hi:[0,0,0]
	v_mfma_scale_f32_16x16x128_f8f6f4 v[4:7], v[198:205], v[190:197], v[4:7], v165, v164 op_sel_hi:[0,0,0]
	v_mfma_scale_f32_16x16x128_f8f6f4 v[0:3], v[206:213], v[190:197], v[0:3], v165, v164 op_sel_hi:[0,0,0]
	v_mfma_scale_f32_16x16x128_f8f6f4 v[64:67], v[228:235], v[166:173], v[64:67], v165, v164 op_sel_hi:[0,0,0]
	v_mfma_scale_f32_16x16x128_f8f6f4 v[60:63], v[236:243], v[166:173], v[60:63], v165, v164 op_sel_hi:[0,0,0]
	v_mfma_scale_f32_16x16x128_f8f6f4 v[44:47], v[228:235], v[174:181], v[44:47], v165, v164 op_sel_hi:[0,0,0]
	v_mfma_scale_f32_16x16x128_f8f6f4 v[40:43], v[236:243], v[174:181], v[40:43], v165, v164 op_sel_hi:[0,0,0]
	v_mfma_scale_f32_16x16x128_f8f6f4 v[28:31], v[228:235], v[182:189], v[28:31], v165, v164 op_sel_hi:[0,0,0]
	v_mfma_scale_f32_16x16x128_f8f6f4 v[24:27], v[236:243], v[182:189], v[24:27], v165, v164 op_sel_hi:[0,0,0]
	v_mfma_scale_f32_16x16x128_f8f6f4 v[12:15], v[228:235], v[190:197], v[12:15], v165, v164 op_sel_hi:[0,0,0]
	v_mfma_scale_f32_16x16x128_f8f6f4 v[8:11], v[236:243], v[190:197], v[8:11], v165, v164 op_sel_hi:[0,0,0]
	s_setprio 0
	s_waitcnt vmcnt(0)
	s_barrier
	s_add_i32 s74, s74, 2
	s_cmp_lt_u32 s74, 16
	s_cbranch_scc1 .Lkl_m2npre_x
	s_branch .Lkl_m2npre_end
.Lkl_m2npre_y:
	s_mov_b32 s74, 0
; #define G_WAIT_V(n) asm volatile("s_waitcnt vmcnt(" #n ")" ::: "memory")
; #define G_BAR() __builtin_amdgcn_s_barrier()
; #define G_SCHED() __builtin_amdgcn_sched_barrier(0)
; #define D_STAGE_A(slot, half, kt) D_STAGE(rsA, voffA, slot, half, kt)
; #define D_STAGE_B(slot, half, kt) D_STAGE(rsB, voffB, slot, half, kt)
; #define D_LDA(dst, slot) do { _Pragma("unroll") for (int m = 0; m < 4; ++m) _Pragma("unroll") for (int k = 0; k < 2; ++k) \
;     dst[m][k] = *(const LDS_AS bf16x8*)(lds + (slot) + aoff + m * 2048 + k * 1024); } while (0)
; #define D_LDB(dst, slot) do { _Pragma("unroll") for (int n = 0; n < 2; ++n) _Pragma("unroll") for (int k = 0; k < 2; ++k) \
;     dst[n][k] = *(const LDS_AS bf16x8*)(lds + (slot) + boff + n * 2048 + k * 1024); } while (0)
; #define D_MMA(ai, bj, At, Bf) do { __builtin_amdgcn_s_setprio(1); _Pragma("unroll") for (int m = 0; m < 4; ++m) _Pragma("unroll") for (int n = 0; n < 2; ++n) _Pragma("unroll") for (int k = 0; k < 2; ++k) \
;     acc[ai][bj][m][n] = __builtin_amdgcn_mfma_f32_16x16x32_bf16(Bf[n][k], At[m][k], acc[ai][bj][m][n], 0, 0, 0); __builtin_amdgcn_s_setprio(0); } while (0)
; #define D_WAIT_L(n) asm volatile("s_waitcnt lgkmcnt(" #n ")" ::: "memory")
; #define D_STAGE_A(slot, half, kt) D_STAGE(rsA, voffA, slot, half, kt)
; #define D_STAGE_B(slot, half, kt) do { _Pragma("unroll") for (int _i = 0; _i < 2; ++_i) { const unsigned _m0 = ldsw + (unsigned)((slot) + _i * 8192); const unsigned _so = (unsigned)(kt) * 128u + (half) * bt_half + _i * bt_piece; \
;     asm volatile("s_mov_b32 m0, %0\n\ts_nop 4\n\tbuffer_load_dwordx4 %1, %2, %3 offen lds" :: "s"(_m0), "v"(voffB0), "s"(rsB), "s"(_so) : "m0", "memory"); } } while (0)
; #define D_WAIT_L(n) asm volatile("s_waitcnt lgkmcnt(" #n ")" ::: "memory")
;     ...
;     D_LDB(B0, G_SB(0, 0)); G_SCHED(); D_LDA(At, G_SA(0, 0)); D_STAGE_A(G_SA(1, 1), 1, t1);
;     D_WAIT_L(8); G_BAR(); D_WAIT_L(0); G_SCHED(); D_MMA(0, 0, At, B0); G_BAR(); G_SCHED();
;     D_LDB(B1, G_SB(0, 1)); D_STAGE_B(G_SB(0, 0), 0, t2);
;     G_BAR(); D_WAIT_L(0); G_SCHED(); D_MMA(0, 1, At, B1); G_BAR(); G_SCHED();
;     D_LDA(At, G_SA(0, 1)); D_STAGE_A(G_SA(0, 0), 0, t2);
;     G_BAR(); D_WAIT_L(0); G_SCHED(); D_MMA(1, 0, At, B0); G_BAR(); G_SCHED();
;     D_STAGE_B(G_SB(0, 1), 1, t2);
;     G_WAIT_V(6); G_BAR(); G_SCHED(); D_MMA(1, 1, At, B1); G_BAR(); G_SCHED();
.Lkl_m2npre_yl:
	ds_read_b128 v[198:201], v214
	ds_read_b128 v[202:205], v215
	ds_read_b128 v[206:209], v214 offset:2048
	ds_read_b128 v[210:213], v215 offset:2048
	ds_read_b128 v[228:231], v220
	ds_read_b128 v[232:235], v221
	ds_read_b128 v[236:239], v220 offset:2048
	ds_read_b128 v[240:243], v221 offset:2048
	ds_read_b128 v[68:71], v135 offset:16
	ds_read_b128 v[72:75], v136 offset:16
	ds_read_b128 v[138:141], v135 offset:2064
	ds_read_b128 v[142:145], v136 offset:2064
	ds_read_b128 v[146:149], v135 offset:4112
	ds_read_b128 v[150:153], v136 offset:4112
	ds_read_b128 v[154:157], v135 offset:6160
	ds_read_b128 v[158:161], v136 offset:6160
	ds_read_b128 v[166:169], v135 offset:16400
	ds_read_b128 v[170:173], v136 offset:16400
	ds_read_b128 v[174:177], v135 offset:18448
	ds_read_b128 v[178:181], v136 offset:18448
	ds_read_b128 v[182:185], v135 offset:20496
	ds_read_b128 v[186:189], v136 offset:20496
	ds_read_b128 v[190:193], v135 offset:22544
	ds_read_b128 v[194:197], v136 offset:22544
	s_waitcnt lgkmcnt(0)
	s_waitcnt vmcnt(0)
	s_barrier
	s_setprio 1
	s_cmp_ge_u32 s74, 14
	s_cbranch_scc1 .Lkl_m2npre_y_nd0
	s_lshl_b32 s69, s74, 7
	s_addk_i32 s69, 0x100
	s_add_i32 s70, s69, 0x20000
	s_add_i32 s71, s69, 0x40000
	s_add_i32 s72, s69, 0x60000
	v_mfma_scale_f32_16x16x128_f8f6f4 v[124:127], v[198:205], v[68:75], v[124:127], v165, v164 op_sel_hi:[0,0,0]
	v_mfma_scale_f32_16x16x128_f8f6f4 v[120:123], v[206:213], v[68:75], v[120:123], v165, v164 op_sel_hi:[0,0,0]
	v_mfma_scale_f32_16x16x128_f8f6f4 v[108:111], v[198:205], v[138:145], v[108:111], v165, v164 op_sel_hi:[0,0,0]
	s_mov_b32 m0, s39
	s_nop 0
	buffer_load_dwordx4 v130, s[4:7], s69 offen lds
	v_mfma_scale_f32_16x16x128_f8f6f4 v[100:103], v[206:213], v[138:145], v[100:103], v165, v164 op_sel_hi:[0,0,0]
	v_mfma_scale_f32_16x16x128_f8f6f4 v[84:87], v[198:205], v[146:153], v[84:87], v165, v164 op_sel_hi:[0,0,0]
	v_mfma_scale_f32_16x16x128_f8f6f4 v[80:83], v[206:213], v[146:153], v[80:83], v165, v164 op_sel_hi:[0,0,0]
	s_mov_b32 m0, s51
	s_nop 0
	buffer_load_dwordx4 v128, s[8:11], s69 offen lds
	v_mfma_scale_f32_16x16x128_f8f6f4 v[216:219], v[198:205], v[154:161], v[216:219], v165, v164 op_sel_hi:[0,0,0]
	v_mfma_scale_f32_16x16x128_f8f6f4 v[48:51], v[206:213], v[154:161], v[48:51], v165, v164 op_sel_hi:[0,0,0]
	v_mfma_scale_f32_16x16x128_f8f6f4 v[116:119], v[228:235], v[68:75], v[116:119], v165, v164 op_sel_hi:[0,0,0]
	s_mov_b32 m0, s50
	s_nop 0
	buffer_load_dwordx4 v130, s[4:7], s70 offen lds
	v_mfma_scale_f32_16x16x128_f8f6f4 v[112:115], v[236:243], v[68:75], v[112:115], v165, v164 op_sel_hi:[0,0,0]
	v_mfma_scale_f32_16x16x128_f8f6f4 v[104:107], v[228:235], v[138:145], v[104:107], v165, v164 op_sel_hi:[0,0,0]
	v_mfma_scale_f32_16x16x128_f8f6f4 v[96:99], v[236:243], v[138:145], v[96:99], v165, v164 op_sel_hi:[0,0,0]
	s_mov_b32 m0, s54
	s_nop 0
	buffer_load_dwordx4 v131, s[8:11], s69 offen lds
	v_mfma_scale_f32_16x16x128_f8f6f4 v[92:95], v[228:235], v[146:153], v[92:95], v165, v164 op_sel_hi:[0,0,0]
	v_mfma_scale_f32_16x16x128_f8f6f4 v[88:91], v[236:243], v[146:153], v[88:91], v165, v164 op_sel_hi:[0,0,0]
	v_mfma_scale_f32_16x16x128_f8f6f4 v[76:79], v[228:235], v[154:161], v[76:79], v165, v164 op_sel_hi:[0,0,0]
	s_mov_b32 m0, s55
	s_nop 0
	buffer_load_dwordx4 v130, s[4:7], s71 offen lds
	v_mfma_scale_f32_16x16x128_f8f6f4 v[16:19], v[236:243], v[154:161], v[16:19], v165, v164 op_sel_hi:[0,0,0]
	v_mfma_scale_f32_16x16x128_f8f6f4 v[56:59], v[198:205], v[166:173], v[56:59], v165, v164 op_sel_hi:[0,0,0]
	v_mfma_scale_f32_16x16x128_f8f6f4 v[52:55], v[206:213], v[166:173], v[52:55], v165, v164 op_sel_hi:[0,0,0]
	s_mov_b32 m0, s59
	s_nop 0
	buffer_load_dwordx4 v129, s[8:11], s69 offen lds
	v_mfma_scale_f32_16x16x128_f8f6f4 v[36:39], v[198:205], v[174:181], v[36:39], v165, v164 op_sel_hi:[0,0,0]
	v_mfma_scale_f32_16x16x128_f8f6f4 v[32:35], v[206:213], v[174:181], v[32:35], v165, v164 op_sel_hi:[0,0,0]
	v_mfma_scale_f32_16x16x128_f8f6f4 v[20:23], v[198:205], v[182:189], v[20:23], v165, v164 op_sel_hi:[0,0,0]
	s_mov_b32 m0, s58
	s_nop 0
	buffer_load_dwordx4 v130, s[4:7], s72 offen lds
	v_mfma_scale_f32_16x16x128_f8f6f4 v[224:227], v[206:213], v[182:189], v[224:227], v165, v164 op_sel_hi:[0,0,0]
	v_mfma_scale_f32_16x16x128_f8f6f4 v[4:7], v[198:205], v[190:197], v[4:7], v165, v164 op_sel_hi:[0,0,0]
	v_mfma_scale_f32_16x16x128_f8f6f4 v[0:3], v[206:213], v[190:197], v[0:3], v165, v164 op_sel_hi:[0,0,0]
	s_mov_b32 m0, s60
	s_nop 0
	buffer_load_dwordx4 v132, s[8:11], s69 offen lds
	v_mfma_scale_f32_16x16x128_f8f6f4 v[64:67], v[228:235], v[166:173], v[64:67], v165, v164 op_sel_hi:[0,0,0]
	v_mfma_scale_f32_16x16x128_f8f6f4 v[60:63], v[236:243], v[166:173], v[60:63], v165, v164 op_sel_hi:[0,0,0]
	v_mfma_scale_f32_16x16x128_f8f6f4 v[44:47], v[228:235], v[174:181], v[44:47], v165, v164 op_sel_hi:[0,0,0]
	v_mfma_scale_f32_16x16x128_f8f6f4 v[40:43], v[236:243], v[174:181], v[40:43], v165, v164 op_sel_hi:[0,0,0]
	v_mfma_scale_f32_16x16x128_f8f6f4 v[28:31], v[228:235], v[182:189], v[28:31], v165, v164 op_sel_hi:[0,0,0]
	v_mfma_scale_f32_16x16x128_f8f6f4 v[24:27], v[236:243], v[182:189], v[24:27], v165, v164 op_sel_hi:[0,0,0]
	v_mfma_scale_f32_16x16x128_f8f6f4 v[12:15], v[228:235], v[190:197], v[12:15], v165, v164 op_sel_hi:[0,0,0]
	v_mfma_scale_f32_16x16x128_f8f6f4 v[8:11], v[236:243], v[190:197], v[8:11], v165, v164 op_sel_hi:[0,0,0]
	s_branch .Lkl_m2npre_y_nd0_j
; #define G_WAIT_V(n) asm volatile("s_waitcnt vmcnt(" #n ")" ::: "memory")
; #define G_BAR() __builtin_amdgcn_s_barrier()
; #define G_SCHED() __builtin_amdgcn_sched_barrier(0)
; #define D_STAGE_B(slot, half, kt) D_STAGE(rsB, voffB, slot, half, kt)
; #define D_MMA(ai, bj, At, Bf) do { __builtin_amdgcn_s_setprio(1); _Pragma("unroll") for (int m = 0; m < 4; ++m) _Pragma("unroll") for (int n = 0; n < 2; ++n) _Pragma("unroll") for (int k = 0; k < 2; ++k) \
;     acc[ai][bj][m][n] = __builtin_amdgcn_mfma_f32_16x16x32_bf16(Bf[n][k], At[m][k], acc[ai][bj][m][n], 0, 0, 0); __builtin_amdgcn_s_setprio(0); } while (0)
; #define D_WAIT_L(n) asm volatile("s_waitcnt lgkmcnt(" #n ")" ::: "memory")
; #define D_STAGE_B(slot, half, kt) do { _Pragma("unroll") for (int _i = 0; _i < 2; ++_i) { const unsigned _m0 = ldsw + (unsigned)((slot) + _i * 8192); const unsigned _so = (unsigned)(kt) * 128u + (half) * bt_half + _i * bt_piece; \
;     asm volatile("s_mov_b32 m0, %0\n\ts_nop 4\n\tbuffer_load_dwordx4 %1, %2, %3 offen lds" :: "s"(_m0), "v"(voffB0), "s"(rsB), "s"(_so) : "m0", "memory"); } } while (0)
; #define D_MMA(ai, bj, At, Bf) do { if ((ai) && TOPHALF) break; __builtin_amdgcn_s_setprio(1); _Pragma("unroll") for (int m = 0; m < 4; ++m) _Pragma("unroll") for (int n = 0; n < 2; ++n) \
;     acc[ai][bj][m][n] = __builtin_amdgcn_mfma_scale_f32_16x16x128_f8f6f4(Bf[n], At[m], acc[ai][bj][m][n], 0, 0, 0, scw, 0, scx); __builtin_amdgcn_s_setprio(0); } while (0)
; #define D_WAIT_L(n) asm volatile("s_waitcnt lgkmcnt(" #n ")" ::: "memory")
;     ...
;     G_BAR(); D_WAIT_L(0); G_SCHED(); D_MMA(1, 0, At, B0); G_BAR(); G_SCHED();
;     D_STAGE_B(G_SB(0, 1), 1, t2);
;     G_WAIT_V(6); G_BAR(); G_SCHED(); D_MMA(1, 1, At, B1); G_BAR(); G_SCHED();
.Lkl_m2npre_y_nd0:
	v_mfma_scale_f32_16x16x128_f8f6f4 v[124:127], v[198:205], v[68:75], v[124:127], v165, v164 op_sel_hi:[0,0,0]
	v_mfma_scale_f32_16x16x128_f8f6f4 v[120:123], v[206:213], v[68:75], v[120:123], v165, v164 op_sel_hi:[0,0,0]
	v_mfma_scale_f32_16x16x128_f8f6f4 v[108:111], v[198:205], v[138:145], v[108:111], v165, v164 op_sel_hi:[0,0,0]
	v_mfma_scale_f32_16x16x128_f8f6f4 v[100:103], v[206:213], v[138:145], v[100:103], v165, v164 op_sel_hi:[0,0,0]
	v_mfma_scale_f32_16x16x128_f8f6f4 v[84:87], v[198:205], v[146:153], v[84:87], v165, v164 op_sel_hi:[0,0,0]
	v_mfma_scale_f32_16x16x128_f8f6f4 v[80:83], v[206:213], v[146:153], v[80:83], v165, v164 op_sel_hi:[0,0,0]
	v_mfma_scale_f32_16x16x128_f8f6f4 v[216:219], v[198:205], v[154:161], v[216:219], v165, v164 op_sel_hi:[0,0,0]
	v_mfma_scale_f32_16x16x128_f8f6f4 v[48:51], v[206:213], v[154:161], v[48:51], v165, v164 op_sel_hi:[0,0,0]
	v_mfma_scale_f32_16x16x128_f8f6f4 v[116:119], v[228:235], v[68:75], v[116:119], v165, v164 op_sel_hi:[0,0,0]
	v_mfma_scale_f32_16x16x128_f8f6f4 v[112:115], v[236:243], v[68:75], v[112:115], v165, v164 op_sel_hi:[0,0,0]
	v_mfma_scale_f32_16x16x128_f8f6f4 v[104:107], v[228:235], v[138:145], v[104:107], v165, v164 op_sel_hi:[0,0,0]
	v_mfma_scale_f32_16x16x128_f8f6f4 v[96:99], v[236:243], v[138:145], v[96:99], v165, v164 op_sel_hi:[0,0,0]
	v_mfma_scale_f32_16x16x128_f8f6f4 v[92:95], v[228:235], v[146:153], v[92:95], v165, v164 op_sel_hi:[0,0,0]
	v_mfma_scale_f32_16x16x128_f8f6f4 v[88:91], v[236:243], v[146:153], v[88:91], v165, v164 op_sel_hi:[0,0,0]
	v_mfma_scale_f32_16x16x128_f8f6f4 v[76:79], v[228:235], v[154:161], v[76:79], v165, v164 op_sel_hi:[0,0,0]
	v_mfma_scale_f32_16x16x128_f8f6f4 v[16:19], v[236:243], v[154:161], v[16:19], v165, v164 op_sel_hi:[0,0,0]
	v_mfma_scale_f32_16x16x128_f8f6f4 v[56:59], v[198:205], v[166:173], v[56:59], v165, v164 op_sel_hi:[0,0,0]
	v_mfma_scale_f32_16x16x128_f8f6f4 v[52:55], v[206:213], v[166:173], v[52:55], v165, v164 op_sel_hi:[0,0,0]
	v_mfma_scale_f32_16x16x128_f8f6f4 v[36:39], v[198:205], v[174:181], v[36:39], v165, v164 op_sel_hi:[0,0,0]
	v_mfma_scale_f32_16x16x128_f8f6f4 v[32:35], v[206:213], v[174:181], v[32:35], v165, v164 op_sel_hi:[0,0,0]
	v_mfma_scale_f32_16x16x128_f8f6f4 v[20:23], v[198:205], v[182:189], v[20:23], v165, v164 op_sel_hi:[0,0,0]
	v_mfma_scale_f32_16x16x128_f8f6f4 v[224:227], v[206:213], v[182:189], v[224:227], v165, v164 op_sel_hi:[0,0,0]
	v_mfma_scale_f32_16x16x128_f8f6f4 v[4:7], v[198:205], v[190:197], v[4:7], v165, v164 op_sel_hi:[0,0,0]
	v_mfma_scale_f32_16x16x128_f8f6f4 v[0:3], v[206:213], v[190:197], v[0:3], v165, v164 op_sel_hi:[0,0,0]
	v_mfma_scale_f32_16x16x128_f8f6f4 v[64:67], v[228:235], v[166:173], v[64:67], v165, v164 op_sel_hi:[0,0,0]
	v_mfma_scale_f32_16x16x128_f8f6f4 v[60:63], v[236:243], v[166:173], v[60:63], v165, v164 op_sel_hi:[0,0,0]
	v_mfma_scale_f32_16x16x128_f8f6f4 v[44:47], v[228:235], v[174:181], v[44:47], v165, v164 op_sel_hi:[0,0,0]
	v_mfma_scale_f32_16x16x128_f8f6f4 v[40:43], v[236:243], v[174:181], v[40:43], v165, v164 op_sel_hi:[0,0,0]
	v_mfma_scale_f32_16x16x128_f8f6f4 v[28:31], v[228:235], v[182:189], v[28:31], v165, v164 op_sel_hi:[0,0,0]
	v_mfma_scale_f32_16x16x128_f8f6f4 v[24:27], v[236:243], v[182:189], v[24:27], v165, v164 op_sel_hi:[0,0,0]
	v_mfma_scale_f32_16x16x128_f8f6f4 v[12:15], v[228:235], v[190:197], v[12:15], v165, v164 op_sel_hi:[0,0,0]
	v_mfma_scale_f32_16x16x128_f8f6f4 v[8:11], v[236:243], v[190:197], v[8:11], v165, v164 op_sel_hi:[0,0,0]
; #define G_WAIT_V(n) asm volatile("s_waitcnt vmcnt(" #n ")" ::: "memory")
; #define G_BAR() __builtin_amdgcn_s_barrier()
; #define G_SCHED() __builtin_amdgcn_sched_barrier(0)
; #define D_STAGE_A(slot, half, kt) D_STAGE(rsA, voffA, slot, half, kt)
; #define D_STAGE_B(slot, half, kt) D_STAGE(rsB, voffB, slot, half, kt)
; #define D_LDA(dst, slot) do { _Pragma("unroll") for (int m = 0; m < 4; ++m) _Pragma("unroll") for (int k = 0; k < 2; ++k) \
;     dst[m][k] = *(const LDS_AS bf16x8*)(lds + (slot) + aoff + m * 2048 + k * 1024); } while (0)
; #define D_LDB(dst, slot) do { _Pragma("unroll") for (int n = 0; n < 2; ++n) _Pragma("unroll") for (int k = 0; k < 2; ++k) \
;     dst[n][k] = *(const LDS_AS bf16x8*)(lds + (slot) + boff + n * 2048 + k * 1024); } while (0)
; #define D_MMA(ai, bj, At, Bf) do { __builtin_amdgcn_s_setprio(1); _Pragma("unroll") for (int m = 0; m < 4; ++m) _Pragma("unroll") for (int n = 0; n < 2; ++n) _Pragma("unroll") for (int k = 0; k < 2; ++k) \
;     acc[ai][bj][m][n] = __builtin_amdgcn_mfma_f32_16x16x32_bf16(Bf[n][k], At[m][k], acc[ai][bj][m][n], 0, 0, 0); __builtin_amdgcn_s_setprio(0); } while (0)
; #define D_WAIT_L(n) asm volatile("s_waitcnt lgkmcnt(" #n ")" ::: "memory")
; #define D_STAGE_A(slot, half, kt) D_STAGE(rsA, voffA, slot, half, kt)
; #define D_STAGE_B(slot, half, kt) do { _Pragma("unroll") for (int _i = 0; _i < 2; ++_i) { const unsigned _m0 = ldsw + (unsigned)((slot) + _i * 8192); const unsigned _so = (unsigned)(kt) * 128u + (half) * bt_half + _i * bt_piece; \
;     asm volatile("s_mov_b32 m0, %0\n\ts_nop 4\n\tbuffer_load_dwordx4 %1, %2, %3 offen lds" :: "s"(_m0), "v"(voffB0), "s"(rsB), "s"(_so) : "m0", "memory"); } } while (0)
; #define D_WAIT_L(n) asm volatile("s_waitcnt lgkmcnt(" #n ")" ::: "memory")
;     ...
;     D_LDB(B0, G_SB(1, 0)); G_SCHED(); D_LDA(At, G_SA(1, 0)); D_STAGE_A(G_SA(0, 1), 1, t2);
;     D_WAIT_L(8); G_BAR(); D_WAIT_L(0); G_SCHED(); D_MMA(0, 0, At, B0); G_BAR(); G_SCHED();
;     D_LDB(B1, G_SB(1, 1)); D_STAGE_B(G_SB(1, 0), 0, t3);
;     G_BAR(); D_WAIT_L(0); G_SCHED(); D_MMA(0, 1, At, B1); G_BAR(); G_SCHED();
;     D_LDA(At, G_SA(1, 1)); D_STAGE_A(G_SA(1, 0), 0, t3);
;     G_BAR(); D_WAIT_L(0); G_SCHED(); D_MMA(1, 0, At, B0); G_BAR(); G_SCHED();
;     D_STAGE_B(G_SB(1, 1), 1, t3);
;     G_WAIT_V(6); G_BAR(); G_SCHED(); D_MMA(1, 1, At, B1); G_BAR(); G_SCHED();
.Lkl_m2npre_y_nd0_j:
	s_setprio 0
	s_barrier
	ds_read_b128 v[198:201], v222
	ds_read_b128 v[202:205], v223
	ds_read_b128 v[206:209], v222 offset:2048
	ds_read_b128 v[210:213], v223 offset:2048
	ds_read_b128 v[228:231], v244
	ds_read_b128 v[232:235], v245
	ds_read_b128 v[236:239], v244 offset:2048
	ds_read_b128 v[240:243], v245 offset:2048
	ds_read_b128 v[68:71], v135 offset:32784
	ds_read_b128 v[72:75], v136 offset:32784
	ds_read_b128 v[138:141], v135 offset:34832
	ds_read_b128 v[142:145], v136 offset:34832
	ds_read_b128 v[146:149], v135 offset:36880
	ds_read_b128 v[150:153], v136 offset:36880
	ds_read_b128 v[154:157], v135 offset:38928
	ds_read_b128 v[158:161], v136 offset:38928
	ds_read_b128 v[166:169], v135 offset:49168
	ds_read_b128 v[170:173], v136 offset:49168
	ds_read_b128 v[174:177], v135 offset:51216
	ds_read_b128 v[178:181], v136 offset:51216
	ds_read_b128 v[182:185], v135 offset:53264
	ds_read_b128 v[186:189], v136 offset:53264
	ds_read_b128 v[190:193], v135 offset:55312
	ds_read_b128 v[194:197], v136 offset:55312
	s_waitcnt lgkmcnt(0)
	s_waitcnt vmcnt(0)
	s_barrier
	s_setprio 1
	s_cmp_ge_u32 s74, 14
	s_cbranch_scc1 .Lkl_m2npre_y_nd1
	s_lshl_b32 s69, s74, 7
	s_addk_i32 s69, 0x180
	s_add_i32 s70, s69, 0x20000
	s_add_i32 s71, s69, 0x40000
	s_add_i32 s72, s69, 0x60000
	v_mfma_scale_f32_16x16x128_f8f6f4 v[124:127], v[198:205], v[68:75], v[124:127], v165, v164 op_sel_hi:[0,0,0]
	v_mfma_scale_f32_16x16x128_f8f6f4 v[120:123], v[206:213], v[68:75], v[120:123], v165, v164 op_sel_hi:[0,0,0]
	v_mfma_scale_f32_16x16x128_f8f6f4 v[108:111], v[198:205], v[138:145], v[108:111], v165, v164 op_sel_hi:[0,0,0]
	s_mov_b32 m0, s61
	s_nop 0
	buffer_load_dwordx4 v130, s[4:7], s69 offen lds
	v_mfma_scale_f32_16x16x128_f8f6f4 v[100:103], v[206:213], v[138:145], v[100:103], v165, v164 op_sel_hi:[0,0,0]
	v_mfma_scale_f32_16x16x128_f8f6f4 v[84:87], v[198:205], v[146:153], v[84:87], v165, v164 op_sel_hi:[0,0,0]
	v_mfma_scale_f32_16x16x128_f8f6f4 v[80:83], v[206:213], v[146:153], v[80:83], v165, v164 op_sel_hi:[0,0,0]
	s_mov_b32 m0, s63
	s_nop 0
	buffer_load_dwordx4 v128, s[8:11], s69 offen lds
	v_mfma_scale_f32_16x16x128_f8f6f4 v[216:219], v[198:205], v[154:161], v[216:219], v165, v164 op_sel_hi:[0,0,0]
	v_mfma_scale_f32_16x16x128_f8f6f4 v[48:51], v[206:213], v[154:161], v[48:51], v165, v164 op_sel_hi:[0,0,0]
	v_mfma_scale_f32_16x16x128_f8f6f4 v[116:119], v[228:235], v[68:75], v[116:119], v165, v164 op_sel_hi:[0,0,0]
	s_mov_b32 m0, s62
	s_nop 0
	buffer_load_dwordx4 v130, s[4:7], s70 offen lds
	v_mfma_scale_f32_16x16x128_f8f6f4 v[112:115], v[236:243], v[68:75], v[112:115], v165, v164 op_sel_hi:[0,0,0]
	v_mfma_scale_f32_16x16x128_f8f6f4 v[104:107], v[228:235], v[138:145], v[104:107], v165, v164 op_sel_hi:[0,0,0]
	v_mfma_scale_f32_16x16x128_f8f6f4 v[96:99], v[236:243], v[138:145], v[96:99], v165, v164 op_sel_hi:[0,0,0]
	s_mov_b32 m0, s64
	s_nop 0
	buffer_load_dwordx4 v131, s[8:11], s69 offen lds
	v_mfma_scale_f32_16x16x128_f8f6f4 v[92:95], v[228:235], v[146:153], v[92:95], v165, v164 op_sel_hi:[0,0,0]
	v_mfma_scale_f32_16x16x128_f8f6f4 v[88:91], v[236:243], v[146:153], v[88:91], v165, v164 op_sel_hi:[0,0,0]
	v_mfma_scale_f32_16x16x128_f8f6f4 v[76:79], v[228:235], v[154:161], v[76:79], v165, v164 op_sel_hi:[0,0,0]
	s_mov_b32 m0, s65
	s_nop 0
	buffer_load_dwordx4 v130, s[4:7], s71 offen lds
	v_mfma_scale_f32_16x16x128_f8f6f4 v[16:19], v[236:243], v[154:161], v[16:19], v165, v164 op_sel_hi:[0,0,0]
	v_mfma_scale_f32_16x16x128_f8f6f4 v[56:59], v[198:205], v[166:173], v[56:59], v165, v164 op_sel_hi:[0,0,0]
	v_mfma_scale_f32_16x16x128_f8f6f4 v[52:55], v[206:213], v[166:173], v[52:55], v165, v164 op_sel_hi:[0,0,0]
	s_mov_b32 m0, s67
	s_nop 0
	buffer_load_dwordx4 v129, s[8:11], s69 offen lds
	v_mfma_scale_f32_16x16x128_f8f6f4 v[36:39], v[198:205], v[174:181], v[36:39], v165, v164 op_sel_hi:[0,0,0]
	v_mfma_scale_f32_16x16x128_f8f6f4 v[32:35], v[206:213], v[174:181], v[32:35], v165, v164 op_sel_hi:[0,0,0]
	v_mfma_scale_f32_16x16x128_f8f6f4 v[20:23], v[198:205], v[182:189], v[20:23], v165, v164 op_sel_hi:[0,0,0]
	s_mov_b32 m0, s66
	s_nop 0
	buffer_load_dwordx4 v130, s[4:7], s72 offen lds
	v_mfma_scale_f32_16x16x128_f8f6f4 v[224:227], v[206:213], v[182:189], v[224:227], v165, v164 op_sel_hi:[0,0,0]
	v_mfma_scale_f32_16x16x128_f8f6f4 v[4:7], v[198:205], v[190:197], v[4:7], v165, v164 op_sel_hi:[0,0,0]
	v_mfma_scale_f32_16x16x128_f8f6f4 v[0:3], v[206:213], v[190:197], v[0:3], v165, v164 op_sel_hi:[0,0,0]
	s_mov_b32 m0, s68
	s_nop 0
	buffer_load_dwordx4 v132, s[8:11], s69 offen lds
	v_mfma_scale_f32_16x16x128_f8f6f4 v[64:67], v[228:235], v[166:173], v[64:67], v165, v164 op_sel_hi:[0,0,0]
	v_mfma_scale_f32_16x16x128_f8f6f4 v[60:63], v[236:243], v[166:173], v[60:63], v165, v164 op_sel_hi:[0,0,0]
	v_mfma_scale_f32_16x16x128_f8f6f4 v[44:47], v[228:235], v[174:181], v[44:47], v165, v164 op_sel_hi:[0,0,0]
	v_mfma_scale_f32_16x16x128_f8f6f4 v[40:43], v[236:243], v[174:181], v[40:43], v165, v164 op_sel_hi:[0,0,0]
	v_mfma_scale_f32_16x16x128_f8f6f4 v[28:31], v[228:235], v[182:189], v[28:31], v165, v164 op_sel_hi:[0,0,0]
	v_mfma_scale_f32_16x16x128_f8f6f4 v[24:27], v[236:243], v[182:189], v[24:27], v165, v164 op_sel_hi:[0,0,0]
	v_mfma_scale_f32_16x16x128_f8f6f4 v[12:15], v[228:235], v[190:197], v[12:15], v165, v164 op_sel_hi:[0,0,0]
	v_mfma_scale_f32_16x16x128_f8f6f4 v[8:11], v[236:243], v[190:197], v[8:11], v165, v164 op_sel_hi:[0,0,0]
	s_branch .Lkl_m2npre_y_nd1_j

; #define G_WAIT_V(n) asm volatile("s_waitcnt vmcnt(" #n ")" ::: "memory")
; #define G_BAR() __builtin_amdgcn_s_barrier()
; #define G_SCHED() __builtin_amdgcn_sched_barrier(0)
; #define D_STAGE_A(slot, half, kt) D_STAGE(rsA, voffA, slot, half, kt)
; #define D_STAGE_B(slot, half, kt) D_STAGE(rsB, voffB, slot, half, kt)
; #define D_LDA(dst, slot) do { _Pragma("unroll") for (int m = 0; m < 4; ++m) _Pragma("unroll") for (int k = 0; k < 2; ++k) \
;     dst[m][k] = *(const LDS_AS bf16x8*)(lds + (slot) + aoff + m * 2048 + k * 1024); } while (0)
; #define D_LDB(dst, slot) do { _Pragma("unroll") for (int n = 0; n < 2; ++n) _Pragma("unroll") for (int k = 0; k < 2; ++k) \
;     dst[n][k] = *(const LDS_AS bf16x8*)(lds + (slot) + boff + n * 2048 + k * 1024); } while (0)
; #define D_MMA(ai, bj, At, Bf) do { __builtin_amdgcn_s_setprio(1); _Pragma("unroll") for (int m = 0; m < 4; ++m) _Pragma("unroll") for (int n = 0; n < 2; ++n) _Pragma("unroll") for (int k = 0; k < 2; ++k) \
;     acc[ai][bj][m][n] = __builtin_amdgcn_mfma_f32_16x16x32_bf16(Bf[n][k], At[m][k], acc[ai][bj][m][n], 0, 0, 0); __builtin_amdgcn_s_setprio(0); } while (0)
;     ...
;     D_STAGE_B(G_SB(1, 1), 1, t3);
;     G_WAIT_V(6); G_BAR(); G_SCHED(); D_MMA(1, 1, At, B1); G_BAR(); G_SCHED();
;   }
;   if (!F8_PEEL) G_WAIT_V(0);
;   if (F8_PEEL) {
;     D_LDB(B0, G_SB(0, 0)); G_SCHED(); D_LDA(At, G_SA(0, 0)); D_STAGE_A(G_SA(1, 1), 1, nt - 1);
;     D_WAIT_L(8); G_BAR(); D_WAIT_L(0); G_SCHED(); D_MMA(0, 0, At, B0); D_PIN(0, 0); G_BAR(); G_SCHED();
;     D_LDB(B1, G_SB(0, 1));
;     G_BAR(); D_WAIT_L(0); G_SCHED(); D_MMA(0, 1, At, B1); D_PIN(0, 1); G_BAR(); G_SCHED();
;     D_LDA(At, G_SA(0, 1));
;     G_BAR(); D_WAIT_L(0); G_SCHED(); D_MMA(1, 0, At, B0); D_PIN(1, 0); G_BAR(); G_SCHED();
;     G_WAIT_V(0); G_BAR(); G_SCHED(); D_MMA(1, 1, At, B1); D_PIN(1, 1); G_BAR(); G_SCHED();
;     D_LDB(B0, G_SB(1, 0)); G_SCHED(); D_LDA(At, G_SA(1, 0));
;     D_WAIT_L(8); G_BAR(); D_WAIT_L(0); G_SCHED(); D_MMA(0, 0, At, B0); D_PIN(0, 0); G_BAR(); G_SCHED();
;     D_LDB(B1, G_SB(1, 1));
;     G_BAR(); D_WAIT_L(0); G_SCHED(); D_MMA(0, 1, At, B1); D_PIN(0, 1); G_BAR(); G_SCHED();
;     D_LDA(At, G_SA(1, 1));
;     G_BAR(); D_WAIT_L(0); G_SCHED(); D_MMA(1, 0, At, B0); D_PIN(1, 0); G_BAR(); G_SCHED();
;     G_BAR(); G_SCHED(); D_MMA(1, 1, At, B1); D_PIN(1, 1); G_BAR(); G_SCHED();
;   }
;   if (wr == 0) G_BAR();
.Lkl_m2npre_y_nd1_j:
	s_setprio 0
	s_barrier
	s_add_i32 s74, s74, 2
	s_cmp_lt_u32 s74, 16
	s_cbranch_scc1 .Lkl_m2npre_yl
.Lkl_m2npre_end:
	s_waitcnt vmcnt(0)
	s_cmpk_lt_u32 s13, 0x100
	s_cbranch_scc0 .LBB0_1609
	s_barrier

; #define G_BAR() __builtin_amdgcn_s_barrier()
;     ...
;   unsigned aoff[2], boff[2];
; #pragma unroll
;   for (int j = 0; j < 2; ++j) {
;     aoff[j] = (unsigned)(64 * wr + fr) * 128u + 16u * ((2u * fq + j) ^ ((unsigned)fr & 7u));
;     boff[j] = (unsigned)(32 * wc + fr) * 128u + 16u * ((2u * fq + j) ^ ((unsigned)fr & 7u));
;   }
;     ...
;   const int scw = cfg.scale_w(), scx = cfg.scale_x();
;     ...
;   f32x4 acc[2][2][4][2];
; #pragma unroll
;   for (int a = 0; a < 2; ++a)
; #pragma unroll
;     for (int b = 0; b < 2; ++b)
; #pragma unroll
;       for (int m = 0; m < 4; ++m)
; #pragma unroll
;         for (int n = 0; n < 2; ++n) acc[a][b][m][n] = (f32x4){0.f, 0.f, 0.f, 0.f};
;   i32x8 At[4], B0[2], B1[2];
;   if (!PRE) {
;     D_STAGE_B(G_SB(0, 0), 0, 0); D_STAGE_A(G_SA(0, 0), 0, 0); D_STAGE_B(G_SB(0, 1), 1, 0); D_STAGE_A(G_SA(0, 1), 1, 0);
;     D_STAGE_B(G_SB(1, 0), 0, 1); D_STAGE_A(G_SA(1, 0), 0, 1); D_STAGE_B(G_SB(1, 1), 1, 1);
;   }
;   G_WAIT_V(0); G_BAR();
;   if (wr == 1) G_BAR();
; #pragma clang loop unroll(disable)
;   for (int t = 0; t < (F8_PEEL ? nt - 2 : nt); t += 2) {
;     const int t1 = t + 1;
;     const int t2 = (F8_PEEL || t + 2 < nt) ? t + 2 : t;
;     const int t3 = (F8_PEEL || t + 2 < nt) ? t + 3 : t + 1;
;     D_LDB(B0, G_SB(0, 0)); G_SCHED(); D_LDA(At, G_SA(0, 0)); D_STAGE_A(G_SA(1, 1), 1, t1);
;     D_WAIT_L(8); G_BAR(); D_WAIT_L(0); G_SCHED(); D_MMA(0, 0, At, B0); G_BAR(); G_SCHED();
;     D_LDB(B1, G_SB(0, 1)); D_STAGE_B(G_SB(0, 0), 0, t2);
;     G_BAR(); D_WAIT_L(0); G_SCHED(); D_MMA(0, 1, At, B1); G_BAR(); G_SCHED();
;     D_LDA(At, G_SA(0, 1)); D_STAGE_A(G_SA(0, 0), 0, t2);
;     G_BAR(); D_WAIT_L(0); G_SCHED(); D_MMA(1, 0, At, B0); G_BAR(); G_SCHED();
;     D_STAGE_B(G_SB(0, 1), 1, t2);
;     G_WAIT_V(6); G_BAR(); G_SCHED(); D_MMA(1, 1, At, B1); G_BAR(); G_SCHED();
;     D_LDB(B0, G_SB(1, 0)); G_SCHED(); D_LDA(At, G_SA(1, 0)); D_STAGE_A(G_SA(0, 1), 1, t2);
;     D_WAIT_L(8); G_BAR(); D_WAIT_L(0); G_SCHED(); D_MMA(0, 0, At, B0); G_BAR(); G_SCHED();
;     D_LDB(B1, G_SB(1, 1)); D_STAGE_B(G_SB(1, 0), 0, t3);
;     G_BAR(); D_WAIT_L(0); G_SCHED(); D_MMA(0, 1, At, B1); G_BAR(); G_SCHED();
;     D_LDA(At, G_SA(1, 1)); D_STAGE_A(G_SA(1, 0), 0, t3);
;     G_BAR(); D_WAIT_L(0); G_SCHED(); D_MMA(1, 0, At, B0); G_BAR(); G_SCHED();
;     D_STAGE_B(G_SB(1, 1), 1, t3);
;     G_WAIT_V(6); G_BAR(); G_SCHED(); D_MMA(1, 1, At, B1); G_BAR(); G_SCHED();
;   }
.LBB0_1674:
	s_mov_b32 s67, 0x10010
	v_add_u32_e32 v68, s67, v132
	v_add_u32_e32 v69, s67, v133
	s_mov_b32 s67, 0x14010
	v_add_u32_e32 v70, s67, v132
	v_add_u32_e32 v71, s67, v133
	s_mov_b32 s67, 0x18010
	v_add_u32_e32 v128, s67, v132
	v_add_u32_e32 v129, s67, v133
	s_mov_b32 s67, 0x1c010
	v_add_u32_e32 v130, s67, v132
	v_add_u32_e32 v131, s67, v133
	s_movk_i32 s63, 0x80
	s_mov_b32 m0, s24
	s_nop 0
	buffer_load_dwordx4 v166, s[8:11], s63 offen lds
	s_mov_b32 m0, s51
	s_nop 0
	buffer_load_dwordx4 v167, s[8:11], s63 offen lds
	s_cmpk_lt_u32 s13, 0x100
	s_cbranch_scc0 .Lkl_m2pre_y
	s_mov_b32 s68, 0
.Lkl_m2pre_x:
	ds_read_b128 v[208:211], v68
	ds_read_b128 v[212:215], v69
	ds_read_b128 v[224:227], v68 offset:2048
	ds_read_b128 v[228:231], v69 offset:2048
	ds_read_b128 v[232:235], v70
	ds_read_b128 v[236:239], v71
	ds_read_b128 v[240:243], v70 offset:2048
	ds_read_b128 v[244:247], v71 offset:2048
	ds_read_b128 v[138:141], v135 offset:16
	ds_read_b128 v[142:145], v136 offset:16
	ds_read_b128 v[146:149], v135 offset:2064
	ds_read_b128 v[150:153], v136 offset:2064
	ds_read_b128 v[154:157], v135 offset:4112
	ds_read_b128 v[158:161], v136 offset:4112
	ds_read_b128 v[168:171], v135 offset:6160
	ds_read_b128 v[172:175], v136 offset:6160
	ds_read_b128 v[176:179], v135 offset:16400
	ds_read_b128 v[180:183], v136 offset:16400
	ds_read_b128 v[184:187], v135 offset:18448
	ds_read_b128 v[188:191], v136 offset:18448
	ds_read_b128 v[192:195], v135 offset:20496
	ds_read_b128 v[196:199], v136 offset:20496
	ds_read_b128 v[200:203], v135 offset:22544
	ds_read_b128 v[204:207], v136 offset:22544
	s_cmp_eq_u32 s68, 0
	s_cbranch_scc1 .Lkl_m2pre_x_nd0
	s_lshl_b32 s63, s68, 7
	s_addk_i32 s63, 0x80
	s_add_i32 s64, s63, 0x20000
	s_add_i32 s65, s63, 0x40000
	s_add_i32 s66, s63, 0x60000
	s_mov_b32 m0, s39
	s_nop 0
	buffer_load_dwordx4 v134, s[4:7], s63 offen lds
	s_mov_b32 m0, s49
	s_nop 0
	buffer_load_dwordx4 v162, s[8:11], s63 offen lds
	s_mov_b32 m0, s60
	s_nop 0
	buffer_load_dwordx4 v134, s[4:7], s64 offen lds
	s_mov_b32 m0, s61
	s_nop 0
	buffer_load_dwordx4 v163, s[8:11], s63 offen lds
	s_mov_b32 m0, s50
	s_nop 0
	buffer_load_dwordx4 v134, s[4:7], s65 offen lds
	s_mov_b32 m0, s24
	s_nop 0
	buffer_load_dwordx4 v166, s[8:11], s63 offen lds
	s_mov_b32 m0, s62
	s_nop 0
	buffer_load_dwordx4 v134, s[4:7], s66 offen lds
	s_mov_b32 m0, s51
	s_nop 0
	buffer_load_dwordx4 v167, s[8:11], s63 offen lds
.Lkl_m2pre_x_nd0:
	s_waitcnt lgkmcnt(0)
	s_barrier
	s_setprio 1
	v_mfma_scale_f32_16x16x128_f8f6f4 v[124:127], v[208:215], v[138:145], v[124:127], v165, v164 op_sel_hi:[0,0,0]
	v_mfma_scale_f32_16x16x128_f8f6f4 v[120:123], v[224:231], v[138:145], v[120:123], v165, v164 op_sel_hi:[0,0,0]
	v_mfma_scale_f32_16x16x128_f8f6f4 v[108:111], v[208:215], v[146:153], v[108:111], v165, v164 op_sel_hi:[0,0,0]
	v_mfma_scale_f32_16x16x128_f8f6f4 v[100:103], v[224:231], v[146:153], v[100:103], v165, v164 op_sel_hi:[0,0,0]
	v_mfma_scale_f32_16x16x128_f8f6f4 v[84:87], v[208:215], v[154:161], v[84:87], v165, v164 op_sel_hi:[0,0,0]
	v_mfma_scale_f32_16x16x128_f8f6f4 v[80:83], v[224:231], v[154:161], v[80:83], v165, v164 op_sel_hi:[0,0,0]
	v_mfma_scale_f32_16x16x128_f8f6f4 v[220:223], v[208:215], v[168:175], v[220:223], v165, v164 op_sel_hi:[0,0,0]
	v_mfma_scale_f32_16x16x128_f8f6f4 v[48:51], v[224:231], v[168:175], v[48:51], v165, v164 op_sel_hi:[0,0,0]
	v_mfma_scale_f32_16x16x128_f8f6f4 v[116:119], v[232:239], v[138:145], v[116:119], v165, v164 op_sel_hi:[0,0,0]
	v_mfma_scale_f32_16x16x128_f8f6f4 v[112:115], v[240:247], v[138:145], v[112:115], v165, v164 op_sel_hi:[0,0,0]
	v_mfma_scale_f32_16x16x128_f8f6f4 v[104:107], v[232:239], v[146:153], v[104:107], v165, v164 op_sel_hi:[0,0,0]
	v_mfma_scale_f32_16x16x128_f8f6f4 v[96:99], v[240:247], v[146:153], v[96:99], v165, v164 op_sel_hi:[0,0,0]
	v_mfma_scale_f32_16x16x128_f8f6f4 v[92:95], v[232:239], v[154:161], v[92:95], v165, v164 op_sel_hi:[0,0,0]
	v_mfma_scale_f32_16x16x128_f8f6f4 v[88:91], v[240:247], v[154:161], v[88:91], v165, v164 op_sel_hi:[0,0,0]
	v_mfma_scale_f32_16x16x128_f8f6f4 v[76:79], v[232:239], v[168:175], v[76:79], v165, v164 op_sel_hi:[0,0,0]
	v_mfma_scale_f32_16x16x128_f8f6f4 v[72:75], v[240:247], v[168:175], v[72:75], v165, v164 op_sel_hi:[0,0,0]
	v_mfma_scale_f32_16x16x128_f8f6f4 v[56:59], v[208:215], v[176:183], v[56:59], v165, v164 op_sel_hi:[0,0,0]
	v_mfma_scale_f32_16x16x128_f8f6f4 v[52:55], v[224:231], v[176:183], v[52:55], v165, v164 op_sel_hi:[0,0,0]
	v_mfma_scale_f32_16x16x128_f8f6f4 v[36:39], v[208:215], v[184:191], v[36:39], v165, v164 op_sel_hi:[0,0,0]
	v_mfma_scale_f32_16x16x128_f8f6f4 v[32:35], v[224:231], v[184:191], v[32:35], v165, v164 op_sel_hi:[0,0,0]
	v_mfma_scale_f32_16x16x128_f8f6f4 v[20:23], v[208:215], v[192:199], v[20:23], v165, v164 op_sel_hi:[0,0,0]
	v_mfma_scale_f32_16x16x128_f8f6f4 v[16:19], v[224:231], v[192:199], v[16:19], v165, v164 op_sel_hi:[0,0,0]
	v_mfma_scale_f32_16x16x128_f8f6f4 v[4:7], v[208:215], v[200:207], v[4:7], v165, v164 op_sel_hi:[0,0,0]
	v_mfma_scale_f32_16x16x128_f8f6f4 v[0:3], v[224:231], v[200:207], v[0:3], v165, v164 op_sel_hi:[0,0,0]
	v_mfma_scale_f32_16x16x128_f8f6f4 v[64:67], v[232:239], v[176:183], v[64:67], v165, v164 op_sel_hi:[0,0,0]
	v_mfma_scale_f32_16x16x128_f8f6f4 v[60:63], v[240:247], v[176:183], v[60:63], v165, v164 op_sel_hi:[0,0,0]
	v_mfma_scale_f32_16x16x128_f8f6f4 v[44:47], v[232:239], v[184:191], v[44:47], v165, v164 op_sel_hi:[0,0,0]
	v_mfma_scale_f32_16x16x128_f8f6f4 v[40:43], v[240:247], v[184:191], v[40:43], v165, v164 op_sel_hi:[0,0,0]
	v_mfma_scale_f32_16x16x128_f8f6f4 v[28:31], v[232:239], v[192:199], v[28:31], v165, v164 op_sel_hi:[0,0,0]
	v_mfma_scale_f32_16x16x128_f8f6f4 v[24:27], v[240:247], v[192:199], v[24:27], v165, v164 op_sel_hi:[0,0,0]
	v_mfma_scale_f32_16x16x128_f8f6f4 v[12:15], v[232:239], v[200:207], v[12:15], v165, v164 op_sel_hi:[0,0,0]
	v_mfma_scale_f32_16x16x128_f8f6f4 v[8:11], v[240:247], v[200:207], v[8:11], v165, v164 op_sel_hi:[0,0,0]
	s_setprio 0
	s_waitcnt vmcnt(0)
	s_barrier
; #define G_WAIT_V(n) asm volatile("s_waitcnt vmcnt(" #n ")" ::: "memory")
; #define G_BAR() __builtin_amdgcn_s_barrier()
; #define G_SCHED() __builtin_amdgcn_sched_barrier(0)
; #define D_STAGE_A(slot, half, kt) D_STAGE(rsA, voffA, slot, half, kt)
; #define D_STAGE_B(slot, half, kt) D_STAGE(rsB, voffB, slot, half, kt)
; #define D_LDA(dst, slot) do { _Pragma("unroll") for (int m = 0; m < 4; ++m) _Pragma("unroll") for (int k = 0; k < 2; ++k) \
;     dst[m][k] = *(const LDS_AS bf16x8*)(lds + (slot) + aoff + m * 2048 + k * 1024); } while (0)
; #define D_LDB(dst, slot) do { _Pragma("unroll") for (int n = 0; n < 2; ++n) _Pragma("unroll") for (int k = 0; k < 2; ++k) \
;     dst[n][k] = *(const LDS_AS bf16x8*)(lds + (slot) + boff + n * 2048 + k * 1024); } while (0)
; #define D_MMA(ai, bj, At, Bf) do { __builtin_amdgcn_s_setprio(1); _Pragma("unroll") for (int m = 0; m < 4; ++m) _Pragma("unroll") for (int n = 0; n < 2; ++n) _Pragma("unroll") for (int k = 0; k < 2; ++k) \
;     acc[ai][bj][m][n] = __builtin_amdgcn_mfma_f32_16x16x32_bf16(Bf[n][k], At[m][k], acc[ai][bj][m][n], 0, 0, 0); __builtin_amdgcn_s_setprio(0); } while (0)
; #define D_WAIT_L(n) asm volatile("s_waitcnt lgkmcnt(" #n ")" ::: "memory")
; #define D_STAGE_A(slot, half, kt) D_STAGE(rsA, voffA, slot, half, kt)
; #define D_STAGE_B(slot, half, kt) do { _Pragma("unroll") for (int _i = 0; _i < 2; ++_i) { const unsigned _m0 = ldsw + (unsigned)((slot) + _i * 8192); const unsigned _so = (unsigned)(kt) * 128u + (half) * bt_half + _i * bt_piece; \
;     asm volatile("s_mov_b32 m0, %0\n\ts_nop 4\n\tbuffer_load_dwordx4 %1, %2, %3 offen lds" :: "s"(_m0), "v"(voffB0), "s"(rsB), "s"(_so) : "m0", "memory"); } } while (0)
; #define D_WAIT_L(n) asm volatile("s_waitcnt lgkmcnt(" #n ")" ::: "memory")
;     ...
;     D_LDB(B0, G_SB(1, 0)); G_SCHED(); D_LDA(At, G_SA(1, 0)); D_STAGE_A(G_SA(0, 1), 1, t2);
;     D_WAIT_L(8); G_BAR(); D_WAIT_L(0); G_SCHED(); D_MMA(0, 0, At, B0); G_BAR(); G_SCHED();
;     D_LDB(B1, G_SB(1, 1)); D_STAGE_B(G_SB(1, 0), 0, t3);
;     G_BAR(); D_WAIT_L(0); G_SCHED(); D_MMA(0, 1, At, B1); G_BAR(); G_SCHED();
;     D_LDA(At, G_SA(1, 1)); D_STAGE_A(G_SA(1, 0), 0, t3);
;     G_BAR(); D_WAIT_L(0); G_SCHED(); D_MMA(1, 0, At, B0); G_BAR(); G_SCHED();
;     D_STAGE_B(G_SB(1, 1), 1, t3);
;     G_WAIT_V(6); G_BAR(); G_SCHED(); D_MMA(1, 1, At, B1); G_BAR(); G_SCHED();
;   }
	ds_read_b128 v[208:211], v128
	ds_read_b128 v[212:215], v129
	ds_read_b128 v[224:227], v128 offset:2048
	ds_read_b128 v[228:231], v129 offset:2048
	ds_read_b128 v[232:235], v130
	ds_read_b128 v[236:239], v131
	ds_read_b128 v[240:243], v130 offset:2048
	ds_read_b128 v[244:247], v131 offset:2048
	ds_read_b128 v[138:141], v135 offset:32784
	ds_read_b128 v[142:145], v136 offset:32784
	ds_read_b128 v[146:149], v135 offset:34832
	ds_read_b128 v[150:153], v136 offset:34832
	ds_read_b128 v[154:157], v135 offset:36880
	ds_read_b128 v[158:161], v136 offset:36880
	ds_read_b128 v[168:171], v135 offset:38928
	ds_read_b128 v[172:175], v136 offset:38928
	ds_read_b128 v[176:179], v135 offset:49168
	ds_read_b128 v[180:183], v136 offset:49168
	ds_read_b128 v[184:187], v135 offset:51216
	ds_read_b128 v[188:191], v136 offset:51216
	ds_read_b128 v[192:195], v135 offset:53264
	ds_read_b128 v[196:199], v136 offset:53264
	ds_read_b128 v[200:203], v135 offset:55312
	ds_read_b128 v[204:207], v136 offset:55312
	s_cmp_ge_u32 s68, 14
	s_cbranch_scc1 .Lkl_m2pre_x_nd1
	s_lshl_b32 s63, s68, 7
	s_addk_i32 s63, 0x100
	s_add_i32 s64, s63, 0x20000
	s_add_i32 s65, s63, 0x40000
	s_add_i32 s66, s63, 0x60000
	s_mov_b32 m0, s25
	s_nop 0
	buffer_load_dwordx4 v134, s[4:7], s63 offen lds
	s_mov_b32 m0, s15
	s_nop 0
	buffer_load_dwordx4 v162, s[8:11], s63 offen lds
	s_mov_b32 m0, s54
	s_nop 0
	buffer_load_dwordx4 v134, s[4:7], s64 offen lds
	s_mov_b32 m0, s55
	s_nop 0
	buffer_load_dwordx4 v163, s[8:11], s63 offen lds
	s_mov_b32 m0, s26
	s_nop 0
	buffer_load_dwordx4 v134, s[4:7], s65 offen lds
	s_mov_b32 m0, s27
	s_nop 0
	buffer_load_dwordx4 v166, s[8:11], s63 offen lds
	s_mov_b32 m0, s58
	s_nop 0
	buffer_load_dwordx4 v134, s[4:7], s66 offen lds
	s_mov_b32 m0, s59
	s_nop 0
	buffer_load_dwordx4 v167, s[8:11], s63 offen lds
.Lkl_m2pre_x_nd1:
	s_waitcnt lgkmcnt(0)
	s_barrier
	s_setprio 1
	v_mfma_scale_f32_16x16x128_f8f6f4 v[124:127], v[208:215], v[138:145], v[124:127], v165, v164 op_sel_hi:[0,0,0]
	v_mfma_scale_f32_16x16x128_f8f6f4 v[120:123], v[224:231], v[138:145], v[120:123], v165, v164 op_sel_hi:[0,0,0]
	v_mfma_scale_f32_16x16x128_f8f6f4 v[108:111], v[208:215], v[146:153], v[108:111], v165, v164 op_sel_hi:[0,0,0]
	v_mfma_scale_f32_16x16x128_f8f6f4 v[100:103], v[224:231], v[146:153], v[100:103], v165, v164 op_sel_hi:[0,0,0]
	v_mfma_scale_f32_16x16x128_f8f6f4 v[84:87], v[208:215], v[154:161], v[84:87], v165, v164 op_sel_hi:[0,0,0]
	v_mfma_scale_f32_16x16x128_f8f6f4 v[80:83], v[224:231], v[154:161], v[80:83], v165, v164 op_sel_hi:[0,0,0]
	v_mfma_scale_f32_16x16x128_f8f6f4 v[220:223], v[208:215], v[168:175], v[220:223], v165, v164 op_sel_hi:[0,0,0]
	v_mfma_scale_f32_16x16x128_f8f6f4 v[48:51], v[224:231], v[168:175], v[48:51], v165, v164 op_sel_hi:[0,0,0]
	v_mfma_scale_f32_16x16x128_f8f6f4 v[116:119], v[232:239], v[138:145], v[116:119], v165, v164 op_sel_hi:[0,0,0]
	v_mfma_scale_f32_16x16x128_f8f6f4 v[112:115], v[240:247], v[138:145], v[112:115], v165, v164 op_sel_hi:[0,0,0]
	v_mfma_scale_f32_16x16x128_f8f6f4 v[104:107], v[232:239], v[146:153], v[104:107], v165, v164 op_sel_hi:[0,0,0]
	v_mfma_scale_f32_16x16x128_f8f6f4 v[96:99], v[240:247], v[146:153], v[96:99], v165, v164 op_sel_hi:[0,0,0]
	v_mfma_scale_f32_16x16x128_f8f6f4 v[92:95], v[232:239], v[154:161], v[92:95], v165, v164 op_sel_hi:[0,0,0]
	v_mfma_scale_f32_16x16x128_f8f6f4 v[88:91], v[240:247], v[154:161], v[88:91], v165, v164 op_sel_hi:[0,0,0]
	v_mfma_scale_f32_16x16x128_f8f6f4 v[76:79], v[232:239], v[168:175], v[76:79], v165, v164 op_sel_hi:[0,0,0]
	v_mfma_scale_f32_16x16x128_f8f6f4 v[72:75], v[240:247], v[168:175], v[72:75], v165, v164 op_sel_hi:[0,0,0]
	v_mfma_scale_f32_16x16x128_f8f6f4 v[56:59], v[208:215], v[176:183], v[56:59], v165, v164 op_sel_hi:[0,0,0]
	v_mfma_scale_f32_16x16x128_f8f6f4 v[52:55], v[224:231], v[176:183], v[52:55], v165, v164 op_sel_hi:[0,0,0]
	v_mfma_scale_f32_16x16x128_f8f6f4 v[36:39], v[208:215], v[184:191], v[36:39], v165, v164 op_sel_hi:[0,0,0]
	v_mfma_scale_f32_16x16x128_f8f6f4 v[32:35], v[224:231], v[184:191], v[32:35], v165, v164 op_sel_hi:[0,0,0]
	v_mfma_scale_f32_16x16x128_f8f6f4 v[20:23], v[208:215], v[192:199], v[20:23], v165, v164 op_sel_hi:[0,0,0]
	v_mfma_scale_f32_16x16x128_f8f6f4 v[16:19], v[224:231], v[192:199], v[16:19], v165, v164 op_sel_hi:[0,0,0]
	v_mfma_scale_f32_16x16x128_f8f6f4 v[4:7], v[208:215], v[200:207], v[4:7], v165, v164 op_sel_hi:[0,0,0]
	v_mfma_scale_f32_16x16x128_f8f6f4 v[0:3], v[224:231], v[200:207], v[0:3], v165, v164 op_sel_hi:[0,0,0]
	v_mfma_scale_f32_16x16x128_f8f6f4 v[64:67], v[232:239], v[176:183], v[64:67], v165, v164 op_sel_hi:[0,0,0]
	v_mfma_scale_f32_16x16x128_f8f6f4 v[60:63], v[240:247], v[176:183], v[60:63], v165, v164 op_sel_hi:[0,0,0]
	v_mfma_scale_f32_16x16x128_f8f6f4 v[44:47], v[232:239], v[184:191], v[44:47], v165, v164 op_sel_hi:[0,0,0]
	v_mfma_scale_f32_16x16x128_f8f6f4 v[40:43], v[240:247], v[184:191], v[40:43], v165, v164 op_sel_hi:[0,0,0]
	v_mfma_scale_f32_16x16x128_f8f6f4 v[28:31], v[232:239], v[192:199], v[28:31], v165, v164 op_sel_hi:[0,0,0]
	v_mfma_scale_f32_16x16x128_f8f6f4 v[24:27], v[240:247], v[192:199], v[24:27], v165, v164 op_sel_hi:[0,0,0]
	v_mfma_scale_f32_16x16x128_f8f6f4 v[12:15], v[232:239], v[200:207], v[12:15], v165, v164 op_sel_hi:[0,0,0]
	v_mfma_scale_f32_16x16x128_f8f6f4 v[8:11], v[240:247], v[200:207], v[8:11], v165, v164 op_sel_hi:[0,0,0]
	s_setprio 0
	s_waitcnt vmcnt(0)
	s_barrier
	s_add_i32 s68, s68, 2
	s_cmp_lt_u32 s68, 16
	s_cbranch_scc1 .Lkl_m2pre_x
	s_branch .Lkl_m2pre_end
.Lkl_m2pre_y:
	s_mov_b32 s68, 0
; #define G_WAIT_V(n) asm volatile("s_waitcnt vmcnt(" #n ")" ::: "memory")
; #define G_BAR() __builtin_amdgcn_s_barrier()
; #define G_SCHED() __builtin_amdgcn_sched_barrier(0)
; #define D_STAGE_A(slot, half, kt) D_STAGE(rsA, voffA, slot, half, kt)
; #define D_STAGE_B(slot, half, kt) D_STAGE(rsB, voffB, slot, half, kt)
; #define D_LDA(dst, slot) do { _Pragma("unroll") for (int m = 0; m < 4; ++m) _Pragma("unroll") for (int k = 0; k < 2; ++k) \
;     dst[m][k] = *(const LDS_AS bf16x8*)(lds + (slot) + aoff + m * 2048 + k * 1024); } while (0)
; #define D_LDB(dst, slot) do { _Pragma("unroll") for (int n = 0; n < 2; ++n) _Pragma("unroll") for (int k = 0; k < 2; ++k) \
;     dst[n][k] = *(const LDS_AS bf16x8*)(lds + (slot) + boff + n * 2048 + k * 1024); } while (0)
; #define D_MMA(ai, bj, At, Bf) do { __builtin_amdgcn_s_setprio(1); _Pragma("unroll") for (int m = 0; m < 4; ++m) _Pragma("unroll") for (int n = 0; n < 2; ++n) _Pragma("unroll") for (int k = 0; k < 2; ++k) \
;     acc[ai][bj][m][n] = __builtin_amdgcn_mfma_f32_16x16x32_bf16(Bf[n][k], At[m][k], acc[ai][bj][m][n], 0, 0, 0); __builtin_amdgcn_s_setprio(0); } while (0)
; #define D_WAIT_L(n) asm volatile("s_waitcnt lgkmcnt(" #n ")" ::: "memory")
; #define D_STAGE_A(slot, half, kt) D_STAGE(rsA, voffA, slot, half, kt)
; #define D_STAGE_B(slot, half, kt) do { _Pragma("unroll") for (int _i = 0; _i < 2; ++_i) { const unsigned _m0 = ldsw + (unsigned)((slot) + _i * 8192); const unsigned _so = (unsigned)(kt) * 128u + (half) * bt_half + _i * bt_piece; \
;     asm volatile("s_mov_b32 m0, %0\n\ts_nop 4\n\tbuffer_load_dwordx4 %1, %2, %3 offen lds" :: "s"(_m0), "v"(voffB0), "s"(rsB), "s"(_so) : "m0", "memory"); } } while (0)
; #define D_WAIT_L(n) asm volatile("s_waitcnt lgkmcnt(" #n ")" ::: "memory")
;     ...
;     D_LDB(B0, G_SB(0, 0)); G_SCHED(); D_LDA(At, G_SA(0, 0)); D_STAGE_A(G_SA(1, 1), 1, t1);
;     D_WAIT_L(8); G_BAR(); D_WAIT_L(0); G_SCHED(); D_MMA(0, 0, At, B0); G_BAR(); G_SCHED();
;     D_LDB(B1, G_SB(0, 1)); D_STAGE_B(G_SB(0, 0), 0, t2);
;     G_BAR(); D_WAIT_L(0); G_SCHED(); D_MMA(0, 1, At, B1); G_BAR(); G_SCHED();
;     D_LDA(At, G_SA(0, 1)); D_STAGE_A(G_SA(0, 0), 0, t2);
;     G_BAR(); D_WAIT_L(0); G_SCHED(); D_MMA(1, 0, At, B0); G_BAR(); G_SCHED();
;     D_STAGE_B(G_SB(0, 1), 1, t2);
;     G_WAIT_V(6); G_BAR(); G_SCHED(); D_MMA(1, 1, At, B1); G_BAR(); G_SCHED();
.Lkl_m2pre_yl:
	ds_read_b128 v[208:211], v68
	ds_read_b128 v[212:215], v69
	ds_read_b128 v[224:227], v68 offset:2048
	ds_read_b128 v[228:231], v69 offset:2048
	ds_read_b128 v[232:235], v70
	ds_read_b128 v[236:239], v71
	ds_read_b128 v[240:243], v70 offset:2048
	ds_read_b128 v[244:247], v71 offset:2048
	ds_read_b128 v[138:141], v135 offset:16
	ds_read_b128 v[142:145], v136 offset:16
	ds_read_b128 v[146:149], v135 offset:2064
	ds_read_b128 v[150:153], v136 offset:2064
	ds_read_b128 v[154:157], v135 offset:4112
	ds_read_b128 v[158:161], v136 offset:4112
	ds_read_b128 v[168:171], v135 offset:6160
	ds_read_b128 v[172:175], v136 offset:6160
	ds_read_b128 v[176:179], v135 offset:16400
	ds_read_b128 v[180:183], v136 offset:16400
	ds_read_b128 v[184:187], v135 offset:18448
	ds_read_b128 v[188:191], v136 offset:18448
	ds_read_b128 v[192:195], v135 offset:20496
	ds_read_b128 v[196:199], v136 offset:20496
	ds_read_b128 v[200:203], v135 offset:22544
	ds_read_b128 v[204:207], v136 offset:22544
	s_waitcnt lgkmcnt(0)
	s_waitcnt vmcnt(0)
	s_barrier
	s_setprio 1
	s_cmp_ge_u32 s68, 14
	s_cbranch_scc1 .Lkl_m2pre_y_nd0
	s_lshl_b32 s63, s68, 7
	s_addk_i32 s63, 0x100
	s_add_i32 s64, s63, 0x20000
	s_add_i32 s65, s63, 0x40000
	s_add_i32 s66, s63, 0x60000
	v_mfma_scale_f32_16x16x128_f8f6f4 v[124:127], v[208:215], v[138:145], v[124:127], v165, v164 op_sel_hi:[0,0,0]
	v_mfma_scale_f32_16x16x128_f8f6f4 v[120:123], v[224:231], v[138:145], v[120:123], v165, v164 op_sel_hi:[0,0,0]
	v_mfma_scale_f32_16x16x128_f8f6f4 v[108:111], v[208:215], v[146:153], v[108:111], v165, v164 op_sel_hi:[0,0,0]
	s_mov_b32 m0, s25
	s_nop 0
	buffer_load_dwordx4 v134, s[4:7], s63 offen lds
	v_mfma_scale_f32_16x16x128_f8f6f4 v[100:103], v[224:231], v[146:153], v[100:103], v165, v164 op_sel_hi:[0,0,0]
	v_mfma_scale_f32_16x16x128_f8f6f4 v[84:87], v[208:215], v[154:161], v[84:87], v165, v164 op_sel_hi:[0,0,0]
	v_mfma_scale_f32_16x16x128_f8f6f4 v[80:83], v[224:231], v[154:161], v[80:83], v165, v164 op_sel_hi:[0,0,0]
	s_mov_b32 m0, s15
	s_nop 0
	buffer_load_dwordx4 v162, s[8:11], s63 offen lds
	v_mfma_scale_f32_16x16x128_f8f6f4 v[220:223], v[208:215], v[168:175], v[220:223], v165, v164 op_sel_hi:[0,0,0]
	v_mfma_scale_f32_16x16x128_f8f6f4 v[48:51], v[224:231], v[168:175], v[48:51], v165, v164 op_sel_hi:[0,0,0]
	v_mfma_scale_f32_16x16x128_f8f6f4 v[116:119], v[232:239], v[138:145], v[116:119], v165, v164 op_sel_hi:[0,0,0]
	s_mov_b32 m0, s54
	s_nop 0
	buffer_load_dwordx4 v134, s[4:7], s64 offen lds
	v_mfma_scale_f32_16x16x128_f8f6f4 v[112:115], v[240:247], v[138:145], v[112:115], v165, v164 op_sel_hi:[0,0,0]
	v_mfma_scale_f32_16x16x128_f8f6f4 v[104:107], v[232:239], v[146:153], v[104:107], v165, v164 op_sel_hi:[0,0,0]
	v_mfma_scale_f32_16x16x128_f8f6f4 v[96:99], v[240:247], v[146:153], v[96:99], v165, v164 op_sel_hi:[0,0,0]
	s_mov_b32 m0, s55
	s_nop 0
	buffer_load_dwordx4 v163, s[8:11], s63 offen lds
	v_mfma_scale_f32_16x16x128_f8f6f4 v[92:95], v[232:239], v[154:161], v[92:95], v165, v164 op_sel_hi:[0,0,0]
	v_mfma_scale_f32_16x16x128_f8f6f4 v[88:91], v[240:247], v[154:161], v[88:91], v165, v164 op_sel_hi:[0,0,0]
	v_mfma_scale_f32_16x16x128_f8f6f4 v[76:79], v[232:239], v[168:175], v[76:79], v165, v164 op_sel_hi:[0,0,0]
	s_mov_b32 m0, s26
	s_nop 0
	buffer_load_dwordx4 v134, s[4:7], s65 offen lds
	v_mfma_scale_f32_16x16x128_f8f6f4 v[72:75], v[240:247], v[168:175], v[72:75], v165, v164 op_sel_hi:[0,0,0]
	v_mfma_scale_f32_16x16x128_f8f6f4 v[56:59], v[208:215], v[176:183], v[56:59], v165, v164 op_sel_hi:[0,0,0]
	v_mfma_scale_f32_16x16x128_f8f6f4 v[52:55], v[224:231], v[176:183], v[52:55], v165, v164 op_sel_hi:[0,0,0]
	s_mov_b32 m0, s27
	s_nop 0
	buffer_load_dwordx4 v166, s[8:11], s63 offen lds
	v_mfma_scale_f32_16x16x128_f8f6f4 v[36:39], v[208:215], v[184:191], v[36:39], v165, v164 op_sel_hi:[0,0,0]
	v_mfma_scale_f32_16x16x128_f8f6f4 v[32:35], v[224:231], v[184:191], v[32:35], v165, v164 op_sel_hi:[0,0,0]
	v_mfma_scale_f32_16x16x128_f8f6f4 v[20:23], v[208:215], v[192:199], v[20:23], v165, v164 op_sel_hi:[0,0,0]
	s_mov_b32 m0, s58
	s_nop 0
	buffer_load_dwordx4 v134, s[4:7], s66 offen lds
	v_mfma_scale_f32_16x16x128_f8f6f4 v[16:19], v[224:231], v[192:199], v[16:19], v165, v164 op_sel_hi:[0,0,0]
	v_mfma_scale_f32_16x16x128_f8f6f4 v[4:7], v[208:215], v[200:207], v[4:7], v165, v164 op_sel_hi:[0,0,0]
	v_mfma_scale_f32_16x16x128_f8f6f4 v[0:3], v[224:231], v[200:207], v[0:3], v165, v164 op_sel_hi:[0,0,0]
	s_mov_b32 m0, s59
	s_nop 0
	buffer_load_dwordx4 v167, s[8:11], s63 offen lds
	v_mfma_scale_f32_16x16x128_f8f6f4 v[64:67], v[232:239], v[176:183], v[64:67], v165, v164 op_sel_hi:[0,0,0]
	v_mfma_scale_f32_16x16x128_f8f6f4 v[60:63], v[240:247], v[176:183], v[60:63], v165, v164 op_sel_hi:[0,0,0]
	v_mfma_scale_f32_16x16x128_f8f6f4 v[44:47], v[232:239], v[184:191], v[44:47], v165, v164 op_sel_hi:[0,0,0]
	v_mfma_scale_f32_16x16x128_f8f6f4 v[40:43], v[240:247], v[184:191], v[40:43], v165, v164 op_sel_hi:[0,0,0]
	v_mfma_scale_f32_16x16x128_f8f6f4 v[28:31], v[232:239], v[192:199], v[28:31], v165, v164 op_sel_hi:[0,0,0]
	v_mfma_scale_f32_16x16x128_f8f6f4 v[24:27], v[240:247], v[192:199], v[24:27], v165, v164 op_sel_hi:[0,0,0]
	v_mfma_scale_f32_16x16x128_f8f6f4 v[12:15], v[232:239], v[200:207], v[12:15], v165, v164 op_sel_hi:[0,0,0]
	v_mfma_scale_f32_16x16x128_f8f6f4 v[8:11], v[240:247], v[200:207], v[8:11], v165, v164 op_sel_hi:[0,0,0]
	s_branch .Lkl_m2pre_y_nd0_j
; #define G_WAIT_V(n) asm volatile("s_waitcnt vmcnt(" #n ")" ::: "memory")
; #define G_BAR() __builtin_amdgcn_s_barrier()
; #define G_SCHED() __builtin_amdgcn_sched_barrier(0)
; #define D_STAGE_B(slot, half, kt) D_STAGE(rsB, voffB, slot, half, kt)
; #define D_MMA(ai, bj, At, Bf) do { __builtin_amdgcn_s_setprio(1); _Pragma("unroll") for (int m = 0; m < 4; ++m) _Pragma("unroll") for (int n = 0; n < 2; ++n) _Pragma("unroll") for (int k = 0; k < 2; ++k) \
;     acc[ai][bj][m][n] = __builtin_amdgcn_mfma_f32_16x16x32_bf16(Bf[n][k], At[m][k], acc[ai][bj][m][n], 0, 0, 0); __builtin_amdgcn_s_setprio(0); } while (0)
; #define D_WAIT_L(n) asm volatile("s_waitcnt lgkmcnt(" #n ")" ::: "memory")
; #define D_STAGE_B(slot, half, kt) do { _Pragma("unroll") for (int _i = 0; _i < 2; ++_i) { const unsigned _m0 = ldsw + (unsigned)((slot) + _i * 8192); const unsigned _so = (unsigned)(kt) * 128u + (half) * bt_half + _i * bt_piece; \
;     asm volatile("s_mov_b32 m0, %0\n\ts_nop 4\n\tbuffer_load_dwordx4 %1, %2, %3 offen lds" :: "s"(_m0), "v"(voffB0), "s"(rsB), "s"(_so) : "m0", "memory"); } } while (0)
; #define D_MMA(ai, bj, At, Bf) do { if ((ai) && TOPHALF) break; __builtin_amdgcn_s_setprio(1); _Pragma("unroll") for (int m = 0; m < 4; ++m) _Pragma("unroll") for (int n = 0; n < 2; ++n) \
;     acc[ai][bj][m][n] = __builtin_amdgcn_mfma_scale_f32_16x16x128_f8f6f4(Bf[n], At[m], acc[ai][bj][m][n], 0, 0, 0, scw, 0, scx); __builtin_amdgcn_s_setprio(0); } while (0)
; #define D_WAIT_L(n) asm volatile("s_waitcnt lgkmcnt(" #n ")" ::: "memory")
;     ...
;     G_BAR(); D_WAIT_L(0); G_SCHED(); D_MMA(1, 0, At, B0); G_BAR(); G_SCHED();
;     D_STAGE_B(G_SB(0, 1), 1, t2);
;     G_WAIT_V(6); G_BAR(); G_SCHED(); D_MMA(1, 1, At, B1); G_BAR(); G_SCHED();
.Lkl_m2pre_y_nd0:
	v_mfma_scale_f32_16x16x128_f8f6f4 v[124:127], v[208:215], v[138:145], v[124:127], v165, v164 op_sel_hi:[0,0,0]
	v_mfma_scale_f32_16x16x128_f8f6f4 v[120:123], v[224:231], v[138:145], v[120:123], v165, v164 op_sel_hi:[0,0,0]
	v_mfma_scale_f32_16x16x128_f8f6f4 v[108:111], v[208:215], v[146:153], v[108:111], v165, v164 op_sel_hi:[0,0,0]
	v_mfma_scale_f32_16x16x128_f8f6f4 v[100:103], v[224:231], v[146:153], v[100:103], v165, v164 op_sel_hi:[0,0,0]
	v_mfma_scale_f32_16x16x128_f8f6f4 v[84:87], v[208:215], v[154:161], v[84:87], v165, v164 op_sel_hi:[0,0,0]
	v_mfma_scale_f32_16x16x128_f8f6f4 v[80:83], v[224:231], v[154:161], v[80:83], v165, v164 op_sel_hi:[0,0,0]
	v_mfma_scale_f32_16x16x128_f8f6f4 v[220:223], v[208:215], v[168:175], v[220:223], v165, v164 op_sel_hi:[0,0,0]
	v_mfma_scale_f32_16x16x128_f8f6f4 v[48:51], v[224:231], v[168:175], v[48:51], v165, v164 op_sel_hi:[0,0,0]
	v_mfma_scale_f32_16x16x128_f8f6f4 v[116:119], v[232:239], v[138:145], v[116:119], v165, v164 op_sel_hi:[0,0,0]
	v_mfma_scale_f32_16x16x128_f8f6f4 v[112:115], v[240:247], v[138:145], v[112:115], v165, v164 op_sel_hi:[0,0,0]
	v_mfma_scale_f32_16x16x128_f8f6f4 v[104:107], v[232:239], v[146:153], v[104:107], v165, v164 op_sel_hi:[0,0,0]
	v_mfma_scale_f32_16x16x128_f8f6f4 v[96:99], v[240:247], v[146:153], v[96:99], v165, v164 op_sel_hi:[0,0,0]
	v_mfma_scale_f32_16x16x128_f8f6f4 v[92:95], v[232:239], v[154:161], v[92:95], v165, v164 op_sel_hi:[0,0,0]
	v_mfma_scale_f32_16x16x128_f8f6f4 v[88:91], v[240:247], v[154:161], v[88:91], v165, v164 op_sel_hi:[0,0,0]
	v_mfma_scale_f32_16x16x128_f8f6f4 v[76:79], v[232:239], v[168:175], v[76:79], v165, v164 op_sel_hi:[0,0,0]
	v_mfma_scale_f32_16x16x128_f8f6f4 v[72:75], v[240:247], v[168:175], v[72:75], v165, v164 op_sel_hi:[0,0,0]
	v_mfma_scale_f32_16x16x128_f8f6f4 v[56:59], v[208:215], v[176:183], v[56:59], v165, v164 op_sel_hi:[0,0,0]
	v_mfma_scale_f32_16x16x128_f8f6f4 v[52:55], v[224:231], v[176:183], v[52:55], v165, v164 op_sel_hi:[0,0,0]
	v_mfma_scale_f32_16x16x128_f8f6f4 v[36:39], v[208:215], v[184:191], v[36:39], v165, v164 op_sel_hi:[0,0,0]
	v_mfma_scale_f32_16x16x128_f8f6f4 v[32:35], v[224:231], v[184:191], v[32:35], v165, v164 op_sel_hi:[0,0,0]
	v_mfma_scale_f32_16x16x128_f8f6f4 v[20:23], v[208:215], v[192:199], v[20:23], v165, v164 op_sel_hi:[0,0,0]
	v_mfma_scale_f32_16x16x128_f8f6f4 v[16:19], v[224:231], v[192:199], v[16:19], v165, v164 op_sel_hi:[0,0,0]
	v_mfma_scale_f32_16x16x128_f8f6f4 v[4:7], v[208:215], v[200:207], v[4:7], v165, v164 op_sel_hi:[0,0,0]
	v_mfma_scale_f32_16x16x128_f8f6f4 v[0:3], v[224:231], v[200:207], v[0:3], v165, v164 op_sel_hi:[0,0,0]
	v_mfma_scale_f32_16x16x128_f8f6f4 v[64:67], v[232:239], v[176:183], v[64:67], v165, v164 op_sel_hi:[0,0,0]
	v_mfma_scale_f32_16x16x128_f8f6f4 v[60:63], v[240:247], v[176:183], v[60:63], v165, v164 op_sel_hi:[0,0,0]
	v_mfma_scale_f32_16x16x128_f8f6f4 v[44:47], v[232:239], v[184:191], v[44:47], v165, v164 op_sel_hi:[0,0,0]
	v_mfma_scale_f32_16x16x128_f8f6f4 v[40:43], v[240:247], v[184:191], v[40:43], v165, v164 op_sel_hi:[0,0,0]
	v_mfma_scale_f32_16x16x128_f8f6f4 v[28:31], v[232:239], v[192:199], v[28:31], v165, v164 op_sel_hi:[0,0,0]
	v_mfma_scale_f32_16x16x128_f8f6f4 v[24:27], v[240:247], v[192:199], v[24:27], v165, v164 op_sel_hi:[0,0,0]
	v_mfma_scale_f32_16x16x128_f8f6f4 v[12:15], v[232:239], v[200:207], v[12:15], v165, v164 op_sel_hi:[0,0,0]
	v_mfma_scale_f32_16x16x128_f8f6f4 v[8:11], v[240:247], v[200:207], v[8:11], v165, v164 op_sel_hi:[0,0,0]
; #define G_WAIT_V(n) asm volatile("s_waitcnt vmcnt(" #n ")" ::: "memory")
; #define G_BAR() __builtin_amdgcn_s_barrier()
; #define G_SCHED() __builtin_amdgcn_sched_barrier(0)
; #define D_STAGE_A(slot, half, kt) D_STAGE(rsA, voffA, slot, half, kt)
; #define D_STAGE_B(slot, half, kt) D_STAGE(rsB, voffB, slot, half, kt)
; #define D_LDA(dst, slot) do { _Pragma("unroll") for (int m = 0; m < 4; ++m) _Pragma("unroll") for (int k = 0; k < 2; ++k) \
;     dst[m][k] = *(const LDS_AS bf16x8*)(lds + (slot) + aoff + m * 2048 + k * 1024); } while (0)
; #define D_LDB(dst, slot) do { _Pragma("unroll") for (int n = 0; n < 2; ++n) _Pragma("unroll") for (int k = 0; k < 2; ++k) \
;     dst[n][k] = *(const LDS_AS bf16x8*)(lds + (slot) + boff + n * 2048 + k * 1024); } while (0)
; #define D_MMA(ai, bj, At, Bf) do { __builtin_amdgcn_s_setprio(1); _Pragma("unroll") for (int m = 0; m < 4; ++m) _Pragma("unroll") for (int n = 0; n < 2; ++n) _Pragma("unroll") for (int k = 0; k < 2; ++k) \
;     acc[ai][bj][m][n] = __builtin_amdgcn_mfma_f32_16x16x32_bf16(Bf[n][k], At[m][k], acc[ai][bj][m][n], 0, 0, 0); __builtin_amdgcn_s_setprio(0); } while (0)
; #define D_WAIT_L(n) asm volatile("s_waitcnt lgkmcnt(" #n ")" ::: "memory")
; #define D_STAGE_A(slot, half, kt) D_STAGE(rsA, voffA, slot, half, kt)
; #define D_STAGE_B(slot, half, kt) do { _Pragma("unroll") for (int _i = 0; _i < 2; ++_i) { const unsigned _m0 = ldsw + (unsigned)((slot) + _i * 8192); const unsigned _so = (unsigned)(kt) * 128u + (half) * bt_half + _i * bt_piece; \
;     asm volatile("s_mov_b32 m0, %0\n\ts_nop 4\n\tbuffer_load_dwordx4 %1, %2, %3 offen lds" :: "s"(_m0), "v"(voffB0), "s"(rsB), "s"(_so) : "m0", "memory"); } } while (0)
; #define D_WAIT_L(n) asm volatile("s_waitcnt lgkmcnt(" #n ")" ::: "memory")
;     ...
;     D_LDB(B0, G_SB(1, 0)); G_SCHED(); D_LDA(At, G_SA(1, 0)); D_STAGE_A(G_SA(0, 1), 1, t2);
;     D_WAIT_L(8); G_BAR(); D_WAIT_L(0); G_SCHED(); D_MMA(0, 0, At, B0); G_BAR(); G_SCHED();
;     D_LDB(B1, G_SB(1, 1)); D_STAGE_B(G_SB(1, 0), 0, t3);
;     G_BAR(); D_WAIT_L(0); G_SCHED(); D_MMA(0, 1, At, B1); G_BAR(); G_SCHED();
;     D_LDA(At, G_SA(1, 1)); D_STAGE_A(G_SA(1, 0), 0, t3);
;     G_BAR(); D_WAIT_L(0); G_SCHED(); D_MMA(1, 0, At, B0); G_BAR(); G_SCHED();
;     D_STAGE_B(G_SB(1, 1), 1, t3);
;     G_WAIT_V(6); G_BAR(); G_SCHED(); D_MMA(1, 1, At, B1); G_BAR(); G_SCHED();
.Lkl_m2pre_y_nd0_j:
	s_setprio 0
	s_barrier
	ds_read_b128 v[208:211], v128
	ds_read_b128 v[212:215], v129
	ds_read_b128 v[224:227], v128 offset:2048
	ds_read_b128 v[228:231], v129 offset:2048
	ds_read_b128 v[232:235], v130
	ds_read_b128 v[236:239], v131
	ds_read_b128 v[240:243], v130 offset:2048
	ds_read_b128 v[244:247], v131 offset:2048
	ds_read_b128 v[138:141], v135 offset:32784
	ds_read_b128 v[142:145], v136 offset:32784
	ds_read_b128 v[146:149], v135 offset:34832
	ds_read_b128 v[150:153], v136 offset:34832
	ds_read_b128 v[154:157], v135 offset:36880
	ds_read_b128 v[158:161], v136 offset:36880
	ds_read_b128 v[168:171], v135 offset:38928
	ds_read_b128 v[172:175], v136 offset:38928
	ds_read_b128 v[176:179], v135 offset:49168
	ds_read_b128 v[180:183], v136 offset:49168
	ds_read_b128 v[184:187], v135 offset:51216
	ds_read_b128 v[188:191], v136 offset:51216
	ds_read_b128 v[192:195], v135 offset:53264
	ds_read_b128 v[196:199], v136 offset:53264
	ds_read_b128 v[200:203], v135 offset:55312
	ds_read_b128 v[204:207], v136 offset:55312
	s_waitcnt lgkmcnt(0)
	s_waitcnt vmcnt(0)
	s_barrier
	s_setprio 1
	s_cmp_ge_u32 s68, 14
	s_cbranch_scc1 .Lkl_m2pre_y_nd1
	s_lshl_b32 s63, s68, 7
	s_addk_i32 s63, 0x180
	s_add_i32 s64, s63, 0x20000
	s_add_i32 s65, s63, 0x40000
	s_add_i32 s66, s63, 0x60000
	v_mfma_scale_f32_16x16x128_f8f6f4 v[124:127], v[208:215], v[138:145], v[124:127], v165, v164 op_sel_hi:[0,0,0]
	v_mfma_scale_f32_16x16x128_f8f6f4 v[120:123], v[224:231], v[138:145], v[120:123], v165, v164 op_sel_hi:[0,0,0]
	v_mfma_scale_f32_16x16x128_f8f6f4 v[108:111], v[208:215], v[146:153], v[108:111], v165, v164 op_sel_hi:[0,0,0]
	s_mov_b32 m0, s39
	s_nop 0
	buffer_load_dwordx4 v134, s[4:7], s63 offen lds
	v_mfma_scale_f32_16x16x128_f8f6f4 v[100:103], v[224:231], v[146:153], v[100:103], v165, v164 op_sel_hi:[0,0,0]
	v_mfma_scale_f32_16x16x128_f8f6f4 v[84:87], v[208:215], v[154:161], v[84:87], v165, v164 op_sel_hi:[0,0,0]
	v_mfma_scale_f32_16x16x128_f8f6f4 v[80:83], v[224:231], v[154:161], v[80:83], v165, v164 op_sel_hi:[0,0,0]
	s_mov_b32 m0, s49
	s_nop 0
	buffer_load_dwordx4 v162, s[8:11], s63 offen lds
	v_mfma_scale_f32_16x16x128_f8f6f4 v[220:223], v[208:215], v[168:175], v[220:223], v165, v164 op_sel_hi:[0,0,0]
	v_mfma_scale_f32_16x16x128_f8f6f4 v[48:51], v[224:231], v[168:175], v[48:51], v165, v164 op_sel_hi:[0,0,0]
	v_mfma_scale_f32_16x16x128_f8f6f4 v[116:119], v[232:239], v[138:145], v[116:119], v165, v164 op_sel_hi:[0,0,0]
	s_mov_b32 m0, s60
	s_nop 0
	buffer_load_dwordx4 v134, s[4:7], s64 offen lds
	v_mfma_scale_f32_16x16x128_f8f6f4 v[112:115], v[240:247], v[138:145], v[112:115], v165, v164 op_sel_hi:[0,0,0]
	v_mfma_scale_f32_16x16x128_f8f6f4 v[104:107], v[232:239], v[146:153], v[104:107], v165, v164 op_sel_hi:[0,0,0]
	v_mfma_scale_f32_16x16x128_f8f6f4 v[96:99], v[240:247], v[146:153], v[96:99], v165, v164 op_sel_hi:[0,0,0]
	s_mov_b32 m0, s61
	s_nop 0
	buffer_load_dwordx4 v163, s[8:11], s63 offen lds
	v_mfma_scale_f32_16x16x128_f8f6f4 v[92:95], v[232:239], v[154:161], v[92:95], v165, v164 op_sel_hi:[0,0,0]
	v_mfma_scale_f32_16x16x128_f8f6f4 v[88:91], v[240:247], v[154:161], v[88:91], v165, v164 op_sel_hi:[0,0,0]
	v_mfma_scale_f32_16x16x128_f8f6f4 v[76:79], v[232:239], v[168:175], v[76:79], v165, v164 op_sel_hi:[0,0,0]
	s_mov_b32 m0, s50
	s_nop 0
	buffer_load_dwordx4 v134, s[4:7], s65 offen lds
	v_mfma_scale_f32_16x16x128_f8f6f4 v[72:75], v[240:247], v[168:175], v[72:75], v165, v164 op_sel_hi:[0,0,0]
	v_mfma_scale_f32_16x16x128_f8f6f4 v[56:59], v[208:215], v[176:183], v[56:59], v165, v164 op_sel_hi:[0,0,0]
	v_mfma_scale_f32_16x16x128_f8f6f4 v[52:55], v[224:231], v[176:183], v[52:55], v165, v164 op_sel_hi:[0,0,0]
	s_mov_b32 m0, s24
	s_nop 0
	buffer_load_dwordx4 v166, s[8:11], s63 offen lds
	v_mfma_scale_f32_16x16x128_f8f6f4 v[36:39], v[208:215], v[184:191], v[36:39], v165, v164 op_sel_hi:[0,0,0]
	v_mfma_scale_f32_16x16x128_f8f6f4 v[32:35], v[224:231], v[184:191], v[32:35], v165, v164 op_sel_hi:[0,0,0]
	v_mfma_scale_f32_16x16x128_f8f6f4 v[20:23], v[208:215], v[192:199], v[20:23], v165, v164 op_sel_hi:[0,0,0]
	s_mov_b32 m0, s62
	s_nop 0
	buffer_load_dwordx4 v134, s[4:7], s66 offen lds
	v_mfma_scale_f32_16x16x128_f8f6f4 v[16:19], v[224:231], v[192:199], v[16:19], v165, v164 op_sel_hi:[0,0,0]
	v_mfma_scale_f32_16x16x128_f8f6f4 v[4:7], v[208:215], v[200:207], v[4:7], v165, v164 op_sel_hi:[0,0,0]
	v_mfma_scale_f32_16x16x128_f8f6f4 v[0:3], v[224:231], v[200:207], v[0:3], v165, v164 op_sel_hi:[0,0,0]
	s_mov_b32 m0, s51
	s_nop 0
	buffer_load_dwordx4 v167, s[8:11], s63 offen lds
	v_mfma_scale_f32_16x16x128_f8f6f4 v[64:67], v[232:239], v[176:183], v[64:67], v165, v164 op_sel_hi:[0,0,0]
	v_mfma_scale_f32_16x16x128_f8f6f4 v[60:63], v[240:247], v[176:183], v[60:63], v165, v164 op_sel_hi:[0,0,0]
	v_mfma_scale_f32_16x16x128_f8f6f4 v[44:47], v[232:239], v[184:191], v[44:47], v165, v164 op_sel_hi:[0,0,0]
	v_mfma_scale_f32_16x16x128_f8f6f4 v[40:43], v[240:247], v[184:191], v[40:43], v165, v164 op_sel_hi:[0,0,0]
	v_mfma_scale_f32_16x16x128_f8f6f4 v[28:31], v[232:239], v[192:199], v[28:31], v165, v164 op_sel_hi:[0,0,0]
	v_mfma_scale_f32_16x16x128_f8f6f4 v[24:27], v[240:247], v[192:199], v[24:27], v165, v164 op_sel_hi:[0,0,0]
	v_mfma_scale_f32_16x16x128_f8f6f4 v[12:15], v[232:239], v[200:207], v[12:15], v165, v164 op_sel_hi:[0,0,0]
	v_mfma_scale_f32_16x16x128_f8f6f4 v[8:11], v[240:247], v[200:207], v[8:11], v165, v164 op_sel_hi:[0,0,0]
	s_branch .Lkl_m2pre_y_nd1_j

; #define G_WAIT_V(n) asm volatile("s_waitcnt vmcnt(" #n ")" ::: "memory")
; #define G_BAR() __builtin_amdgcn_s_barrier()
; #define G_SCHED() __builtin_amdgcn_sched_barrier(0)
; #define D_STAGE_B(slot, half, kt) D_STAGE(rsB, voffB, slot, half, kt)
; #define D_MMA(ai, bj, At, Bf) do { __builtin_amdgcn_s_setprio(1); _Pragma("unroll") for (int m = 0; m < 4; ++m) _Pragma("unroll") for (int n = 0; n < 2; ++n) _Pragma("unroll") for (int k = 0; k < 2; ++k) \
;     acc[ai][bj][m][n] = __builtin_amdgcn_mfma_f32_16x16x32_bf16(Bf[n][k], At[m][k], acc[ai][bj][m][n], 0, 0, 0); __builtin_amdgcn_s_setprio(0); } while (0)
; #define D_STAGE_B(slot, half, kt) do { _Pragma("unroll") for (int _i = 0; _i < 2; ++_i) { const unsigned _m0 = ldsw + (unsigned)((slot) + _i * 8192); const unsigned _so = (unsigned)(kt) * 128u + (half) * bt_half + _i * bt_piece; \
;     asm volatile("s_mov_b32 m0, %0\n\ts_nop 4\n\tbuffer_load_dwordx4 %1, %2, %3 offen lds" :: "s"(_m0), "v"(voffB0), "s"(rsB), "s"(_so) : "m0", "memory"); } } while (0)
; #define D_MMA(ai, bj, At, Bf) do { if ((ai) && TOPHALF) break; __builtin_amdgcn_s_setprio(1); _Pragma("unroll") for (int m = 0; m < 4; ++m) _Pragma("unroll") for (int n = 0; n < 2; ++n) \
;     acc[ai][bj][m][n] = __builtin_amdgcn_mfma_scale_f32_16x16x128_f8f6f4(Bf[n], At[m], acc[ai][bj][m][n], 0, 0, 0, scw, 0, scx); __builtin_amdgcn_s_setprio(0); } while (0)
;     ...
;     D_STAGE_B(G_SB(1, 1), 1, t3);
;     G_WAIT_V(6); G_BAR(); G_SCHED(); D_MMA(1, 1, At, B1); G_BAR(); G_SCHED();
;   }
.Lkl_m2pre_y_nd1_j:
	s_setprio 0
	s_barrier
	s_add_i32 s68, s68, 2
	s_cmp_lt_u32 s68, 16
	s_cbranch_scc1 .Lkl_m2pre_yl
